# v17 + packed f32 VALU (pk_fma/pk_mul/pk_add) in the NSA phase unpacked into scalar f32 ops (bit-exact)
# speedup vs baseline: 1.0145x; 1.0140x over previous
.LBB0_1653:
	s_nop 7
	v_max_f32_e32 v2, v21, v21
	v_max_f32_e32 v45, v20, v20
	v_max_f32_e32 v2, v45, v2
	v_max3_f32 v2, v2, v22, v23
	v_max3_f32 v2, v2, v24, v25
	v_max3_f32 v2, v2, v26, v27
	v_max3_f32 v2, v2, v28, v29
	v_max3_f32 v2, v2, v30, v31
	v_max3_f32 v2, v2, v32, v33
	v_max3_f32 v2, v2, v34, v35
	v_max3_f32 v2, v2, v4, v5
	v_max3_f32 v2, v2, v6, v7
	v_max3_f32 v2, v2, v8, v9
	v_max3_f32 v2, v2, v10, v11
	v_max3_f32 v2, v2, v12, v13
	v_max3_f32 v2, v2, v14, v15
	v_max3_f32 v2, v2, v16, v17
	v_max3_f32 v2, v2, v18, v19
	v_mov_b32_e32 v45, v2
	s_nop 1
	v_permlane32_swap_b32_e32 v2, v45
	v_max3_f32 v45, v44, v2, v45
	v_mul_f32_e32 v47, 0xbe0293ee, v45
	v_fmamk_f32 v2, v20, 0x3e0293ee, v47
	v_exp_f32_e32 v20, v2
	v_fmamk_f32 v2, v4, 0x3e0293ee, v47
	v_exp_f32_e32 v48, v2
	v_fmamk_f32 v2, v21, 0x3e0293ee, v47
	v_exp_f32_e32 v4, v2
	v_fmamk_f32 v2, v5, 0x3e0293ee, v47
	v_exp_f32_e32 v2, v2
	v_add_f32_e32 v5, v20, v48
	s_waitcnt vmcnt(0) lgkmcnt(0)
	s_barrier
	v_add_f32_e32 v4, v4, v2
	v_add_f32_e32 v5, v5, v3
	v_fmamk_f32 v2, v22, 0x3e0293ee, v47
	v_add_f32_e32 v5, v4, v5
	v_add_f32_e32 v4, v4, v4
	v_fmamk_f32 v4, v6, 0x3e0293ee, v47
	v_exp_f32_e32 v20, v4
	v_fmamk_f32 v4, v23, 0x3e0293ee, v47
	v_exp_f32_e32 v2, v2
	v_exp_f32_e32 v6, v4
	v_fmamk_f32 v4, v7, 0x3e0293ee, v47
	v_exp_f32_e32 v4, v4
	v_add_f32_e32 v7, v2, v20
	v_fmamk_f32 v2, v24, 0x3e0293ee, v47
	v_exp_f32_e32 v2, v2
	v_add_f32_e32 v4, v6, v4
	v_add_f32_e32 v5, v7, v5
	s_andn2_b64 vcc, exec, s[8:9]
	v_add_f32_e32 v5, v4, v5
	v_add_f32_e32 v4, v4, v4
	v_fmamk_f32 v4, v8, 0x3e0293ee, v47
	v_exp_f32_e32 v7, v4
	v_fmamk_f32 v4, v25, 0x3e0293ee, v47
	v_exp_f32_e32 v6, v4
	v_fmamk_f32 v4, v9, 0x3e0293ee, v47
	v_exp_f32_e32 v4, v4
	v_add_f32_e32 v7, v2, v7
	v_fmamk_f32 v2, v26, 0x3e0293ee, v47
	v_exp_f32_e32 v2, v2
	v_add_f32_e32 v4, v6, v4
	v_add_f32_e32 v5, v7, v5
	s_nop 0
	v_add_f32_e32 v5, v4, v5
	v_add_f32_e32 v4, v4, v4
	v_fmamk_f32 v4, v10, 0x3e0293ee, v47
	v_exp_f32_e32 v7, v4
	v_fmamk_f32 v4, v27, 0x3e0293ee, v47
	v_exp_f32_e32 v6, v4
	v_fmamk_f32 v4, v11, 0x3e0293ee, v47
	v_exp_f32_e32 v4, v4
	v_add_f32_e32 v7, v2, v7
	v_fmamk_f32 v2, v28, 0x3e0293ee, v47
	v_exp_f32_e32 v2, v2
	v_add_f32_e32 v4, v6, v4
	v_add_f32_e32 v5, v7, v5
	s_nop 0
	v_add_f32_e32 v5, v4, v5
	v_add_f32_e32 v4, v4, v4
	v_fmamk_f32 v4, v12, 0x3e0293ee, v47
	v_exp_f32_e32 v7, v4
	v_fmamk_f32 v4, v29, 0x3e0293ee, v47
	v_exp_f32_e32 v6, v4
	v_fmamk_f32 v4, v13, 0x3e0293ee, v47
	v_exp_f32_e32 v4, v4
	v_add_f32_e32 v7, v2, v7
	v_fmamk_f32 v2, v30, 0x3e0293ee, v47
	v_exp_f32_e32 v2, v2
	v_add_f32_e32 v4, v6, v4
	v_add_f32_e32 v5, v7, v5
	s_nop 0
	v_add_f32_e32 v5, v4, v5
	v_add_f32_e32 v4, v4, v4
	v_fmamk_f32 v4, v14, 0x3e0293ee, v47
	v_exp_f32_e32 v7, v4
	v_fmamk_f32 v4, v31, 0x3e0293ee, v47
	v_exp_f32_e32 v6, v4
	v_fmamk_f32 v4, v15, 0x3e0293ee, v47
	v_exp_f32_e32 v4, v4
	v_add_f32_e32 v7, v2, v7
	v_fmamk_f32 v2, v32, 0x3e0293ee, v47
	v_exp_f32_e32 v2, v2
	v_add_f32_e32 v4, v6, v4
	v_add_f32_e32 v5, v7, v5
	s_nop 0
	v_add_f32_e32 v5, v4, v5
	v_add_f32_e32 v4, v4, v4
	v_fmamk_f32 v4, v16, 0x3e0293ee, v47
	v_exp_f32_e32 v7, v4
	v_fmamk_f32 v4, v33, 0x3e0293ee, v47
	v_exp_f32_e32 v6, v4
	v_fmamk_f32 v4, v17, 0x3e0293ee, v47
	v_exp_f32_e32 v4, v4
	v_add_f32_e32 v7, v2, v7
	v_fmamk_f32 v2, v34, 0x3e0293ee, v47
	v_exp_f32_e32 v2, v2
	v_add_f32_e32 v4, v6, v4
	v_add_f32_e32 v5, v7, v5
	s_nop 0
	v_add_f32_e32 v5, v4, v5
	v_add_f32_e32 v4, v4, v4
	v_fmamk_f32 v4, v18, 0x3e0293ee, v47
	v_exp_f32_e32 v7, v4
	v_fmamk_f32 v4, v35, 0x3e0293ee, v47
	v_fmac_f32_e32 v47, 0x3e0293ee, v19
	v_exp_f32_e32 v6, v4
	v_exp_f32_e32 v4, v47
	v_add_f32_e32 v7, v2, v7
	v_add_f32_e32 v4, v6, v4
	v_add_f32_e32 v5, v7, v5
	s_nop 0
	v_pk_add_f32 v[4:5], v[4:5], v[4:5] op_sel:[0,1] op_sel_hi:[1,0]
	s_nop 0
	v_sub_f32_e32 v5, v44, v45
	v_mul_f32_e32 v5, 0x3e0293ee, v5
	v_exp_f32_e32 v5, v5
	v_mov_b32_e32 v2, v4
	s_nop 1
	v_permlane32_swap_b32_e32 v4, v2
	v_add_f32_e32 v47, v4, v2
	v_fmac_f32_e32 v47, v46, v5
	s_cbranch_vccnz .LBB0_1647
	s_cmp_ge_u32 s6, s18
	s_cbranch_scc1 .LBB0_1656
	s_mov_b32 m0, s42
	s_mov_b32 s14, s94
	buffer_load_dwordx4 v0, s[92:95], s3 offen lds
	s_mov_b32 s15, s95
	s_mov_b32 m0, s41
	s_nop 0
	buffer_load_dwordx4 v1, s[12:15], s3 offen lds
	s_mov_b32 m0, s43
	s_nop 0
	buffer_load_dwordx4 v36, s[92:95], s3 offen lds
	s_mov_b32 m0, s44
	s_nop 0
	buffer_load_dwordx4 v37, s[12:15], s3 offen lds

.LBB0_1658:
	s_nop 7
	v_max_f32_e32 v2, v21, v21
	v_max_f32_e32 v44, v20, v20
	v_max_f32_e32 v2, v44, v2
	v_max3_f32 v2, v2, v22, v23
	v_max3_f32 v2, v2, v24, v25
	v_max3_f32 v2, v2, v26, v27
	v_max3_f32 v2, v2, v28, v29
	v_max3_f32 v2, v2, v30, v31
	v_max3_f32 v2, v2, v32, v33
	v_max3_f32 v2, v2, v34, v35
	v_max3_f32 v2, v2, v4, v5
	v_max3_f32 v2, v2, v6, v7
	v_max3_f32 v2, v2, v8, v9
	v_max3_f32 v2, v2, v10, v11
	v_max3_f32 v2, v2, v12, v13
	v_max3_f32 v2, v2, v14, v15
	v_max3_f32 v2, v2, v16, v17
	v_max3_f32 v2, v2, v18, v19
	v_mov_b32_e32 v44, v2
	s_nop 1
	v_permlane32_swap_b32_e32 v2, v44
	v_max3_f32 v44, v45, v2, v44
	v_mul_f32_e32 v46, 0xbe0293ee, v44
	v_fmamk_f32 v2, v20, 0x3e0293ee, v46
	v_exp_f32_e32 v20, v2
	v_fmamk_f32 v2, v4, 0x3e0293ee, v46
	v_exp_f32_e32 v48, v2
	v_fmamk_f32 v2, v21, 0x3e0293ee, v46
	v_exp_f32_e32 v4, v2
	v_fmamk_f32 v2, v5, 0x3e0293ee, v46
	v_exp_f32_e32 v2, v2
	v_add_f32_e32 v5, v20, v48
	s_waitcnt vmcnt(0) lgkmcnt(0)
	s_barrier
	v_add_f32_e32 v4, v4, v2
	v_add_f32_e32 v5, v5, v3
	v_fmamk_f32 v2, v22, 0x3e0293ee, v46
	v_add_f32_e32 v5, v4, v5
	v_add_f32_e32 v4, v4, v4
	v_fmamk_f32 v4, v6, 0x3e0293ee, v46
	v_exp_f32_e32 v20, v4
	v_fmamk_f32 v4, v23, 0x3e0293ee, v46
	v_exp_f32_e32 v2, v2
	v_exp_f32_e32 v6, v4
	v_fmamk_f32 v4, v7, 0x3e0293ee, v46
	v_exp_f32_e32 v4, v4
	v_add_f32_e32 v7, v2, v20
	v_fmamk_f32 v2, v24, 0x3e0293ee, v46
	v_exp_f32_e32 v2, v2
	v_add_f32_e32 v4, v6, v4
	v_add_f32_e32 v5, v7, v5
	s_nop 0
	v_add_f32_e32 v5, v4, v5
	v_add_f32_e32 v4, v4, v4
	v_fmamk_f32 v4, v8, 0x3e0293ee, v46
	v_exp_f32_e32 v7, v4
	v_fmamk_f32 v4, v25, 0x3e0293ee, v46
	v_exp_f32_e32 v6, v4
	v_fmamk_f32 v4, v9, 0x3e0293ee, v46
	v_exp_f32_e32 v4, v4
	v_add_f32_e32 v7, v2, v7
	v_fmamk_f32 v2, v26, 0x3e0293ee, v46
	v_exp_f32_e32 v2, v2
	v_add_f32_e32 v4, v6, v4
	v_add_f32_e32 v5, v7, v5
	s_nop 0
	v_add_f32_e32 v5, v4, v5
	v_add_f32_e32 v4, v4, v4
	v_fmamk_f32 v4, v10, 0x3e0293ee, v46
	v_exp_f32_e32 v7, v4
	v_fmamk_f32 v4, v27, 0x3e0293ee, v46
	v_exp_f32_e32 v6, v4
	v_fmamk_f32 v4, v11, 0x3e0293ee, v46
	v_exp_f32_e32 v4, v4
	v_add_f32_e32 v7, v2, v7
	v_fmamk_f32 v2, v28, 0x3e0293ee, v46
	v_exp_f32_e32 v2, v2
	v_add_f32_e32 v4, v6, v4
	v_add_f32_e32 v5, v7, v5
	s_nop 0
	v_add_f32_e32 v5, v4, v5
	v_add_f32_e32 v4, v4, v4
	v_fmamk_f32 v4, v12, 0x3e0293ee, v46
	v_exp_f32_e32 v7, v4
	v_fmamk_f32 v4, v29, 0x3e0293ee, v46
	v_exp_f32_e32 v6, v4
	v_fmamk_f32 v4, v13, 0x3e0293ee, v46
	v_exp_f32_e32 v4, v4
	v_add_f32_e32 v7, v2, v7
	v_fmamk_f32 v2, v30, 0x3e0293ee, v46
	v_exp_f32_e32 v2, v2
	v_add_f32_e32 v4, v6, v4
	v_add_f32_e32 v5, v7, v5
	s_nop 0
	v_add_f32_e32 v5, v4, v5
	v_add_f32_e32 v4, v4, v4
	v_fmamk_f32 v4, v14, 0x3e0293ee, v46
	v_exp_f32_e32 v7, v4
	v_fmamk_f32 v4, v31, 0x3e0293ee, v46
	v_exp_f32_e32 v6, v4
	v_fmamk_f32 v4, v15, 0x3e0293ee, v46
	v_exp_f32_e32 v4, v4
	v_add_f32_e32 v7, v2, v7
	v_fmamk_f32 v2, v32, 0x3e0293ee, v46
	v_exp_f32_e32 v2, v2
	v_add_f32_e32 v4, v6, v4
	v_add_f32_e32 v5, v7, v5
	s_nop 0
	v_add_f32_e32 v5, v4, v5
	v_add_f32_e32 v4, v4, v4
	v_fmamk_f32 v4, v16, 0x3e0293ee, v46
	v_exp_f32_e32 v7, v4
	v_fmamk_f32 v4, v33, 0x3e0293ee, v46
	v_exp_f32_e32 v6, v4
	v_fmamk_f32 v4, v17, 0x3e0293ee, v46
	v_exp_f32_e32 v4, v4
	v_add_f32_e32 v7, v2, v7
	v_fmamk_f32 v2, v34, 0x3e0293ee, v46
	v_exp_f32_e32 v2, v2
	v_add_f32_e32 v4, v6, v4
	v_add_f32_e32 v5, v7, v5
	s_nop 0
	v_add_f32_e32 v5, v4, v5
	v_add_f32_e32 v4, v4, v4
	v_fmamk_f32 v4, v18, 0x3e0293ee, v46
	v_exp_f32_e32 v7, v4
	v_fmamk_f32 v4, v35, 0x3e0293ee, v46
	v_fmac_f32_e32 v46, 0x3e0293ee, v19
	v_exp_f32_e32 v6, v4
	v_exp_f32_e32 v4, v46
	v_add_f32_e32 v7, v2, v7
	v_add_f32_e32 v4, v6, v4
	v_add_f32_e32 v5, v7, v5
	s_nop 0
	v_pk_add_f32 v[4:5], v[4:5], v[4:5] op_sel:[0,1] op_sel_hi:[1,0]
	s_nop 0
	v_sub_f32_e32 v5, v45, v44
	v_mul_f32_e32 v5, 0x3e0293ee, v5
	v_exp_f32_e32 v5, v5
	v_mov_b32_e32 v2, v4
	s_nop 1
	v_permlane32_swap_b32_e32 v4, v2
	v_add_f32_e32 v46, v4, v2
	v_fmac_f32_e32 v46, v47, v5
	s_branch .LBB0_1648

.LBB0_1668:
	s_nop 10
	v_fmamk_f32 v1, v80, 0x3e0293ee, v178
	v_fmamk_f32 v2, v81, 0x3e0293ee, v178
	v_fmamk_f32 v0, v96, 0x3e0293ee, v178
	v_exp_f32_e32 v4, v1
	v_fmamk_f32 v1, v97, 0x3e0293ee, v178
	v_exp_f32_e32 v5, v2
	v_fmamk_f32 v2, v98, 0x3e0293ee, v178
	v_exp_f32_e32 v0, v0
	v_exp_f32_e32 v1, v1
	v_exp_f32_e32 v14, v2
	v_fmamk_f32 v2, v82, 0x3e0293ee, v178
	v_exp_f32_e32 v98, v2
	v_fmamk_f32 v2, v99, 0x3e0293ee, v178
	v_exp_f32_e32 v15, v2
	v_mul_f32_e32 v6, v150, v0
	v_mul_f32_e32 v7, v151, v1
	v_fmamk_f32 v2, v83, 0x3e0293ee, v178
	v_exp_f32_e32 v99, v2
	v_mov_b32_dpp v8, v6 quad_perm:[1,0,3,2] row_mask:0xf bank_mask:0xf bound_ctrl:1
	v_mov_b32_dpp v9, v7 quad_perm:[1,0,3,2] row_mask:0xf bank_mask:0xf bound_ctrl:1
	v_fma_f32 v10, v150, v0, v8
	v_fma_f32 v11, v151, v1, v9
	v_mul_f32_e32 v8, v150, v14
	v_mul_f32_e32 v9, v151, v15
	s_nop 0
	v_mov_b32_dpp v12, v10 quad_perm:[2,3,0,1] row_mask:0xf bank_mask:0xf bound_ctrl:1
	v_mov_b32_dpp v0, v8 quad_perm:[1,0,3,2] row_mask:0xf bank_mask:0xf bound_ctrl:1
	v_mov_b32_dpp v1, v9 quad_perm:[1,0,3,2] row_mask:0xf bank_mask:0xf bound_ctrl:1
	v_fma_f32 v14, v150, v14, v0
	v_fma_f32 v15, v151, v15, v1
	v_mul_f32_e32 v0, v150, v4
	v_mul_f32_e32 v1, v151, v5
	v_mov_b32_dpp v13, v11 quad_perm:[2,3,0,1] row_mask:0xf bank_mask:0xf bound_ctrl:1
	v_mov_b32_dpp v82, v14 quad_perm:[2,3,0,1] row_mask:0xf bank_mask:0xf bound_ctrl:1
	v_mov_b32_dpp v80, v0 quad_perm:[1,0,3,2] row_mask:0xf bank_mask:0xf bound_ctrl:1
	v_mov_b32_dpp v81, v1 quad_perm:[1,0,3,2] row_mask:0xf bank_mask:0xf bound_ctrl:1
	v_fma_f32 v80, v150, v4, v80
	v_fma_f32 v81, v151, v5, v81
	v_mul_f32_e32 v4, v150, v98
	v_mul_f32_e32 v5, v151, v99
	v_mov_b32_dpp v83, v15 quad_perm:[2,3,0,1] row_mask:0xf bank_mask:0xf bound_ctrl:1
	v_mov_b32_dpp v96, v80 quad_perm:[2,3,0,1] row_mask:0xf bank_mask:0xf bound_ctrl:1
	v_mov_b32_dpp v154, v4 quad_perm:[1,0,3,2] row_mask:0xf bank_mask:0xf bound_ctrl:1
	v_mov_b32_dpp v155, v5 quad_perm:[1,0,3,2] row_mask:0xf bank_mask:0xf bound_ctrl:1
	v_fma_f32 v98, v150, v98, v154
	v_fma_f32 v99, v151, v99, v155
	v_mov_b32_dpp v97, v81 quad_perm:[2,3,0,1] row_mask:0xf bank_mask:0xf bound_ctrl:1
	s_nop 0
	v_mov_b32_dpp v154, v98 quad_perm:[2,3,0,1] row_mask:0xf bank_mask:0xf bound_ctrl:1
	v_mov_b32_dpp v155, v99 quad_perm:[2,3,0,1] row_mask:0xf bank_mask:0xf bound_ctrl:1
	s_and_saveexec_b64 s[14:15], s[8:9]
	s_cbranch_execz .LBB0_1670
	v_add_f32_e32 v14, v14, v82
	v_add_f32_e32 v15, v15, v83
	v_add_f32_e32 v12, v10, v12
	v_add_f32_e32 v13, v11, v13
	v_add_f32_e32 v82, v98, v154
	v_add_f32_e32 v83, v99, v155
	v_add_f32_e32 v80, v80, v96
	v_add_f32_e32 v81, v81, v97
	ds_write_b128 v179, v[12:15]
	ds_write_b128 v179, v[80:83] offset:128
.LBB0_1670:
	s_or_b64 exec, exec, s[14:15]
	v_fmamk_f32 v2, v100, 0x3e0293ee, v178
	v_exp_f32_e32 v82, v2
	v_fmamk_f32 v2, v84, 0x3e0293ee, v178
	v_exp_f32_e32 v96, v2
	v_fmamk_f32 v2, v101, 0x3e0293ee, v178
	v_exp_f32_e32 v83, v2
	v_fmamk_f32 v2, v85, 0x3e0293ee, v178
	v_exp_f32_e32 v97, v2
	v_fmamk_f32 v2, v102, 0x3e0293ee, v178
	v_exp_f32_e32 v98, v2
	v_fmamk_f32 v2, v86, 0x3e0293ee, v178
	v_exp_f32_e32 v102, v2
	v_fmamk_f32 v2, v103, 0x3e0293ee, v178
	v_exp_f32_e32 v99, v2
	v_fmamk_f32 v2, v87, 0x3e0293ee, v178
	v_exp_f32_e32 v103, v2
	v_mul_f32_e32 v80, v150, v82
	v_mul_f32_e32 v81, v151, v83
	v_mul_f32_e32 v14, v150, v98
	v_mul_f32_e32 v15, v151, v99
	v_mul_f32_e32 v10, v150, v96
	v_mul_f32_e32 v11, v151, v97
	v_mul_f32_e32 v12, v150, v102
	v_mul_f32_e32 v13, v151, v103
	v_mov_b32_dpp v86, v14 quad_perm:[1,0,3,2] row_mask:0xf bank_mask:0xf bound_ctrl:1
	v_mov_b32_dpp v87, v15 quad_perm:[1,0,3,2] row_mask:0xf bank_mask:0xf bound_ctrl:1
	v_mov_b32_dpp v84, v80 quad_perm:[1,0,3,2] row_mask:0xf bank_mask:0xf bound_ctrl:1
	v_mov_b32_dpp v85, v81 quad_perm:[1,0,3,2] row_mask:0xf bank_mask:0xf bound_ctrl:1
	v_fma_f32 v98, v150, v98, v86
	v_fma_f32 v99, v151, v99, v87
	v_mov_b32_dpp v86, v10 quad_perm:[1,0,3,2] row_mask:0xf bank_mask:0xf bound_ctrl:1
	v_mov_b32_dpp v87, v11 quad_perm:[1,0,3,2] row_mask:0xf bank_mask:0xf bound_ctrl:1
	v_mov_b32_dpp v154, v12 quad_perm:[1,0,3,2] row_mask:0xf bank_mask:0xf bound_ctrl:1
	v_mov_b32_dpp v155, v13 quad_perm:[1,0,3,2] row_mask:0xf bank_mask:0xf bound_ctrl:1
	v_fma_f32 v82, v150, v82, v84
	v_fma_f32 v83, v151, v83, v85
	v_fma_f32 v86, v150, v96, v86
	v_fma_f32 v87, v151, v97, v87
	v_fma_f32 v102, v150, v102, v154
	v_fma_f32 v103, v151, v103, v155
	v_mov_b32_dpp v84, v82 quad_perm:[2,3,0,1] row_mask:0xf bank_mask:0xf bound_ctrl:1
	v_mov_b32_dpp v85, v83 quad_perm:[2,3,0,1] row_mask:0xf bank_mask:0xf bound_ctrl:1
	v_mov_b32_dpp v100, v98 quad_perm:[2,3,0,1] row_mask:0xf bank_mask:0xf bound_ctrl:1
	v_mov_b32_dpp v101, v99 quad_perm:[2,3,0,1] row_mask:0xf bank_mask:0xf bound_ctrl:1
	v_mov_b32_dpp v96, v86 quad_perm:[2,3,0,1] row_mask:0xf bank_mask:0xf bound_ctrl:1
	v_mov_b32_dpp v97, v87 quad_perm:[2,3,0,1] row_mask:0xf bank_mask:0xf bound_ctrl:1
	v_mov_b32_dpp v154, v102 quad_perm:[2,3,0,1] row_mask:0xf bank_mask:0xf bound_ctrl:1
	v_mov_b32_dpp v155, v103 quad_perm:[2,3,0,1] row_mask:0xf bank_mask:0xf bound_ctrl:1
	s_and_saveexec_b64 s[14:15], s[8:9]
	s_cbranch_execz .LBB0_1672
	v_add_f32_e32 v100, v98, v100
	v_add_f32_e32 v101, v99, v101
	v_add_f32_e32 v98, v82, v84
	v_add_f32_e32 v99, v83, v85
	v_add_f32_e32 v84, v102, v154
	v_add_f32_e32 v85, v103, v155
	v_add_f32_e32 v82, v86, v96
	v_add_f32_e32 v83, v87, v97
	ds_write_b128 v179, v[98:101] offset:32
	ds_write_b128 v179, v[82:85] offset:160
.LBB0_1672:
	s_or_b64 exec, exec, s[14:15]
	v_fmamk_f32 v2, v104, 0x3e0293ee, v178
	v_exp_f32_e32 v96, v2
	v_fmamk_f32 v2, v88, 0x3e0293ee, v178
	v_exp_f32_e32 v98, v2
	v_fmamk_f32 v2, v105, 0x3e0293ee, v178
	v_exp_f32_e32 v97, v2
	v_fmamk_f32 v2, v89, 0x3e0293ee, v178
	v_exp_f32_e32 v99, v2
	v_fmamk_f32 v2, v106, 0x3e0293ee, v178
	v_exp_f32_e32 v100, v2
	v_fmamk_f32 v2, v90, 0x3e0293ee, v178
	v_exp_f32_e32 v106, v2
	v_fmamk_f32 v2, v107, 0x3e0293ee, v178
	v_exp_f32_e32 v101, v2
	v_fmamk_f32 v2, v91, 0x3e0293ee, v178
	v_exp_f32_e32 v107, v2
	v_mul_f32_e32 v88, v150, v96
	v_mul_f32_e32 v89, v151, v97
	v_mul_f32_e32 v86, v150, v100
	v_mul_f32_e32 v87, v151, v101
	v_mul_f32_e32 v82, v150, v98
	v_mul_f32_e32 v83, v151, v99
	v_mul_f32_e32 v84, v150, v106
	v_mul_f32_e32 v85, v151, v107
	v_mov_b32_dpp v102, v86 quad_perm:[1,0,3,2] row_mask:0xf bank_mask:0xf bound_ctrl:1
	v_mov_b32_dpp v103, v87 quad_perm:[1,0,3,2] row_mask:0xf bank_mask:0xf bound_ctrl:1
	v_mov_b32_dpp v90, v88 quad_perm:[1,0,3,2] row_mask:0xf bank_mask:0xf bound_ctrl:1
	v_mov_b32_dpp v91, v89 quad_perm:[1,0,3,2] row_mask:0xf bank_mask:0xf bound_ctrl:1
	v_fma_f32 v102, v150, v100, v102
	v_fma_f32 v103, v151, v101, v103
	v_mov_b32_dpp v100, v82 quad_perm:[1,0,3,2] row_mask:0xf bank_mask:0xf bound_ctrl:1
	v_mov_b32_dpp v101, v83 quad_perm:[1,0,3,2] row_mask:0xf bank_mask:0xf bound_ctrl:1
	v_mov_b32_dpp v154, v84 quad_perm:[1,0,3,2] row_mask:0xf bank_mask:0xf bound_ctrl:1
	v_mov_b32_dpp v155, v85 quad_perm:[1,0,3,2] row_mask:0xf bank_mask:0xf bound_ctrl:1
	v_fma_f32 v90, v150, v96, v90
	v_fma_f32 v91, v151, v97, v91
	v_fma_f32 v98, v150, v98, v100
	v_fma_f32 v99, v151, v99, v101
	v_fma_f32 v106, v150, v106, v154
	v_fma_f32 v107, v151, v107, v155
	v_mov_b32_dpp v96, v90 quad_perm:[2,3,0,1] row_mask:0xf bank_mask:0xf bound_ctrl:1
	v_mov_b32_dpp v97, v91 quad_perm:[2,3,0,1] row_mask:0xf bank_mask:0xf bound_ctrl:1
	v_mov_b32_dpp v104, v102 quad_perm:[2,3,0,1] row_mask:0xf bank_mask:0xf bound_ctrl:1
	v_mov_b32_dpp v105, v103 quad_perm:[2,3,0,1] row_mask:0xf bank_mask:0xf bound_ctrl:1
	v_mov_b32_dpp v100, v98 quad_perm:[2,3,0,1] row_mask:0xf bank_mask:0xf bound_ctrl:1
	v_mov_b32_dpp v101, v99 quad_perm:[2,3,0,1] row_mask:0xf bank_mask:0xf bound_ctrl:1
	v_mov_b32_dpp v154, v106 quad_perm:[2,3,0,1] row_mask:0xf bank_mask:0xf bound_ctrl:1
	v_mov_b32_dpp v155, v107 quad_perm:[2,3,0,1] row_mask:0xf bank_mask:0xf bound_ctrl:1
	s_and_saveexec_b64 s[14:15], s[8:9]
	s_cbranch_execz .LBB0_1674
	v_add_f32_e32 v104, v102, v104
	v_add_f32_e32 v105, v103, v105
	v_add_f32_e32 v102, v90, v96
	v_add_f32_e32 v103, v91, v97
	v_add_f32_e32 v188, v106, v154
	v_add_f32_e32 v189, v107, v155
	v_add_f32_e32 v186, v98, v100
	v_add_f32_e32 v187, v99, v101
	ds_write_b128 v179, v[102:105] offset:64
	ds_write_b128 v179, v[186:189] offset:192
.LBB0_1674:
	s_or_b64 exec, exec, s[14:15]
	v_fmamk_f32 v2, v108, 0x3e0293ee, v178
	v_exp_f32_e32 v98, v2
	v_fmamk_f32 v2, v92, 0x3e0293ee, v178
	v_exp_f32_e32 v102, v2
	v_fmamk_f32 v2, v109, 0x3e0293ee, v178
	v_exp_f32_e32 v99, v2
	v_fmamk_f32 v2, v93, 0x3e0293ee, v178
	v_exp_f32_e32 v103, v2
	v_fmamk_f32 v2, v110, 0x3e0293ee, v178
	v_exp_f32_e32 v104, v2
	v_fmamk_f32 v2, v94, 0x3e0293ee, v178
	v_exp_f32_e32 v110, v2
	v_fmamk_f32 v2, v111, 0x3e0293ee, v178
	v_exp_f32_e32 v105, v2
	v_fmamk_f32 v2, v95, 0x3e0293ee, v178
	v_exp_f32_e32 v111, v2
	v_mul_f32_e32 v96, v150, v98
	v_mul_f32_e32 v97, v151, v99
	v_mul_f32_e32 v94, v150, v104
	v_mul_f32_e32 v95, v151, v105
	v_mul_f32_e32 v90, v150, v102
	v_mul_f32_e32 v91, v151, v103
	v_mul_f32_e32 v92, v150, v110
	v_mul_f32_e32 v93, v151, v111
	v_mov_b32_dpp v106, v94 quad_perm:[1,0,3,2] row_mask:0xf bank_mask:0xf bound_ctrl:1
	v_mov_b32_dpp v107, v95 quad_perm:[1,0,3,2] row_mask:0xf bank_mask:0xf bound_ctrl:1
	v_mov_b32_dpp v100, v96 quad_perm:[1,0,3,2] row_mask:0xf bank_mask:0xf bound_ctrl:1
	v_mov_b32_dpp v101, v97 quad_perm:[1,0,3,2] row_mask:0xf bank_mask:0xf bound_ctrl:1
	v_fma_f32 v106, v150, v104, v106
	v_fma_f32 v107, v151, v105, v107
	v_mov_b32_dpp v104, v90 quad_perm:[1,0,3,2] row_mask:0xf bank_mask:0xf bound_ctrl:1
	v_mov_b32_dpp v105, v91 quad_perm:[1,0,3,2] row_mask:0xf bank_mask:0xf bound_ctrl:1
	v_mov_b32_dpp v154, v92 quad_perm:[1,0,3,2] row_mask:0xf bank_mask:0xf bound_ctrl:1
	v_mov_b32_dpp v155, v93 quad_perm:[1,0,3,2] row_mask:0xf bank_mask:0xf bound_ctrl:1
	v_fma_f32 v98, v150, v98, v100
	v_fma_f32 v99, v151, v99, v101
	v_fma_f32 v102, v150, v102, v104
	v_fma_f32 v103, v151, v103, v105
	v_fma_f32 v110, v150, v110, v154
	v_fma_f32 v111, v151, v111, v155
	v_mov_b32_dpp v100, v98 quad_perm:[2,3,0,1] row_mask:0xf bank_mask:0xf bound_ctrl:1
	v_mov_b32_dpp v101, v99 quad_perm:[2,3,0,1] row_mask:0xf bank_mask:0xf bound_ctrl:1
	v_mov_b32_dpp v108, v106 quad_perm:[2,3,0,1] row_mask:0xf bank_mask:0xf bound_ctrl:1
	v_mov_b32_dpp v109, v107 quad_perm:[2,3,0,1] row_mask:0xf bank_mask:0xf bound_ctrl:1
	v_mov_b32_dpp v104, v102 quad_perm:[2,3,0,1] row_mask:0xf bank_mask:0xf bound_ctrl:1
	v_mov_b32_dpp v105, v103 quad_perm:[2,3,0,1] row_mask:0xf bank_mask:0xf bound_ctrl:1
	v_mov_b32_dpp v154, v110 quad_perm:[2,3,0,1] row_mask:0xf bank_mask:0xf bound_ctrl:1
	v_mov_b32_dpp v155, v111 quad_perm:[2,3,0,1] row_mask:0xf bank_mask:0xf bound_ctrl:1
	s_and_saveexec_b64 s[14:15], s[8:9]
	s_cbranch_execz .LBB0_1676
	v_add_f32_e32 v108, v106, v108
	v_add_f32_e32 v109, v107, v109
	v_add_f32_e32 v106, v98, v100
	v_add_f32_e32 v107, v99, v101
	v_add_f32_e32 v100, v110, v154
	v_add_f32_e32 v101, v111, v155
	v_add_f32_e32 v98, v102, v104
	v_add_f32_e32 v99, v103, v105
	ds_write_b128 v179, v[106:109] offset:96
	ds_write_b128 v179, v[98:101] offset:224

.LBB0_1681:
	s_nop 10
	v_fmamk_f32 v1, v80, 0x3e0293ee, v178
	v_fmamk_f32 v2, v81, 0x3e0293ee, v178
	v_fmamk_f32 v0, v96, 0x3e0293ee, v178
	v_exp_f32_e32 v4, v1
	v_fmamk_f32 v1, v97, 0x3e0293ee, v178
	v_exp_f32_e32 v5, v2
	v_fmamk_f32 v2, v98, 0x3e0293ee, v178
	v_exp_f32_e32 v0, v0
	v_exp_f32_e32 v1, v1
	v_exp_f32_e32 v14, v2
	v_fmamk_f32 v2, v82, 0x3e0293ee, v178
	v_exp_f32_e32 v98, v2
	v_fmamk_f32 v2, v99, 0x3e0293ee, v178
	v_exp_f32_e32 v15, v2
	v_mul_f32_e32 v6, v150, v0
	v_mul_f32_e32 v7, v151, v1
	v_fmamk_f32 v2, v83, 0x3e0293ee, v178
	v_exp_f32_e32 v99, v2
	v_mov_b32_dpp v8, v6 quad_perm:[1,0,3,2] row_mask:0xf bank_mask:0xf bound_ctrl:1
	v_mov_b32_dpp v9, v7 quad_perm:[1,0,3,2] row_mask:0xf bank_mask:0xf bound_ctrl:1
	v_fma_f32 v10, v150, v0, v8
	v_fma_f32 v11, v151, v1, v9
	v_mul_f32_e32 v8, v150, v14
	v_mul_f32_e32 v9, v151, v15
	s_nop 0
	v_mov_b32_dpp v12, v10 quad_perm:[2,3,0,1] row_mask:0xf bank_mask:0xf bound_ctrl:1
	v_mov_b32_dpp v0, v8 quad_perm:[1,0,3,2] row_mask:0xf bank_mask:0xf bound_ctrl:1
	v_mov_b32_dpp v1, v9 quad_perm:[1,0,3,2] row_mask:0xf bank_mask:0xf bound_ctrl:1
	v_fma_f32 v14, v150, v14, v0
	v_fma_f32 v15, v151, v15, v1
	v_mul_f32_e32 v0, v150, v4
	v_mul_f32_e32 v1, v151, v5
	v_mov_b32_dpp v13, v11 quad_perm:[2,3,0,1] row_mask:0xf bank_mask:0xf bound_ctrl:1
	v_mov_b32_dpp v82, v14 quad_perm:[2,3,0,1] row_mask:0xf bank_mask:0xf bound_ctrl:1
	v_mov_b32_dpp v80, v0 quad_perm:[1,0,3,2] row_mask:0xf bank_mask:0xf bound_ctrl:1
	v_mov_b32_dpp v81, v1 quad_perm:[1,0,3,2] row_mask:0xf bank_mask:0xf bound_ctrl:1
	v_fma_f32 v80, v150, v4, v80
	v_fma_f32 v81, v151, v5, v81
	v_mul_f32_e32 v4, v150, v98
	v_mul_f32_e32 v5, v151, v99
	v_mov_b32_dpp v83, v15 quad_perm:[2,3,0,1] row_mask:0xf bank_mask:0xf bound_ctrl:1
	v_mov_b32_dpp v96, v80 quad_perm:[2,3,0,1] row_mask:0xf bank_mask:0xf bound_ctrl:1
	v_mov_b32_dpp v154, v4 quad_perm:[1,0,3,2] row_mask:0xf bank_mask:0xf bound_ctrl:1
	v_mov_b32_dpp v155, v5 quad_perm:[1,0,3,2] row_mask:0xf bank_mask:0xf bound_ctrl:1
	v_fma_f32 v98, v150, v98, v154
	v_fma_f32 v99, v151, v99, v155
	v_mov_b32_dpp v97, v81 quad_perm:[2,3,0,1] row_mask:0xf bank_mask:0xf bound_ctrl:1
	s_nop 0
	v_mov_b32_dpp v154, v98 quad_perm:[2,3,0,1] row_mask:0xf bank_mask:0xf bound_ctrl:1
	v_mov_b32_dpp v155, v99 quad_perm:[2,3,0,1] row_mask:0xf bank_mask:0xf bound_ctrl:1
	s_and_saveexec_b64 s[14:15], s[8:9]
	s_cbranch_execz .LBB0_1683
	v_add_f32_e32 v14, v14, v82
	v_add_f32_e32 v15, v15, v83
	v_add_f32_e32 v12, v10, v12
	v_add_f32_e32 v13, v11, v13
	v_add_f32_e32 v82, v98, v154
	v_add_f32_e32 v83, v99, v155
	v_add_f32_e32 v80, v80, v96
	v_add_f32_e32 v81, v81, v97
	ds_write_b128 v179, v[12:15] offset:256
	ds_write_b128 v179, v[80:83] offset:384
.LBB0_1683:
	s_or_b64 exec, exec, s[14:15]
	v_fmamk_f32 v2, v100, 0x3e0293ee, v178
	v_exp_f32_e32 v82, v2
	v_fmamk_f32 v2, v84, 0x3e0293ee, v178
	v_exp_f32_e32 v96, v2
	v_fmamk_f32 v2, v101, 0x3e0293ee, v178
	v_exp_f32_e32 v83, v2
	v_fmamk_f32 v2, v85, 0x3e0293ee, v178
	v_exp_f32_e32 v97, v2
	v_fmamk_f32 v2, v102, 0x3e0293ee, v178
	v_exp_f32_e32 v98, v2
	v_fmamk_f32 v2, v86, 0x3e0293ee, v178
	v_exp_f32_e32 v102, v2
	v_fmamk_f32 v2, v103, 0x3e0293ee, v178
	v_exp_f32_e32 v99, v2
	v_fmamk_f32 v2, v87, 0x3e0293ee, v178
	v_exp_f32_e32 v103, v2
	v_mul_f32_e32 v80, v150, v82
	v_mul_f32_e32 v81, v151, v83
	v_mul_f32_e32 v14, v150, v98
	v_mul_f32_e32 v15, v151, v99
	v_mul_f32_e32 v10, v150, v96
	v_mul_f32_e32 v11, v151, v97
	v_mul_f32_e32 v12, v150, v102
	v_mul_f32_e32 v13, v151, v103
	v_mov_b32_dpp v86, v14 quad_perm:[1,0,3,2] row_mask:0xf bank_mask:0xf bound_ctrl:1
	v_mov_b32_dpp v87, v15 quad_perm:[1,0,3,2] row_mask:0xf bank_mask:0xf bound_ctrl:1
	v_mov_b32_dpp v84, v80 quad_perm:[1,0,3,2] row_mask:0xf bank_mask:0xf bound_ctrl:1
	v_mov_b32_dpp v85, v81 quad_perm:[1,0,3,2] row_mask:0xf bank_mask:0xf bound_ctrl:1
	v_fma_f32 v98, v150, v98, v86
	v_fma_f32 v99, v151, v99, v87
	v_mov_b32_dpp v86, v10 quad_perm:[1,0,3,2] row_mask:0xf bank_mask:0xf bound_ctrl:1
	v_mov_b32_dpp v87, v11 quad_perm:[1,0,3,2] row_mask:0xf bank_mask:0xf bound_ctrl:1
	v_mov_b32_dpp v154, v12 quad_perm:[1,0,3,2] row_mask:0xf bank_mask:0xf bound_ctrl:1
	v_mov_b32_dpp v155, v13 quad_perm:[1,0,3,2] row_mask:0xf bank_mask:0xf bound_ctrl:1
	v_fma_f32 v82, v150, v82, v84
	v_fma_f32 v83, v151, v83, v85
	v_fma_f32 v86, v150, v96, v86
	v_fma_f32 v87, v151, v97, v87
	v_fma_f32 v102, v150, v102, v154
	v_fma_f32 v103, v151, v103, v155
	v_mov_b32_dpp v84, v82 quad_perm:[2,3,0,1] row_mask:0xf bank_mask:0xf bound_ctrl:1
	v_mov_b32_dpp v85, v83 quad_perm:[2,3,0,1] row_mask:0xf bank_mask:0xf bound_ctrl:1
	v_mov_b32_dpp v100, v98 quad_perm:[2,3,0,1] row_mask:0xf bank_mask:0xf bound_ctrl:1
	v_mov_b32_dpp v101, v99 quad_perm:[2,3,0,1] row_mask:0xf bank_mask:0xf bound_ctrl:1
	v_mov_b32_dpp v96, v86 quad_perm:[2,3,0,1] row_mask:0xf bank_mask:0xf bound_ctrl:1
	v_mov_b32_dpp v97, v87 quad_perm:[2,3,0,1] row_mask:0xf bank_mask:0xf bound_ctrl:1
	v_mov_b32_dpp v154, v102 quad_perm:[2,3,0,1] row_mask:0xf bank_mask:0xf bound_ctrl:1
	v_mov_b32_dpp v155, v103 quad_perm:[2,3,0,1] row_mask:0xf bank_mask:0xf bound_ctrl:1
	s_and_saveexec_b64 s[14:15], s[8:9]
	s_cbranch_execz .LBB0_1685
	v_add_f32_e32 v100, v98, v100
	v_add_f32_e32 v101, v99, v101
	v_add_f32_e32 v98, v82, v84
	v_add_f32_e32 v99, v83, v85
	v_add_f32_e32 v84, v102, v154
	v_add_f32_e32 v85, v103, v155
	v_add_f32_e32 v82, v86, v96
	v_add_f32_e32 v83, v87, v97
	ds_write_b128 v179, v[98:101] offset:288
	ds_write_b128 v179, v[82:85] offset:416
.LBB0_1685:
	s_or_b64 exec, exec, s[14:15]
	v_fmamk_f32 v2, v104, 0x3e0293ee, v178
	v_exp_f32_e32 v96, v2
	v_fmamk_f32 v2, v88, 0x3e0293ee, v178
	v_exp_f32_e32 v98, v2
	v_fmamk_f32 v2, v105, 0x3e0293ee, v178
	v_exp_f32_e32 v97, v2
	v_fmamk_f32 v2, v89, 0x3e0293ee, v178
	v_exp_f32_e32 v99, v2
	v_fmamk_f32 v2, v106, 0x3e0293ee, v178
	v_exp_f32_e32 v100, v2
	v_fmamk_f32 v2, v90, 0x3e0293ee, v178
	v_exp_f32_e32 v106, v2
	v_fmamk_f32 v2, v107, 0x3e0293ee, v178
	v_exp_f32_e32 v101, v2
	v_fmamk_f32 v2, v91, 0x3e0293ee, v178
	v_exp_f32_e32 v107, v2
	v_mul_f32_e32 v88, v150, v96
	v_mul_f32_e32 v89, v151, v97
	v_mul_f32_e32 v86, v150, v100
	v_mul_f32_e32 v87, v151, v101
	v_mul_f32_e32 v82, v150, v98
	v_mul_f32_e32 v83, v151, v99
	v_mul_f32_e32 v84, v150, v106
	v_mul_f32_e32 v85, v151, v107
	v_mov_b32_dpp v102, v86 quad_perm:[1,0,3,2] row_mask:0xf bank_mask:0xf bound_ctrl:1
	v_mov_b32_dpp v103, v87 quad_perm:[1,0,3,2] row_mask:0xf bank_mask:0xf bound_ctrl:1
	v_mov_b32_dpp v90, v88 quad_perm:[1,0,3,2] row_mask:0xf bank_mask:0xf bound_ctrl:1
	v_mov_b32_dpp v91, v89 quad_perm:[1,0,3,2] row_mask:0xf bank_mask:0xf bound_ctrl:1
	v_fma_f32 v102, v150, v100, v102
	v_fma_f32 v103, v151, v101, v103
	v_mov_b32_dpp v100, v82 quad_perm:[1,0,3,2] row_mask:0xf bank_mask:0xf bound_ctrl:1
	v_mov_b32_dpp v101, v83 quad_perm:[1,0,3,2] row_mask:0xf bank_mask:0xf bound_ctrl:1
	v_mov_b32_dpp v154, v84 quad_perm:[1,0,3,2] row_mask:0xf bank_mask:0xf bound_ctrl:1
	v_mov_b32_dpp v155, v85 quad_perm:[1,0,3,2] row_mask:0xf bank_mask:0xf bound_ctrl:1
	v_fma_f32 v90, v150, v96, v90
	v_fma_f32 v91, v151, v97, v91
	v_fma_f32 v98, v150, v98, v100
	v_fma_f32 v99, v151, v99, v101
	v_fma_f32 v106, v150, v106, v154
	v_fma_f32 v107, v151, v107, v155
	v_mov_b32_dpp v96, v90 quad_perm:[2,3,0,1] row_mask:0xf bank_mask:0xf bound_ctrl:1
	v_mov_b32_dpp v97, v91 quad_perm:[2,3,0,1] row_mask:0xf bank_mask:0xf bound_ctrl:1
	v_mov_b32_dpp v104, v102 quad_perm:[2,3,0,1] row_mask:0xf bank_mask:0xf bound_ctrl:1
	v_mov_b32_dpp v105, v103 quad_perm:[2,3,0,1] row_mask:0xf bank_mask:0xf bound_ctrl:1
	v_mov_b32_dpp v100, v98 quad_perm:[2,3,0,1] row_mask:0xf bank_mask:0xf bound_ctrl:1
	v_mov_b32_dpp v101, v99 quad_perm:[2,3,0,1] row_mask:0xf bank_mask:0xf bound_ctrl:1
	v_mov_b32_dpp v154, v106 quad_perm:[2,3,0,1] row_mask:0xf bank_mask:0xf bound_ctrl:1
	v_mov_b32_dpp v155, v107 quad_perm:[2,3,0,1] row_mask:0xf bank_mask:0xf bound_ctrl:1
	s_and_saveexec_b64 s[14:15], s[8:9]
	s_cbranch_execz .LBB0_1687
	v_add_f32_e32 v104, v102, v104
	v_add_f32_e32 v105, v103, v105
	v_add_f32_e32 v102, v90, v96
	v_add_f32_e32 v103, v91, v97
	v_add_f32_e32 v188, v106, v154
	v_add_f32_e32 v189, v107, v155
	v_add_f32_e32 v186, v98, v100
	v_add_f32_e32 v187, v99, v101
	ds_write_b128 v179, v[102:105] offset:320
	ds_write_b128 v179, v[186:189] offset:448
.LBB0_1687:
	s_or_b64 exec, exec, s[14:15]
	v_fmamk_f32 v2, v108, 0x3e0293ee, v178
	v_exp_f32_e32 v98, v2
	v_fmamk_f32 v2, v92, 0x3e0293ee, v178
	v_exp_f32_e32 v102, v2
	v_fmamk_f32 v2, v109, 0x3e0293ee, v178
	v_exp_f32_e32 v99, v2
	v_fmamk_f32 v2, v93, 0x3e0293ee, v178
	v_exp_f32_e32 v103, v2
	v_fmamk_f32 v2, v110, 0x3e0293ee, v178
	v_exp_f32_e32 v104, v2
	v_fmamk_f32 v2, v94, 0x3e0293ee, v178
	v_exp_f32_e32 v110, v2
	v_fmamk_f32 v2, v111, 0x3e0293ee, v178
	v_exp_f32_e32 v105, v2
	v_fmamk_f32 v2, v95, 0x3e0293ee, v178
	v_exp_f32_e32 v111, v2
	v_mul_f32_e32 v96, v150, v98
	v_mul_f32_e32 v97, v151, v99
	v_mul_f32_e32 v94, v150, v104
	v_mul_f32_e32 v95, v151, v105
	v_mul_f32_e32 v90, v150, v102
	v_mul_f32_e32 v91, v151, v103
	v_mul_f32_e32 v92, v150, v110
	v_mul_f32_e32 v93, v151, v111
	v_mov_b32_dpp v106, v94 quad_perm:[1,0,3,2] row_mask:0xf bank_mask:0xf bound_ctrl:1
	v_mov_b32_dpp v107, v95 quad_perm:[1,0,3,2] row_mask:0xf bank_mask:0xf bound_ctrl:1
	v_mov_b32_dpp v100, v96 quad_perm:[1,0,3,2] row_mask:0xf bank_mask:0xf bound_ctrl:1
	v_mov_b32_dpp v101, v97 quad_perm:[1,0,3,2] row_mask:0xf bank_mask:0xf bound_ctrl:1
	v_fma_f32 v106, v150, v104, v106
	v_fma_f32 v107, v151, v105, v107
	v_mov_b32_dpp v104, v90 quad_perm:[1,0,3,2] row_mask:0xf bank_mask:0xf bound_ctrl:1
	v_mov_b32_dpp v105, v91 quad_perm:[1,0,3,2] row_mask:0xf bank_mask:0xf bound_ctrl:1
	v_mov_b32_dpp v154, v92 quad_perm:[1,0,3,2] row_mask:0xf bank_mask:0xf bound_ctrl:1
	v_mov_b32_dpp v155, v93 quad_perm:[1,0,3,2] row_mask:0xf bank_mask:0xf bound_ctrl:1
	v_fma_f32 v98, v150, v98, v100
	v_fma_f32 v99, v151, v99, v101
	v_fma_f32 v102, v150, v102, v104
	v_fma_f32 v103, v151, v103, v105
	v_fma_f32 v110, v150, v110, v154
	v_fma_f32 v111, v151, v111, v155
	v_mov_b32_dpp v100, v98 quad_perm:[2,3,0,1] row_mask:0xf bank_mask:0xf bound_ctrl:1
	v_mov_b32_dpp v101, v99 quad_perm:[2,3,0,1] row_mask:0xf bank_mask:0xf bound_ctrl:1
	v_mov_b32_dpp v108, v106 quad_perm:[2,3,0,1] row_mask:0xf bank_mask:0xf bound_ctrl:1
	v_mov_b32_dpp v109, v107 quad_perm:[2,3,0,1] row_mask:0xf bank_mask:0xf bound_ctrl:1
	v_mov_b32_dpp v104, v102 quad_perm:[2,3,0,1] row_mask:0xf bank_mask:0xf bound_ctrl:1
	v_mov_b32_dpp v105, v103 quad_perm:[2,3,0,1] row_mask:0xf bank_mask:0xf bound_ctrl:1
	v_mov_b32_dpp v154, v110 quad_perm:[2,3,0,1] row_mask:0xf bank_mask:0xf bound_ctrl:1
	v_mov_b32_dpp v155, v111 quad_perm:[2,3,0,1] row_mask:0xf bank_mask:0xf bound_ctrl:1
	s_and_saveexec_b64 s[14:15], s[8:9]
	s_cbranch_execz .LBB0_1662
	v_add_f32_e32 v108, v106, v108
	v_add_f32_e32 v109, v107, v109
	v_add_f32_e32 v106, v98, v100
	v_add_f32_e32 v107, v99, v101
	v_add_f32_e32 v100, v110, v154
	v_add_f32_e32 v101, v111, v155
	v_add_f32_e32 v98, v102, v104
	v_add_f32_e32 v99, v103, v105
	ds_write_b128 v179, v[106:109] offset:352
	ds_write_b128 v179, v[98:101] offset:480
	s_branch .LBB0_1662

.LBB0_1707:
	s_or_b64 exec, exec, s[4:5]
	s_waitcnt lgkmcnt(0)
	s_waitcnt lgkmcnt(0)
	v_lshlrev_b32_e32 v1, 2, v2
	v_lshl_add_u32 v2, v2, 4, s45
	ds_read_b128 v[4:7], v2
	s_add_i32 s72, 0, 0x10000
	v_lshl_add_u32 v0, v0, 1, s72
	v_or_b32_e32 v8, s48, v1
	v_mad_u64_u32 v[8:9], s[4:5], v8, s71, v[0:1]
	s_waitcnt lgkmcnt(0)
	v_mul_f32_e32 v9, v64, v4
	v_bfe_u32 v10, v9, 16, 1
	v_add3_u32 v9, v9, v10, s96
	ds_write_b16_d16_hi v8, v9
	v_mul_f32_e32 v9, v48, v4
	v_bfe_u32 v10, v9, 16, 1
	v_add3_u32 v9, v9, v10, s96
	ds_write_b16_d16_hi v8, v9 offset:64
	v_mul_f32_e32 v9, v32, v4
	v_bfe_u32 v10, v9, 16, 1
	v_add3_u32 v9, v9, v10, s96
	v_mul_f32_e32 v4, v16, v4
	ds_write_b16_d16_hi v8, v9 offset:128
	v_bfe_u32 v9, v4, 16, 1
	v_add3_u32 v4, v4, v9, s96
	ds_write_b16_d16_hi v8, v4 offset:192
	v_or_b32_e32 v4, s49, v1
	v_mad_u64_u32 v[8:9], s[4:5], v4, s71, v[0:1]
	v_mul_f32_e32 v4, v65, v5
	v_bfe_u32 v9, v4, 16, 1
	v_add3_u32 v4, v4, v9, s96
	ds_write_b16_d16_hi v8, v4
	v_mul_f32_e32 v4, v49, v5
	v_bfe_u32 v9, v4, 16, 1
	v_add3_u32 v4, v4, v9, s96
	ds_write_b16_d16_hi v8, v4 offset:64
	v_mul_f32_e32 v4, v33, v5
	v_bfe_u32 v9, v4, 16, 1
	v_add3_u32 v4, v4, v9, s96
	ds_write_b16_d16_hi v8, v4 offset:128
	v_mul_f32_e32 v4, v17, v5
	v_bfe_u32 v5, v4, 16, 1
	v_add3_u32 v4, v4, v5, s96
	ds_write_b16_d16_hi v8, v4 offset:192
	v_or_b32_e32 v4, s56, v1
	v_mad_u64_u32 v[4:5], s[4:5], v4, s71, v[0:1]
	v_mul_f32_e32 v5, v66, v6
	v_bfe_u32 v8, v5, 16, 1
	v_add3_u32 v5, v5, v8, s96
	ds_write_b16_d16_hi v4, v5
	v_mul_f32_e32 v5, v50, v6
	v_bfe_u32 v8, v5, 16, 1
	v_add3_u32 v5, v5, v8, s96
	ds_write_b16_d16_hi v4, v5 offset:64
	v_mul_f32_e32 v5, v34, v6
	v_bfe_u32 v8, v5, 16, 1
	v_add3_u32 v5, v5, v8, s96
	ds_write_b16_d16_hi v4, v5 offset:128
	v_mul_f32_e32 v5, v18, v6
	v_bfe_u32 v6, v5, 16, 1
	v_add3_u32 v5, v5, v6, s96
	ds_write_b16_d16_hi v4, v5 offset:192
	v_or_b32_e32 v4, s57, v1
	v_mad_u64_u32 v[4:5], s[4:5], v4, s71, v[0:1]
	v_mul_f32_e32 v5, v67, v7
	v_bfe_u32 v6, v5, 16, 1
	v_add3_u32 v5, v5, v6, s96
	ds_write_b16_d16_hi v4, v5
	v_mul_f32_e32 v5, v51, v7
	v_bfe_u32 v6, v5, 16, 1
	v_add3_u32 v5, v5, v6, s96
	ds_write_b16_d16_hi v4, v5 offset:64
	v_mul_f32_e32 v5, v35, v7
	v_bfe_u32 v6, v5, 16, 1
	v_add3_u32 v5, v5, v6, s96
	ds_write_b16_d16_hi v4, v5 offset:128
	v_mul_f32_e32 v5, v19, v7
	v_bfe_u32 v6, v5, 16, 1
	v_add3_u32 v5, v5, v6, s96
	ds_write_b16_d16_hi v4, v5 offset:192
	ds_read_b128 v[4:7], v2 offset:32
	v_or_b32_e32 v8, s58, v1
	v_mad_u64_u32 v[8:9], s[4:5], v8, s71, v[0:1]
	s_mov_b32 s1, 0x100000
	s_waitcnt lgkmcnt(0)
	v_mul_f32_e32 v9, v68, v4
	v_bfe_u32 v10, v9, 16, 1
	v_add3_u32 v9, v9, v10, s96
	ds_write_b16_d16_hi v8, v9
	v_mul_f32_e32 v9, v52, v4
	v_bfe_u32 v10, v9, 16, 1
	v_add3_u32 v9, v9, v10, s96
	ds_write_b16_d16_hi v8, v9 offset:64
	v_mul_f32_e32 v9, v36, v4
	v_bfe_u32 v10, v9, 16, 1
	v_add3_u32 v9, v9, v10, s96
	v_mul_f32_e32 v4, v20, v4
	ds_write_b16_d16_hi v8, v9 offset:128
	v_bfe_u32 v9, v4, 16, 1
	v_add3_u32 v4, v4, v9, s96
	ds_write_b16_d16_hi v8, v4 offset:192
	v_or_b32_e32 v4, s59, v1
	v_mad_u64_u32 v[8:9], s[4:5], v4, s71, v[0:1]
	v_mul_f32_e32 v4, v69, v5
	v_bfe_u32 v9, v4, 16, 1
	v_add3_u32 v4, v4, v9, s96
	ds_write_b16_d16_hi v8, v4
	v_mul_f32_e32 v4, v53, v5
	v_bfe_u32 v9, v4, 16, 1
	v_add3_u32 v4, v4, v9, s96
	ds_write_b16_d16_hi v8, v4 offset:64
	v_mul_f32_e32 v4, v37, v5
	v_bfe_u32 v9, v4, 16, 1
	v_add3_u32 v4, v4, v9, s96
	ds_write_b16_d16_hi v8, v4 offset:128
	v_mul_f32_e32 v4, v21, v5
	v_bfe_u32 v5, v4, 16, 1
	v_add3_u32 v4, v4, v5, s96
	ds_write_b16_d16_hi v8, v4 offset:192
	v_or_b32_e32 v4, s60, v1
	v_mad_u64_u32 v[4:5], s[4:5], v4, s71, v[0:1]
	v_mul_f32_e32 v5, v70, v6
	v_bfe_u32 v8, v5, 16, 1
	v_add3_u32 v5, v5, v8, s96
	ds_write_b16_d16_hi v4, v5
	v_mul_f32_e32 v5, v54, v6
	v_bfe_u32 v8, v5, 16, 1
	v_add3_u32 v5, v5, v8, s96
	ds_write_b16_d16_hi v4, v5 offset:64
	v_mul_f32_e32 v5, v38, v6
	v_bfe_u32 v8, v5, 16, 1
	v_add3_u32 v5, v5, v8, s96
	ds_write_b16_d16_hi v4, v5 offset:128
	v_mul_f32_e32 v5, v22, v6
	v_bfe_u32 v6, v5, 16, 1
	v_add3_u32 v5, v5, v6, s96
	ds_write_b16_d16_hi v4, v5 offset:192
	v_or_b32_e32 v4, s61, v1
	v_mad_u64_u32 v[4:5], s[4:5], v4, s71, v[0:1]
	v_mul_f32_e32 v5, v71, v7
	v_bfe_u32 v6, v5, 16, 1
	v_add3_u32 v5, v5, v6, s96
	ds_write_b16_d16_hi v4, v5
	v_mul_f32_e32 v5, v55, v7
	v_bfe_u32 v6, v5, 16, 1
	v_add3_u32 v5, v5, v6, s96
	ds_write_b16_d16_hi v4, v5 offset:64
	v_mul_f32_e32 v5, v39, v7
	v_bfe_u32 v6, v5, 16, 1
	v_add3_u32 v5, v5, v6, s96
	ds_write_b16_d16_hi v4, v5 offset:128
	v_mul_f32_e32 v5, v23, v7
	v_bfe_u32 v6, v5, 16, 1
	v_add3_u32 v5, v5, v6, s96
	ds_write_b16_d16_hi v4, v5 offset:192
	ds_read_b128 v[4:7], v2 offset:64
	v_or_b32_e32 v8, s62, v1
	v_mad_u64_u32 v[8:9], s[4:5], v8, s71, v[0:1]
	v_lshlrev_b32_e32 v23, 16, v136
	s_waitcnt lgkmcnt(0)
	v_mul_f32_e32 v9, v72, v4
	v_bfe_u32 v10, v9, 16, 1
	v_add3_u32 v9, v9, v10, s96
	ds_write_b16_d16_hi v8, v9
	v_mul_f32_e32 v9, v56, v4
	v_bfe_u32 v10, v9, 16, 1
	v_add3_u32 v9, v9, v10, s96
	ds_write_b16_d16_hi v8, v9 offset:64
	v_mul_f32_e32 v9, v40, v4
	v_bfe_u32 v10, v9, 16, 1
	v_add3_u32 v9, v9, v10, s96
	v_mul_f32_e32 v4, v24, v4
	ds_write_b16_d16_hi v8, v9 offset:128
	v_bfe_u32 v9, v4, 16, 1
	v_add3_u32 v4, v4, v9, s96
	ds_write_b16_d16_hi v8, v4 offset:192
	v_or_b32_e32 v4, s63, v1
	v_mad_u64_u32 v[8:9], s[4:5], v4, s71, v[0:1]
	v_mul_f32_e32 v4, v73, v5
	v_bfe_u32 v9, v4, 16, 1
	v_add3_u32 v4, v4, v9, s96
	ds_write_b16_d16_hi v8, v4
	v_mul_f32_e32 v4, v57, v5
	v_bfe_u32 v9, v4, 16, 1
	v_add3_u32 v4, v4, v9, s96
	ds_write_b16_d16_hi v8, v4 offset:64
	v_mul_f32_e32 v4, v41, v5
	v_bfe_u32 v9, v4, 16, 1
	v_add3_u32 v4, v4, v9, s96
	ds_write_b16_d16_hi v8, v4 offset:128
	v_mul_f32_e32 v4, v25, v5
	v_bfe_u32 v5, v4, 16, 1
	v_add3_u32 v4, v4, v5, s96
	ds_write_b16_d16_hi v8, v4 offset:192
	v_or_b32_e32 v4, s64, v1
	v_mad_u64_u32 v[4:5], s[4:5], v4, s71, v[0:1]
	v_mul_f32_e32 v5, v74, v6
	v_bfe_u32 v8, v5, 16, 1
	v_add3_u32 v5, v5, v8, s96
	ds_write_b16_d16_hi v4, v5
	v_mul_f32_e32 v5, v58, v6
	v_bfe_u32 v8, v5, 16, 1
	v_add3_u32 v5, v5, v8, s96
	ds_write_b16_d16_hi v4, v5 offset:64
	v_mul_f32_e32 v5, v42, v6
	v_bfe_u32 v8, v5, 16, 1
	v_add3_u32 v5, v5, v8, s96
	ds_write_b16_d16_hi v4, v5 offset:128
	v_mul_f32_e32 v5, v26, v6
	v_bfe_u32 v6, v5, 16, 1
	v_add3_u32 v5, v5, v6, s96
	ds_write_b16_d16_hi v4, v5 offset:192
	v_or_b32_e32 v4, s65, v1
	v_mad_u64_u32 v[4:5], s[4:5], v4, s71, v[0:1]
	v_mul_f32_e32 v5, v75, v7
	v_bfe_u32 v6, v5, 16, 1
	v_add3_u32 v5, v5, v6, s96
	ds_write_b16_d16_hi v4, v5
	v_mul_f32_e32 v5, v59, v7
	v_bfe_u32 v6, v5, 16, 1
	v_add3_u32 v5, v5, v6, s96
	ds_write_b16_d16_hi v4, v5 offset:64
	v_mul_f32_e32 v5, v43, v7
	v_bfe_u32 v6, v5, 16, 1
	v_add3_u32 v5, v5, v6, s96
	ds_write_b16_d16_hi v4, v5 offset:128
	v_mul_f32_e32 v5, v27, v7
	v_bfe_u32 v6, v5, 16, 1
	v_add3_u32 v5, v5, v6, s96
	ds_write_b16_d16_hi v4, v5 offset:192
	ds_read_b128 v[4:7], v2 offset:96
	v_or_b32_e32 v2, s66, v1
	v_mad_u64_u32 v[8:9], s[4:5], v2, s71, v[0:1]
	v_lshlrev_b32_e32 v22, 16, v140
	s_waitcnt lgkmcnt(0)
	v_mul_f32_e32 v2, v76, v4
	v_bfe_u32 v9, v2, 16, 1
	v_add3_u32 v2, v2, v9, s96
	ds_write_b16_d16_hi v8, v2
	v_mul_f32_e32 v2, v60, v4
	v_bfe_u32 v9, v2, 16, 1
	v_add3_u32 v2, v2, v9, s96
	ds_write_b16_d16_hi v8, v2 offset:64
	v_mul_f32_e32 v2, v44, v4
	v_bfe_u32 v9, v2, 16, 1
	v_add3_u32 v2, v2, v9, s96
	ds_write_b16_d16_hi v8, v2 offset:128
	v_mul_f32_e32 v2, v28, v4
	v_bfe_u32 v4, v2, 16, 1
	v_add3_u32 v2, v2, v4, s96
	ds_write_b16_d16_hi v8, v2 offset:192
	v_or_b32_e32 v2, s67, v1
	v_mad_u64_u32 v[8:9], s[4:5], v2, s71, v[0:1]
	v_mul_f32_e32 v2, v77, v5
	v_bfe_u32 v4, v2, 16, 1
	v_add3_u32 v2, v2, v4, s96
	ds_write_b16_d16_hi v8, v2
	v_mul_f32_e32 v2, v61, v5
	v_bfe_u32 v4, v2, 16, 1
	v_add3_u32 v2, v2, v4, s96
	ds_write_b16_d16_hi v8, v2 offset:64
	v_mul_f32_e32 v2, v45, v5
	v_bfe_u32 v4, v2, 16, 1
	v_add3_u32 v2, v2, v4, s96
	ds_write_b16_d16_hi v8, v2 offset:128
	v_mul_f32_e32 v2, v29, v5
	v_bfe_u32 v4, v2, 16, 1
	v_add3_u32 v2, v2, v4, s96
	ds_write_b16_d16_hi v8, v2 offset:192
	v_or_b32_e32 v2, s68, v1
	v_mad_u64_u32 v[4:5], s[4:5], v2, s71, v[0:1]
	v_mul_f32_e32 v2, v78, v6
	v_bfe_u32 v5, v2, 16, 1
	v_add3_u32 v2, v2, v5, s96
	ds_write_b16_d16_hi v4, v2
	v_mul_f32_e32 v2, v62, v6
	v_bfe_u32 v5, v2, 16, 1
	v_add3_u32 v2, v2, v5, s96
	ds_write_b16_d16_hi v4, v2 offset:64
	v_mul_f32_e32 v2, v46, v6
	v_bfe_u32 v5, v2, 16, 1
	v_add3_u32 v2, v2, v5, s96
	ds_write_b16_d16_hi v4, v2 offset:128
	v_mul_f32_e32 v2, v30, v6
	v_or_b32_e32 v1, s69, v1
	v_bfe_u32 v5, v2, 16, 1
	v_mad_u64_u32 v[0:1], s[4:5], v1, s71, v[0:1]
	v_add3_u32 v2, v2, v5, s96
	v_mul_f32_e32 v1, v79, v7
	ds_write_b16_d16_hi v4, v2 offset:192
	v_bfe_u32 v2, v1, 16, 1
	v_add3_u32 v1, v1, v2, s96
	ds_write_b16_d16_hi v0, v1
	v_mul_f32_e32 v1, v63, v7
	v_bfe_u32 v2, v1, 16, 1
	v_add3_u32 v1, v1, v2, s96
	ds_write_b16_d16_hi v0, v1 offset:64
	v_mul_f32_e32 v1, v47, v7
	v_bfe_u32 v2, v1, 16, 1
	v_add3_u32 v1, v1, v2, s96
	ds_write_b16_d16_hi v0, v1 offset:128
	v_mul_f32_e32 v1, v31, v7
	v_bfe_u32 v2, v1, 16, 1
	v_add3_u32 v1, v1, v2, s96
	v_readlane_b32 s4, v254, 28
	ds_write_b16_d16_hi v0, v1 offset:192
	v_lshlrev_b64 v[0:1], 8, v[152:153]
	v_readlane_b32 s5, v254, 29
	s_waitcnt lgkmcnt(0)
	ds_read_b64 v[150:151], v167
	s_mov_b64 s[12:13], -1
	v_lshl_add_u64 v[0:1], s[4:5], 0, v[0:1]
	v_lshl_add_u64 v[4:5], v[144:145], 2, v[0:1]
	v_add_co_u32_e32 v14, vcc, s1, v4
	global_load_dwordx4 v[6:9], v[4:5], off offset:16
	global_load_dwordx4 v[10:13], v[4:5], off
	s_mov_b64 s[4:5], 0x100000
	v_addc_co_u32_e32 v15, vcc, 0, v5, vcc
	v_lshl_add_u64 v[0:1], v[4:5], 0, s[4:5]
	global_load_dwordx4 v[14:17], v[14:15], off
	s_nop 0
	global_load_dwordx4 v[18:21], v[0:1], off offset:16
	s_waitcnt lgkmcnt(0)
	v_and_b32_e32 v155, 1, v150
	s_and_b64 vcc, exec, s[50:51]
	v_cmp_ne_u32_e64 s[10:11], 0, v155
	s_waitcnt vmcnt(2)
	v_mov_b32_e32 v25, v10
	s_waitcnt vmcnt(1)
	v_mov_b32_e32 v24, v14
	v_mul_f32_e32 v24, v24, v22
	v_mul_f32_e32 v25, v25, v23
	s_nop 0
	v_sub_f32_e32 v2, v25, v24
	v_mov_b32_e32 v24, v10
	v_mov_b32_e32 v25, v14
	v_mul_f32_e32 v22, v24, v22
	v_mul_f32_e32 v23, v25, v23
	v_mov_b32_e32 v10, v15
	v_add_f32_e32 v26, v22, v23
	v_and_b32_e32 v23, 0xffff0000, v136
	v_and_b32_e32 v22, 0xffff0000, v140
	v_mul_f32_e32 v24, v10, v22
	v_mul_f32_e32 v25, v11, v23
	v_mov_b32_e32 v14, v11
	v_sub_f32_e32 v10, v25, v24
	v_cvt_pk_bf16_f32 v100, v2, v10
	v_mul_f32_e32 v10, v14, v22
	v_mul_f32_e32 v11, v15, v23
	v_mov_b32_e32 v14, v16
	v_add_f32_e32 v2, v10, v11
	v_lshlrev_b32_e32 v11, 16, v137
	v_lshlrev_b32_e32 v10, 16, v141
	v_mov_b32_e32 v15, v12
	v_mul_f32_e32 v14, v14, v10
	v_mul_f32_e32 v15, v15, v11
	v_cvt_pk_bf16_f32 v104, v26, v2
	v_lshlrev_b32_e32 v23, 16, v112
	v_sub_f32_e32 v2, v15, v14
	v_mov_b32_e32 v14, v12
	v_mov_b32_e32 v15, v16
	v_mul_f32_e32 v10, v14, v10
	v_mul_f32_e32 v11, v15, v11
	v_mov_b32_e32 v12, v17
	v_add_f32_e32 v22, v10, v11
	v_and_b32_e32 v11, 0xffff0000, v137
	v_and_b32_e32 v10, 0xffff0000, v141
	v_mul_f32_e32 v14, v12, v10
	v_mul_f32_e32 v15, v13, v11
	v_mov_b32_e32 v16, v13
	v_sub_f32_e32 v12, v15, v14
	v_mul_f32_e32 v10, v16, v10
	v_mul_f32_e32 v11, v17, v11
	v_cvt_pk_bf16_f32 v101, v2, v12
	s_waitcnt vmcnt(0)
	v_mov_b32_e32 v12, v18
	v_add_f32_e32 v2, v10, v11
	v_lshlrev_b32_e32 v11, 16, v138
	v_lshlrev_b32_e32 v10, 16, v142
	v_mov_b32_e32 v13, v6
	v_mul_f32_e32 v12, v12, v10
	v_mul_f32_e32 v13, v13, v11
	v_cvt_pk_bf16_f32 v105, v22, v2
	v_lshlrev_b32_e32 v22, 16, v132
	v_sub_f32_e32 v2, v13, v12
	v_mov_b32_e32 v12, v6
	v_mov_b32_e32 v13, v18
	v_mul_f32_e32 v10, v12, v10
	v_mul_f32_e32 v11, v13, v11
	v_mov_b32_e32 v6, v19
	v_add_f32_e32 v14, v10, v11
	v_and_b32_e32 v11, 0xffff0000, v138
	v_and_b32_e32 v10, 0xffff0000, v142
	v_mul_f32_e32 v12, v6, v10
	v_mul_f32_e32 v13, v7, v11
	v_mov_b32_e32 v18, v7
	v_sub_f32_e32 v6, v13, v12
	v_cvt_pk_bf16_f32 v102, v2, v6
	v_mul_f32_e32 v6, v18, v10
	v_mul_f32_e32 v7, v19, v11
	v_mov_b32_e32 v10, v20
	v_add_f32_e32 v2, v6, v7
	v_lshlrev_b32_e32 v7, 16, v139
	v_lshlrev_b32_e32 v6, 16, v143
	v_mov_b32_e32 v11, v8
	v_mul_f32_e32 v10, v10, v6
	v_mul_f32_e32 v11, v11, v7
	v_cvt_pk_bf16_f32 v106, v14, v2
	s_nop 0
	v_sub_f32_e32 v2, v11, v10
	v_mov_b32_e32 v10, v8
	v_mov_b32_e32 v11, v20
	v_mul_f32_e32 v6, v10, v6
	v_mul_f32_e32 v7, v11, v7
	v_mov_b32_e32 v8, v21
	v_add_f32_e32 v12, v6, v7
	v_and_b32_e32 v7, 0xffff0000, v139
	v_and_b32_e32 v6, 0xffff0000, v143
	v_mul_f32_e32 v10, v8, v6
	v_mul_f32_e32 v11, v9, v7
	v_mov_b32_e32 v20, v9
	v_sub_f32_e32 v8, v11, v10
	v_mul_f32_e32 v6, v20, v6
	v_mul_f32_e32 v7, v21, v7
	v_cvt_pk_bf16_f32 v103, v2, v8
	s_nop 0
	v_add_f32_e32 v2, v6, v7
	v_cvt_pk_bf16_f32 v107, v12, v2
	global_load_dwordx4 v[6:9], v[4:5], off offset:80
	global_load_dwordx4 v[10:13], v[4:5], off offset:64
	global_load_dwordx4 v[14:17], v[0:1], off offset:80
	global_load_dwordx4 v[18:21], v[0:1], off offset:64
	s_waitcnt vmcnt(2)
	v_mov_b32_e32 v25, v10
	s_waitcnt vmcnt(0)
	v_mov_b32_e32 v24, v18
	v_mul_f32_e32 v24, v24, v22
	v_mul_f32_e32 v25, v25, v23
	s_nop 0
	v_sub_f32_e32 v2, v25, v24
	v_mov_b32_e32 v24, v10
	v_mov_b32_e32 v25, v18
	v_mul_f32_e32 v22, v24, v22
	v_mul_f32_e32 v23, v25, v23
	v_mov_b32_e32 v10, v19
	v_add_f32_e32 v26, v22, v23
	v_and_b32_e32 v23, 0xffff0000, v112
	v_and_b32_e32 v22, 0xffff0000, v132
	v_mul_f32_e32 v24, v10, v22
	v_mul_f32_e32 v25, v11, v23
	v_mov_b32_e32 v18, v11
	v_sub_f32_e32 v10, v25, v24
	v_cvt_pk_bf16_f32 v108, v2, v10
	v_mul_f32_e32 v10, v18, v22
	v_mul_f32_e32 v11, v19, v23
	v_mov_b32_e32 v18, v20
	v_add_f32_e32 v2, v10, v11
	v_lshlrev_b32_e32 v11, 16, v113
	v_lshlrev_b32_e32 v10, 16, v133
	v_mov_b32_e32 v19, v12
	v_mul_f32_e32 v18, v18, v10
	v_mul_f32_e32 v19, v19, v11
	v_cvt_pk_bf16_f32 v112, v26, v2
	v_lshlrev_b32_e32 v23, 16, v116
	v_sub_f32_e32 v2, v19, v18
	v_mov_b32_e32 v18, v12
	v_mov_b32_e32 v19, v20
	v_mul_f32_e32 v10, v18, v10
	v_mul_f32_e32 v11, v19, v11
	v_mov_b32_e32 v12, v21
	v_add_f32_e32 v22, v10, v11
	v_and_b32_e32 v11, 0xffff0000, v113
	v_and_b32_e32 v10, 0xffff0000, v133
	v_mul_f32_e32 v18, v12, v10
	v_mul_f32_e32 v19, v13, v11
	v_mov_b32_e32 v20, v13
	v_sub_f32_e32 v12, v19, v18
	v_mul_f32_e32 v10, v20, v10
	v_mul_f32_e32 v11, v21, v11
	v_cvt_pk_bf16_f32 v109, v2, v12
	v_mov_b32_e32 v12, v14
	v_add_f32_e32 v2, v10, v11
	v_lshlrev_b32_e32 v11, 16, v114
	v_lshlrev_b32_e32 v10, 16, v134
	v_mov_b32_e32 v13, v6
	v_mul_f32_e32 v12, v12, v10
	v_mul_f32_e32 v13, v13, v11
	v_cvt_pk_bf16_f32 v113, v22, v2
	v_lshlrev_b32_e32 v22, 16, v120
	v_sub_f32_e32 v2, v13, v12
	v_mov_b32_e32 v12, v6
	v_mov_b32_e32 v13, v14
	v_mul_f32_e32 v10, v12, v10
	v_mul_f32_e32 v11, v13, v11
	v_mov_b32_e32 v6, v15
	v_add_f32_e32 v18, v10, v11
	v_and_b32_e32 v11, 0xffff0000, v114
	v_and_b32_e32 v10, 0xffff0000, v134
	v_mul_f32_e32 v12, v6, v10
	v_mul_f32_e32 v13, v7, v11
	v_mov_b32_e32 v14, v7
	v_sub_f32_e32 v6, v13, v12
	v_cvt_pk_bf16_f32 v110, v2, v6
	v_mul_f32_e32 v6, v14, v10
	v_mul_f32_e32 v7, v15, v11
	v_mov_b32_e32 v10, v16
	v_add_f32_e32 v2, v6, v7
	v_lshlrev_b32_e32 v7, 16, v115
	v_lshlrev_b32_e32 v6, 16, v135
	v_mov_b32_e32 v11, v8
	v_mul_f32_e32 v10, v10, v6
	v_mul_f32_e32 v11, v11, v7
	v_cvt_pk_bf16_f32 v114, v18, v2
	s_nop 0
	v_sub_f32_e32 v2, v11, v10
	v_mov_b32_e32 v10, v8
	v_mov_b32_e32 v11, v16
	v_mul_f32_e32 v6, v10, v6
	v_mul_f32_e32 v7, v11, v7
	v_mov_b32_e32 v8, v17
	v_add_f32_e32 v12, v6, v7
	v_and_b32_e32 v7, 0xffff0000, v115
	v_and_b32_e32 v6, 0xffff0000, v135
	v_mul_f32_e32 v10, v8, v6
	v_mul_f32_e32 v11, v9, v7
	v_mov_b32_e32 v16, v9
	v_sub_f32_e32 v8, v11, v10
	v_mul_f32_e32 v6, v16, v6
	v_mul_f32_e32 v7, v17, v7
	v_cvt_pk_bf16_f32 v111, v2, v8
	s_nop 0
	v_add_f32_e32 v2, v6, v7
	v_cvt_pk_bf16_f32 v115, v12, v2
	global_load_dwordx4 v[6:9], v[4:5], off offset:144
	global_load_dwordx4 v[10:13], v[4:5], off offset:128
	global_load_dwordx4 v[14:17], v[0:1], off offset:144
	global_load_dwordx4 v[18:21], v[0:1], off offset:128
	s_waitcnt vmcnt(2)
	v_mov_b32_e32 v25, v10
	s_waitcnt vmcnt(0)
	v_mov_b32_e32 v24, v18
	v_mul_f32_e32 v24, v24, v22
	v_mul_f32_e32 v25, v25, v23
	s_nop 0
	v_sub_f32_e32 v2, v25, v24
	v_mov_b32_e32 v24, v10
	v_mov_b32_e32 v25, v18
	v_mul_f32_e32 v22, v24, v22
	v_mul_f32_e32 v23, v25, v23
	v_mov_b32_e32 v10, v19
	v_add_f32_e32 v26, v22, v23
	v_and_b32_e32 v23, 0xffff0000, v116
	v_and_b32_e32 v22, 0xffff0000, v120
	v_mul_f32_e32 v24, v10, v22
	v_mul_f32_e32 v25, v11, v23
	v_mov_b32_e32 v18, v11
	v_sub_f32_e32 v10, v25, v24
	v_cvt_pk_bf16_f32 v116, v2, v10
	v_mul_f32_e32 v10, v18, v22
	v_mul_f32_e32 v11, v19, v23
	v_mov_b32_e32 v18, v20
	v_add_f32_e32 v2, v10, v11
	v_lshlrev_b32_e32 v11, 16, v117
	v_lshlrev_b32_e32 v10, 16, v121
	v_mov_b32_e32 v19, v12
	v_mul_f32_e32 v18, v18, v10
	v_mul_f32_e32 v19, v19, v11
	v_cvt_pk_bf16_f32 v120, v26, v2
	s_nop 0
	v_sub_f32_e32 v2, v19, v18
	v_mov_b32_e32 v18, v12
	v_mov_b32_e32 v19, v20
	v_mul_f32_e32 v10, v18, v10
	v_mul_f32_e32 v11, v19, v11
	v_mov_b32_e32 v12, v21
	v_add_f32_e32 v22, v10, v11
	v_and_b32_e32 v11, 0xffff0000, v117
	v_and_b32_e32 v10, 0xffff0000, v121
	v_mul_f32_e32 v18, v12, v10
	v_mul_f32_e32 v19, v13, v11
	v_mov_b32_e32 v20, v13
	v_sub_f32_e32 v12, v19, v18
	v_mul_f32_e32 v10, v20, v10
	v_mul_f32_e32 v11, v21, v11
	v_cvt_pk_bf16_f32 v117, v2, v12
	v_mov_b32_e32 v12, v14
	v_add_f32_e32 v2, v10, v11
	v_lshlrev_b32_e32 v11, 16, v118
	v_lshlrev_b32_e32 v10, 16, v122
	v_mov_b32_e32 v13, v6
	v_mul_f32_e32 v12, v12, v10
	v_mul_f32_e32 v13, v13, v11
	v_cvt_pk_bf16_f32 v121, v22, v2
	s_nop 0
	v_sub_f32_e32 v2, v13, v12
	v_mov_b32_e32 v12, v6
	v_mov_b32_e32 v13, v14
	v_mul_f32_e32 v10, v12, v10
	v_mul_f32_e32 v11, v13, v11
	v_mov_b32_e32 v6, v15
	v_add_f32_e32 v18, v10, v11
	v_and_b32_e32 v11, 0xffff0000, v118
	v_and_b32_e32 v10, 0xffff0000, v122
	v_mul_f32_e32 v12, v6, v10
	v_mul_f32_e32 v13, v7, v11
	v_mov_b32_e32 v14, v7
	v_sub_f32_e32 v6, v13, v12
	v_cvt_pk_bf16_f32 v118, v2, v6
	v_mul_f32_e32 v6, v14, v10
	v_mul_f32_e32 v7, v15, v11
	v_mov_b32_e32 v10, v16
	v_add_f32_e32 v2, v6, v7
	v_lshlrev_b32_e32 v7, 16, v119
	v_lshlrev_b32_e32 v6, 16, v123
	v_mov_b32_e32 v11, v8
	v_mul_f32_e32 v10, v10, v6
	v_mul_f32_e32 v11, v11, v7
	v_cvt_pk_bf16_f32 v122, v18, v2
	s_nop 0
	v_sub_f32_e32 v2, v11, v10
	v_mov_b32_e32 v10, v8
	v_mov_b32_e32 v11, v16
	v_mul_f32_e32 v6, v10, v6
	v_mul_f32_e32 v7, v11, v7
	v_mov_b32_e32 v8, v17
	v_add_f32_e32 v12, v6, v7
	v_and_b32_e32 v7, 0xffff0000, v119
	v_and_b32_e32 v6, 0xffff0000, v123
	v_mul_f32_e32 v10, v8, v6
	v_mul_f32_e32 v11, v9, v7
	v_mov_b32_e32 v16, v9
	v_sub_f32_e32 v8, v11, v10
	v_mul_f32_e32 v6, v16, v6
	v_mul_f32_e32 v7, v17, v7
	v_cvt_pk_bf16_f32 v119, v2, v8
	s_nop 0
	v_add_f32_e32 v2, v6, v7
	v_cvt_pk_bf16_f32 v123, v12, v2
	global_load_dwordx4 v[6:9], v[4:5], off offset:208
	global_load_dwordx4 v[10:13], v[4:5], off offset:192
	global_load_dwordx4 v[14:17], v[0:1], off offset:208
	global_load_dwordx4 v[18:21], v[0:1], off offset:192
	v_lshlrev_b32_e32 v1, 16, v124
	v_lshlrev_b32_e32 v0, 16, v128
	s_waitcnt vmcnt(2)
	v_mov_b32_e32 v5, v10
	s_waitcnt vmcnt(0)
	v_mov_b32_e32 v4, v18
	v_mul_f32_e32 v4, v4, v0
	v_mul_f32_e32 v5, v5, v1
	s_nop 0
	v_sub_f32_e32 v2, v5, v4
	v_mov_b32_e32 v4, v10
	v_mov_b32_e32 v5, v18
	v_mul_f32_e32 v0, v4, v0
	v_mul_f32_e32 v1, v5, v1
	v_mov_b32_e32 v10, v19
	v_add_f32_e32 v22, v0, v1
	v_and_b32_e32 v1, 0xffff0000, v124
	v_and_b32_e32 v0, 0xffff0000, v128
	v_mov_b32_e32 v18, v11
	v_mul_f32_e32 v4, v10, v0
	v_mul_f32_e32 v5, v11, v1
	v_mul_f32_e32 v0, v18, v0
	v_mul_f32_e32 v1, v19, v1
	v_sub_f32_e32 v4, v5, v4
	v_add_f32_e32 v0, v0, v1
	v_cvt_pk_bf16_f32 v124, v2, v4
	v_cvt_pk_bf16_f32 v128, v22, v0
	v_lshlrev_b32_e32 v1, 16, v125
	v_lshlrev_b32_e32 v0, 16, v129
	v_mov_b32_e32 v4, v20
	v_mov_b32_e32 v5, v12
	v_mul_f32_e32 v4, v4, v0
	v_mul_f32_e32 v5, v5, v1
	s_nop 0
	v_sub_f32_e32 v2, v5, v4
	v_mov_b32_e32 v4, v12
	v_mov_b32_e32 v5, v20
	v_mul_f32_e32 v0, v4, v0
	v_mul_f32_e32 v1, v5, v1
	v_mov_b32_e32 v12, v21
	v_add_f32_e32 v10, v0, v1
	v_and_b32_e32 v1, 0xffff0000, v125
	v_and_b32_e32 v0, 0xffff0000, v129
	v_mov_b32_e32 v20, v13
	v_mul_f32_e32 v4, v12, v0
	v_mul_f32_e32 v5, v13, v1
	v_mul_f32_e32 v0, v20, v0
	v_mul_f32_e32 v1, v21, v1
	v_sub_f32_e32 v4, v5, v4
	v_add_f32_e32 v0, v0, v1
	v_cvt_pk_bf16_f32 v125, v2, v4
	v_cvt_pk_bf16_f32 v129, v10, v0
	v_lshlrev_b32_e32 v1, 16, v126
	v_lshlrev_b32_e32 v0, 16, v130
	v_mov_b32_e32 v4, v14
	v_mov_b32_e32 v5, v6
	v_mul_f32_e32 v4, v4, v0
	v_mul_f32_e32 v5, v5, v1
	s_nop 0
	v_sub_f32_e32 v2, v5, v4
	v_mov_b32_e32 v4, v6
	v_mov_b32_e32 v5, v14
	v_mul_f32_e32 v0, v4, v0
	v_mul_f32_e32 v1, v5, v1
	v_mov_b32_e32 v6, v15
	v_add_f32_e32 v10, v0, v1
	v_and_b32_e32 v1, 0xffff0000, v126
	v_and_b32_e32 v0, 0xffff0000, v130
	v_mov_b32_e32 v14, v7
	v_mul_f32_e32 v4, v6, v0
	v_mul_f32_e32 v5, v7, v1
	v_mul_f32_e32 v0, v14, v0
	v_mul_f32_e32 v1, v15, v1
	v_sub_f32_e32 v4, v5, v4
	v_add_f32_e32 v0, v0, v1
	v_cvt_pk_bf16_f32 v126, v2, v4
	v_cvt_pk_bf16_f32 v130, v10, v0
	v_lshlrev_b32_e32 v1, 16, v127
	v_lshlrev_b32_e32 v0, 16, v131
	v_mov_b32_e32 v4, v16
	v_mov_b32_e32 v5, v8
	v_mul_f32_e32 v4, v4, v0
	v_mul_f32_e32 v5, v5, v1
	s_nop 0
	v_sub_f32_e32 v2, v5, v4
	v_mov_b32_e32 v4, v8
	v_mov_b32_e32 v5, v16
	v_mul_f32_e32 v0, v4, v0
	v_mul_f32_e32 v1, v5, v1
	v_mov_b32_e32 v8, v17
	v_add_f32_e32 v6, v0, v1
	v_and_b32_e32 v1, 0xffff0000, v127
	v_and_b32_e32 v0, 0xffff0000, v131
	v_mov_b32_e32 v16, v9
	v_mul_f32_e32 v4, v8, v0
	v_mul_f32_e32 v5, v9, v1
	v_mul_f32_e32 v0, v16, v0
	v_mul_f32_e32 v1, v17, v1
	v_sub_f32_e32 v4, v5, v4
	v_add_f32_e32 v0, v0, v1
	v_cvt_pk_bf16_f32 v127, v2, v4
	v_cvt_pk_bf16_f32 v131, v6, v0
	v_mbcnt_lo_u32_b32 v0, -1, 0
	v_mbcnt_hi_u32_b32 v0, -1, v0
	s_waitcnt vmcnt(0) lgkmcnt(0)
	s_barrier
	v_lshlrev_b32_e32 v4, 4, v0
	v_lshlrev_b32_e32 v2, 3, v0
	v_and_b32_e32 v5, 0xc0, v4
	v_lshlrev_b32_e32 v6, 1, v0
	v_and_or_b32 v5, v2, 24, v5
	v_and_b32_e32 v7, 32, v6
	v_and_b32_e32 v2, 0x100, v2
	v_or3_b32 v139, v5, v7, v2
	v_add_u32_e32 v2, s40, v4
	v_bfe_u32 v7, v0, 2, 2
	v_lshrrev_b32_e32 v8, 1, v0
	v_and_b32_e32 v5, 15, v0
	v_and_or_b32 v7, v8, 8, v7
	v_ashrrev_i32_e32 v8, 8, v2
	v_bitop3_b32 v9, v8, v5, 7 bitop3:0x6c
	v_lshlrev_b32_e32 v10, 10, v8
	v_lshl_or_b32 v132, v9, 4, v10
	v_and_b32_e32 v9, 0xfffff0, v8
	v_lshrrev_b32_e32 v8, 1, v8
	v_and_b32_e32 v8, 4, v8
	v_or3_b32 v8, v9, v8, v7
	v_and_b32_e32 v4, 48, v4
	v_and_b32_e32 v6, 0xc0, v6
	v_mul_i32_i24_e32 v8, 0x6a00, v8
	v_add_u32_e32 v2, 0x400, v2
	v_or3_b32 v133, v8, v6, v4
	v_ashrrev_i32_e32 v6, 8, v2
	v_bitop3_b32 v5, v6, v5, 7 bitop3:0x6c
	v_lshlrev_b32_e32 v8, 10, v6
	v_lshl_or_b32 v134, v5, 4, v8
	v_and_b32_e32 v5, 0xfffff0, v6
	v_lshrrev_b32_e32 v6, 1, v6
	v_and_b32_e32 v6, 4, v6
	v_lshrrev_b32_e32 v1, 5, v0
	v_or3_b32 v5, v5, v6, v7
	v_lshrrev_b32_e32 v2, 3, v2
	v_and_b32_e32 v141, 31, v0
	v_bfe_u32 v140, v0, 5, 1
	v_and_b32_e32 v2, 0xc0, v2
	v_mul_i32_i24_e32 v5, 0x6a00, v5
	v_xor_b32_e32 v0, v1, v0
	v_lshlrev_b32_e32 v1, 4, v141
	v_or3_b32 v135, v5, v2, v4
	v_add_u32_e32 v136, 0, v139
	v_lshlrev_b32_e32 v142, 8, v141
	v_lshlrev_b32_e32 v137, 2, v140
	v_lshlrev_b32_e32 v170, 4, v0
	v_and_b32_e32 v143, 0x60, v1
	v_bitop3_b32 v152, v1, 32, v166 bitop3:0x6c
	v_bitop3_b32 v153, v1, 64, v166 bitop3:0x6c
	v_bitop3_b32 v154, v1, s70, v1 bitop3:0xc
	s_cbranch_vccz .LBB0_1808
	s_waitcnt vmcnt(0) lgkmcnt(0)
	s_barrier
	v_and_b32_e32 v0, 16, v170
	v_add3_u32 v0, 0, v142, v0
	s_cmp_lg_u64 s[10:11], 0
	s_cselect_b64 s[12:13], -1, 0
	v_add_u32_e32 v171, v0, v143
	v_add_u32_e32 v172, v0, v152
	v_add_u32_e32 v173, v0, v153
	v_add_u32_e32 v174, v0, v154
	s_mov_b64 vcc, s[10:11]
	s_cbranch_vccz .LBB0_1714
	ds_read_b128 v[4:7], v171 offset:32768
	ds_read_b128 v[36:39], v172 offset:32768
	v_cndmask_b32_e64 v0, 64, v163, s[8:9]
	v_cndmask_b32_e64 v0, 0, v0, s[10:11]
	v_cmp_lt_u32_e32 vcc, 63, v0
	s_cmp_eq_u64 vcc, exec
	s_waitcnt lgkmcnt(1)
	v_mfma_f32_32x32x16_bf16 v[20:35], v[4:7], v[100:103], 0
	ds_read_b128 v[4:7], v171 offset:40960
	s_waitcnt lgkmcnt(1)
	v_mfma_f32_32x32x16_bf16 v[20:35], v[36:39], v[108:111], v[20:35]
	ds_read_b128 v[36:39], v172 offset:40960
	s_waitcnt lgkmcnt(1)
	v_mfma_f32_32x32x16_bf16 v[4:19], v[4:7], v[100:103], 0
	s_waitcnt lgkmcnt(0)
	v_mfma_f32_32x32x16_bf16 v[4:19], v[36:39], v[108:111], v[4:19]
	ds_read_b128 v[36:39], v173 offset:32768
	s_waitcnt lgkmcnt(0)
	v_mfma_f32_32x32x16_bf16 v[20:35], v[36:39], v[116:119], v[20:35]
	ds_read_b128 v[36:39], v173 offset:40960
	s_waitcnt lgkmcnt(0)
	v_mfma_f32_32x32x16_bf16 v[4:19], v[36:39], v[116:119], v[4:19]
	ds_read_b128 v[36:39], v174 offset:32768
	s_waitcnt lgkmcnt(0)
	v_mfma_f32_32x32x16_bf16 v[20:35], v[36:39], v[124:127], v[20:35]
	ds_read_b128 v[36:39], v174 offset:40960
	s_waitcnt lgkmcnt(0)
	v_mfma_f32_32x32x16_bf16 v[4:19], v[36:39], v[124:127], v[4:19]
	ds_read_b128 v[36:39], v171 offset:32896
	s_waitcnt lgkmcnt(0)
	v_mfma_f32_32x32x16_bf16 v[20:35], v[36:39], v[104:107], v[20:35]
	ds_read_b128 v[36:39], v171 offset:41088
	s_waitcnt lgkmcnt(0)
	v_mfma_f32_32x32x16_bf16 v[4:19], v[36:39], v[104:107], v[4:19]
	ds_read_b128 v[36:39], v172 offset:32896
	s_waitcnt lgkmcnt(0)
	v_mfma_f32_32x32x16_bf16 v[20:35], v[36:39], v[112:115], v[20:35]
	ds_read_b128 v[36:39], v172 offset:41088
	s_waitcnt lgkmcnt(0)
	v_mfma_f32_32x32x16_bf16 v[4:19], v[36:39], v[112:115], v[4:19]
	ds_read_b128 v[36:39], v173 offset:32896
	s_waitcnt lgkmcnt(0)
	v_mfma_f32_32x32x16_bf16 v[20:35], v[36:39], v[120:123], v[20:35]
	ds_read_b128 v[36:39], v173 offset:41088
	s_waitcnt lgkmcnt(0)
	v_mfma_f32_32x32x16_bf16 v[4:19], v[36:39], v[120:123], v[4:19]
	ds_read_b128 v[36:39], v174 offset:32896
	s_waitcnt lgkmcnt(0)
	v_mfma_f32_32x32x16_bf16 v[20:35], v[36:39], v[128:131], v[20:35]
	ds_read_b128 v[36:39], v174 offset:41088
	s_waitcnt lgkmcnt(0)
	v_mfma_f32_32x32x16_bf16 v[4:19], v[36:39], v[128:131], v[4:19]
	s_cbranch_scc1 .LBB0_1711
	v_sub_u32_e32 v0, v0, v137
	v_cmp_lt_i32_e32 vcc, 0, v0
	s_nop 5
	v_cndmask_b32_e32 v20, v168, v20, vcc
	v_cmp_lt_i32_e32 vcc, 32, v0
	s_nop 1
	v_cndmask_b32_e32 v4, v168, v4, vcc
	v_cmp_lt_i32_e32 vcc, 1, v0
	s_nop 1
	v_cndmask_b32_e32 v21, v168, v21, vcc
	v_cmp_lt_i32_e32 vcc, 33, v0
	s_nop 1
	v_cndmask_b32_e32 v5, v168, v5, vcc
	v_cmp_lt_i32_e32 vcc, 2, v0
	s_nop 1
	v_cndmask_b32_e32 v22, v168, v22, vcc
	v_cmp_lt_i32_e32 vcc, 34, v0
	s_nop 1
	v_cndmask_b32_e32 v6, v168, v6, vcc
	v_cmp_lt_i32_e32 vcc, 3, v0
	s_nop 1
	v_cndmask_b32_e32 v23, v168, v23, vcc
	v_cmp_lt_i32_e32 vcc, 35, v0
	s_nop 1
	v_cndmask_b32_e32 v7, v168, v7, vcc
	v_cmp_lt_i32_e32 vcc, 8, v0
	s_nop 1
	v_cndmask_b32_e32 v24, v168, v24, vcc
	v_cmp_lt_i32_e32 vcc, 40, v0
	s_nop 1
	v_cndmask_b32_e32 v8, v168, v8, vcc
	v_cmp_lt_i32_e32 vcc, 9, v0
	s_nop 1
	v_cndmask_b32_e32 v25, v168, v25, vcc
	v_cmp_lt_i32_e32 vcc, 41, v0
	s_nop 1
	v_cndmask_b32_e32 v9, v168, v9, vcc
	v_cmp_lt_i32_e32 vcc, 10, v0
	s_nop 1
	v_cndmask_b32_e32 v26, v168, v26, vcc
	v_cmp_lt_i32_e32 vcc, 42, v0
	s_nop 1
	v_cndmask_b32_e32 v10, v168, v10, vcc
	v_cmp_lt_i32_e32 vcc, 11, v0
	s_nop 1
	v_cndmask_b32_e32 v27, v168, v27, vcc
	v_cmp_lt_i32_e32 vcc, 43, v0
	s_nop 1
	v_cndmask_b32_e32 v11, v168, v11, vcc
	v_cmp_lt_i32_e32 vcc, 16, v0
	s_nop 1
	v_cndmask_b32_e32 v28, v168, v28, vcc
	v_cmp_lt_i32_e32 vcc, 48, v0
	s_nop 1
	v_cndmask_b32_e32 v12, v168, v12, vcc
	v_cmp_lt_i32_e32 vcc, 17, v0
	s_nop 1
	v_cndmask_b32_e32 v29, v168, v29, vcc
	v_cmp_lt_i32_e32 vcc, 49, v0
	s_nop 1
	v_cndmask_b32_e32 v13, v168, v13, vcc
	v_cmp_lt_i32_e32 vcc, 18, v0
	s_nop 1
	v_cndmask_b32_e32 v30, v168, v30, vcc
	v_cmp_lt_i32_e32 vcc, 50, v0
	s_nop 1
	v_cndmask_b32_e32 v14, v168, v14, vcc
	v_cmp_lt_i32_e32 vcc, 19, v0
	s_nop 1
	v_cndmask_b32_e32 v31, v168, v31, vcc
	v_cmp_lt_i32_e32 vcc, 51, v0
	s_nop 1
	v_cndmask_b32_e32 v15, v168, v15, vcc
	v_cmp_lt_i32_e32 vcc, 24, v0
	s_nop 1
	v_cndmask_b32_e32 v32, v168, v32, vcc
	v_cmp_lt_i32_e32 vcc, 56, v0
	s_nop 1
	v_cndmask_b32_e32 v16, v168, v16, vcc
	v_cmp_lt_i32_e32 vcc, 25, v0
	s_nop 1
	v_cndmask_b32_e32 v33, v168, v33, vcc
	v_cmp_lt_i32_e32 vcc, 57, v0
	s_nop 1
	v_cndmask_b32_e32 v17, v168, v17, vcc
	v_cmp_lt_i32_e32 vcc, 26, v0
	s_nop 1
	v_cndmask_b32_e32 v34, v168, v34, vcc
	v_cmp_lt_i32_e32 vcc, 58, v0
	s_nop 1
	v_cndmask_b32_e32 v18, v168, v18, vcc
	v_cmp_lt_i32_e32 vcc, 27, v0
	s_nop 1
	v_cndmask_b32_e32 v35, v168, v35, vcc
	v_cmp_lt_i32_e32 vcc, 59, v0
	s_nop 1
	v_cndmask_b32_e32 v19, v168, v19, vcc

.LBB0_1713:
	v_mul_f32_e32 v0, 0xbe0293ee, v175
	v_fma_f32 v84, v4, s2, v0
	v_fma_f32 v85, v5, s2, v0
	v_fma_f32 v4, v24, s2, v0
	v_fma_f32 v5, v25, s2, v0
	v_fma_f32 v20, v20, s2, v0
	v_fma_f32 v21, v21, s2, v0
	v_exp_f32_e32 v72, v4
	v_exp_f32_e32 v73, v5
	v_fma_f32 v4, v26, s2, v0
	v_fma_f32 v5, v27, s2, v0
	v_exp_f32_e32 v68, v20
	v_exp_f32_e32 v74, v4
	v_exp_f32_e32 v75, v5
	v_fma_f32 v4, v28, s2, v0
	v_fma_f32 v5, v29, s2, v0
	v_exp_f32_e32 v69, v21
	v_exp_f32_e32 v76, v4
	v_exp_f32_e32 v77, v5
	v_fma_f32 v4, v30, s2, v0
	v_fma_f32 v5, v31, s2, v0
	v_fma_f32 v20, v22, s2, v0
	v_fma_f32 v21, v23, s2, v0
	v_exp_f32_e32 v78, v4
	v_exp_f32_e32 v79, v5
	v_fma_f32 v4, v32, s2, v0
	v_fma_f32 v5, v33, s2, v0
	v_exp_f32_e32 v70, v20
	v_exp_f32_e32 v80, v4
	v_exp_f32_e32 v81, v5
	v_fma_f32 v4, v34, s2, v0
	v_fma_f32 v5, v35, s2, v0
	v_exp_f32_e32 v71, v21
	v_exp_f32_e32 v82, v4
	v_exp_f32_e32 v83, v5
	v_fma_f32 v86, v6, s2, v0
	v_fma_f32 v87, v7, s2, v0
	v_fma_f32 v88, v8, s2, v0
	v_fma_f32 v89, v9, s2, v0
	v_fma_f32 v90, v10, s2, v0
	v_fma_f32 v91, v11, s2, v0
	v_fma_f32 v92, v12, s2, v0
	v_fma_f32 v93, v13, s2, v0
	v_fma_f32 v94, v14, s2, v0
	v_fma_f32 v95, v15, s2, v0
	v_fma_f32 v96, v16, s2, v0
	v_fma_f32 v97, v17, s2, v0
	v_fma_f32 v98, v18, s2, v0
	v_fma_f32 v99, v19, s2, v0
	s_branch .LBB0_1715

.LBB0_1717:
	v_readlane_b32 s1, v254, 30
	v_cmp_eq_u32_e64 s[10:11], 0, v140
	s_andn2_b64 vcc, exec, s[12:13]
	v_lshl_add_u32 v176, v141, 2, s1
	v_lshlrev_b32_e32 v177, 4, v140
	s_cbranch_vccnz .LBB0_1722
	v_cmp_gt_f32_e32 vcc, 1.0, v178
	s_cbranch_vccz .LBB0_1723
	s_and_saveexec_b64 s[4:5], s[10:11]
	ds_write_b32 v176, v178
	s_or_b64 exec, exec, s[4:5]
	v_readlane_b32 s1, v254, 30
	s_waitcnt lgkmcnt(0)
	s_nop 1
	v_add_u32_e32 v0, s1, v177
	v_readlane_b32 s1, v254, 32
	s_nop 1
	v_add_u32_e32 v1, s1, v177
	v_readlane_b32 s1, v254, 33
	s_nop 1
	v_add_u32_e32 v2, s1, v177
	v_readlane_b32 s1, v254, 31
	ds_read_b128 v[4:7], v1
	ds_read_b128 v[8:11], v2
	v_add_u32_e32 v1, s1, v177
	ds_read_b128 v[20:23], v1
	ds_read_b128 v[24:27], v0
	s_waitcnt lgkmcnt(3)
	v_mul_f32_e32 v14, 0, v6
	v_mul_f32_e32 v15, 0, v7
	s_waitcnt lgkmcnt(2)
	v_mul_f32_e32 v18, 0, v10
	v_mul_f32_e32 v19, 0, v11
	s_waitcnt lgkmcnt(1)
	v_mul_f32_e32 v10, 0, v22
	v_mul_f32_e32 v11, 0, v23
	s_waitcnt lgkmcnt(0)
	v_mul_f32_e32 v6, 0, v26
	v_mul_f32_e32 v7, 0, v27
	v_mul_f32_e32 v16, 0, v8
	v_mul_f32_e32 v17, 0, v9
	v_mul_f32_e32 v12, 0, v4
	v_mul_f32_e32 v13, 0, v5
	v_mul_f32_e32 v8, 0, v20
	v_mul_f32_e32 v9, 0, v21
	v_mul_f32_e32 v4, 0, v24
	v_mul_f32_e32 v5, 0, v25
	s_branch .LBB0_1724

.LBB0_1724:
	v_exp_f32_e32 v84, v84
	v_exp_f32_e32 v85, v85
	v_exp_f32_e32 v86, v86
	v_exp_f32_e32 v87, v87
	v_exp_f32_e32 v88, v88
	v_exp_f32_e32 v89, v89
	v_exp_f32_e32 v90, v90
	v_exp_f32_e32 v91, v91
	v_exp_f32_e32 v92, v92
	v_exp_f32_e32 v93, v93
	v_add_f32_e32 v32, v68, v84
	v_add_f32_e32 v33, v69, v85
	v_exp_f32_e32 v94, v94
	v_exp_f32_e32 v95, v95
	v_add_f32_e32 v30, v70, v86
	v_add_f32_e32 v31, v71, v87
	v_add_f32_e32 v32, 0, v32
	v_add_f32_e32 v33, 0, v33
	v_exp_f32_e32 v96, v96
	v_exp_f32_e32 v97, v97
	v_add_f32_e32 v28, v72, v88
	v_add_f32_e32 v29, v73, v89
	v_add_f32_e32 v30, v30, v32
	v_add_f32_e32 v31, v31, v33
	v_exp_f32_e32 v98, v98
	v_exp_f32_e32 v99, v99
	v_add_f32_e32 v26, v74, v90
	v_add_f32_e32 v27, v75, v91
	v_add_f32_e32 v28, v28, v30
	v_add_f32_e32 v29, v29, v31
	v_cvt_pk_bf16_f32 v180, v68, v69
	v_cvt_pk_bf16_f32 v181, v70, v71
	v_cvt_pk_bf16_f32 v182, v72, v73
	v_cvt_pk_bf16_f32 v183, v74, v75
	v_cvt_pk_bf16_f32 v184, v76, v77
	v_cvt_pk_bf16_f32 v185, v78, v79
	v_cvt_pk_bf16_f32 v186, v80, v81
	v_cvt_pk_bf16_f32 v187, v82, v83
	v_cvt_pk_bf16_f32 v188, v84, v85
	v_cvt_pk_bf16_f32 v189, v86, v87
	v_cvt_pk_bf16_f32 v190, v88, v89
	v_cvt_pk_bf16_f32 v191, v90, v91
	v_cvt_pk_bf16_f32 v192, v92, v93
	v_cvt_pk_bf16_f32 v193, v94, v95
	v_cvt_pk_bf16_f32 v194, v96, v97
	v_cvt_pk_bf16_f32 v195, v98, v99
	ds_read_b64_tr_b16 v[36:37], v136 offset:0
	v_add_f32_e32 v24, v76, v92
	v_add_f32_e32 v25, v77, v93
	v_add_f32_e32 v26, v26, v28
	v_add_f32_e32 v27, v27, v29
	ds_read_b64_tr_b16 v[38:39], v136 offset:0x800
	v_add_f32_e32 v22, v78, v94
	v_add_f32_e32 v23, v79, v95
	v_add_f32_e32 v24, v24, v26
	v_add_f32_e32 v25, v25, v27
	ds_read_b64_tr_b16 v[40:41], v136 offset:0x1000
	v_add_f32_e32 v20, v80, v96
	v_add_f32_e32 v21, v81, v97
	v_add_f32_e32 v22, v22, v24
	v_add_f32_e32 v23, v23, v25
	ds_read_b64_tr_b16 v[42:43], v136 offset:0x1800
	v_add_f32_e32 v0, v82, v98
	v_add_f32_e32 v1, v83, v99
	v_add_f32_e32 v20, v20, v22
	v_add_f32_e32 v21, v21, v23
	ds_read_b64_tr_b16 v[44:45], v136 offset:0x2000
	ds_read_b64_tr_b16 v[46:47], v136 offset:0x2800
	ds_read_b64_tr_b16 v[48:49], v136 offset:0x3000
	ds_read_b64_tr_b16 v[50:51], v136 offset:0x3800
	s_waitcnt lgkmcnt(0)
	s_nop 0
	v_add_f32_e32 v0, v0, v20
	v_add_f32_e32 v1, v1, v21
	v_permlane32_swap_b32_e32 v180, v182
	v_pk_add_f32 v[0:1], v[0:1], v[0:1] op_sel:[0,1] op_sel_hi:[1,0]
	v_permlane32_swap_b32_e32 v181, v183
	v_mov_b32_e32 v1, v0
	s_nop 1
	v_permlane32_swap_b32_e32 v0, v1
	v_add_f32_e32 v138, v0, v1
	v_fmac_f32_e32 v138, 0, v178
	v_permlane32_swap_b32_e32 v184, v186
	v_permlane32_swap_b32_e32 v185, v187
	v_permlane32_swap_b32_e32 v188, v190
	v_permlane32_swap_b32_e32 v189, v191
	v_permlane32_swap_b32_e32 v192, v194
	v_permlane32_swap_b32_e32 v193, v195
	v_mfma_f32_32x32x16_bf16 v[20:35], v[180:183], v[36:39], v[4:19]
	ds_read_b64_tr_b16 v[52:53], v136 offset:0x200
	ds_read_b64_tr_b16 v[54:55], v136 offset:0xa00
	ds_read_b64_tr_b16 v[56:57], v136 offset:0x1200
	ds_read_b64_tr_b16 v[58:59], v136 offset:0x1a00
	ds_read_b64_tr_b16 v[60:61], v136 offset:0x2200
	ds_read_b64_tr_b16 v[62:63], v136 offset:0x2a00
	ds_read_b64_tr_b16 v[64:65], v136 offset:0x3200
	v_mfma_f32_32x32x16_bf16 v[20:35], v[184:187], v[40:43], v[20:35]
	ds_read_b64_tr_b16 v[66:67], v136 offset:0x3a00
	s_waitcnt lgkmcnt(0)
	v_mfma_f32_32x32x16_bf16 v[20:35], v[188:191], v[44:47], v[20:35]
	v_mfma_f32_32x32x16_bf16 v[20:35], v[192:195], v[48:51], v[20:35]
	v_mfma_f32_32x32x16_bf16 v[36:51], v[180:183], v[52:55], v[4:19]
	ds_read_b64_tr_b16 v[196:197], v136 offset:0x400
	ds_read_b64_tr_b16 v[198:199], v136 offset:0xc00
	ds_read_b64_tr_b16 v[200:201], v136 offset:0x1400
	ds_read_b64_tr_b16 v[202:203], v136 offset:0x1c00
	ds_read_b64_tr_b16 v[204:205], v136 offset:0x2400
	ds_read_b64_tr_b16 v[206:207], v136 offset:0x2c00
	ds_read_b64_tr_b16 v[208:209], v136 offset:0x3400
	v_mfma_f32_32x32x16_bf16 v[36:51], v[184:187], v[56:59], v[36:51]
	ds_read_b64_tr_b16 v[210:211], v136 offset:0x3c00
	s_waitcnt lgkmcnt(0)
	v_mfma_f32_32x32x16_bf16 v[36:51], v[188:191], v[60:63], v[36:51]
	v_mfma_f32_32x32x16_bf16 v[36:51], v[192:195], v[64:67], v[36:51]
	v_mfma_f32_32x32x16_bf16 v[52:67], v[180:183], v[196:199], v[4:19]
	ds_read_b64_tr_b16 v[196:197], v136 offset:0x600
	ds_read_b64_tr_b16 v[198:199], v136 offset:0xe00
	v_mfma_f32_32x32x16_bf16 v[52:67], v[184:187], v[200:203], v[52:67]
	ds_read_b64_tr_b16 v[200:201], v136 offset:0x1600
	ds_read_b64_tr_b16 v[202:203], v136 offset:0x1e00
	v_mfma_f32_32x32x16_bf16 v[52:67], v[188:191], v[204:207], v[52:67]
	ds_read_b64_tr_b16 v[204:205], v136 offset:0x2600
	ds_read_b64_tr_b16 v[206:207], v136 offset:0x2e00
	v_mfma_f32_32x32x16_bf16 v[52:67], v[192:195], v[208:211], v[52:67]
	ds_read_b64_tr_b16 v[208:209], v136 offset:0x3600
	ds_read_b64_tr_b16 v[210:211], v136 offset:0x3e00
	s_waitcnt lgkmcnt(0)
	v_mfma_f32_32x32x16_bf16 v[4:19], v[180:183], v[196:199], v[4:19]
	v_mfma_f32_32x32x16_bf16 v[4:19], v[184:187], v[200:203], v[4:19]
	v_mfma_f32_32x32x16_bf16 v[4:19], v[188:191], v[204:207], v[4:19]
	v_mfma_f32_32x32x16_bf16 v[4:19], v[192:195], v[208:211], v[4:19]

.LBB0_1736:
	v_mul_f32_e32 v2, 0xbe0293ee, v175
	v_cndmask_b32_e64 v2, v168, v2, s[98:99]
	v_fma_f32 v68, v68, s2, v2
	v_fma_f32 v69, v69, s2, v2
	v_fma_f32 v70, v70, s2, v2
	v_fma_f32 v71, v71, s2, v2
	v_fma_f32 v72, v72, s2, v2
	v_fma_f32 v73, v73, s2, v2
	v_fma_f32 v74, v74, s2, v2
	v_fma_f32 v75, v75, s2, v2
	v_fma_f32 v76, v76, s2, v2
	v_fma_f32 v77, v77, s2, v2
	v_fma_f32 v78, v78, s2, v2
	v_fma_f32 v79, v79, s2, v2
	v_fma_f32 v80, v80, s2, v2
	v_fma_f32 v81, v81, s2, v2
	v_fma_f32 v82, v82, s2, v2
	v_fma_f32 v83, v83, s2, v2
	v_exp_f32_e32 v68, v68
	v_exp_f32_e32 v69, v69
	v_exp_f32_e32 v70, v70
	v_exp_f32_e32 v71, v71
	v_exp_f32_e32 v72, v72
	v_exp_f32_e32 v73, v73
	v_exp_f32_e32 v74, v74
	v_exp_f32_e32 v75, v75
	v_exp_f32_e32 v76, v76
	v_exp_f32_e32 v77, v77
	v_exp_f32_e32 v78, v78
	v_exp_f32_e32 v79, v79
	v_exp_f32_e32 v80, v80
	v_exp_f32_e32 v81, v81
	v_exp_f32_e32 v82, v82
	v_exp_f32_e32 v83, v83
	v_fma_f32 v86, v86, s2, v2
	v_fma_f32 v87, v87, s2, v2
	v_fma_f32 v84, v84, s2, v2
	v_fma_f32 v85, v85, s2, v2
	v_fma_f32 v88, v88, s2, v2
	v_fma_f32 v89, v89, s2, v2
	v_fma_f32 v90, v90, s2, v2
	v_fma_f32 v91, v91, s2, v2
	v_fma_f32 v92, v92, s2, v2
	v_fma_f32 v93, v93, s2, v2
	v_fma_f32 v94, v94, s2, v2
	v_fma_f32 v95, v95, s2, v2
	v_fma_f32 v96, v96, s2, v2
	v_fma_f32 v97, v97, s2, v2
	v_fma_f32 v98, v98, s2, v2
	v_fma_f32 v99, v99, s2, v2

.LBB0_1743:
	s_andn2_b64 vcc, exec, s[16:17]
	s_cbranch_vccnz .LBB0_1749
	v_cmp_gt_f32_e32 vcc, 1.0, v178
	s_cbranch_vccz .LBB0_1748
	s_and_saveexec_b64 s[4:5], s[10:11]
	ds_write_b32 v176, v178
	s_or_b64 exec, exec, s[4:5]
	v_readlane_b32 s1, v254, 32
	s_waitcnt lgkmcnt(0)
	s_nop 1
	v_add_u32_e32 v1, s1, v177
	v_readlane_b32 s1, v254, 33
	s_nop 1
	v_add_u32_e32 v2, s1, v177
	v_readlane_b32 s1, v254, 31
	ds_read_b128 v[180:183], v1
	ds_read_b128 v[184:187], v2
	v_add_u32_e32 v1, s1, v177
	v_readlane_b32 s1, v254, 30
	ds_read_b128 v[188:191], v1
	s_waitcnt lgkmcnt(2)
	v_mul_f32_e32 v28, v28, v180
	v_mul_f32_e32 v29, v29, v181
	v_add_u32_e32 v1, s1, v177
	ds_read_b128 v[192:195], v1
	s_waitcnt lgkmcnt(2)
	v_mul_f32_e32 v32, v32, v184
	v_mul_f32_e32 v33, v33, v185
	s_waitcnt lgkmcnt(1)
	v_mul_f32_e32 v24, v24, v188
	v_mul_f32_e32 v25, v25, v189
	v_mul_f32_e32 v34, v34, v186
	v_mul_f32_e32 v35, v35, v187
	v_mul_f32_e32 v30, v30, v182
	v_mul_f32_e32 v31, v31, v183
	v_mul_f32_e32 v26, v26, v190
	v_mul_f32_e32 v27, v27, v191
	s_waitcnt lgkmcnt(0)
	v_mul_f32_e32 v22, v22, v194
	v_mul_f32_e32 v23, v23, v195
	v_mul_f32_e32 v20, v20, v192
	v_mul_f32_e32 v21, v21, v193
	v_mul_f32_e32 v48, v48, v184
	v_mul_f32_e32 v49, v49, v185
	v_mul_f32_e32 v44, v44, v180
	v_mul_f32_e32 v45, v45, v181
	v_mul_f32_e32 v40, v40, v188
	v_mul_f32_e32 v41, v41, v189
	v_mul_f32_e32 v50, v50, v186
	v_mul_f32_e32 v51, v51, v187
	v_mul_f32_e32 v46, v46, v182
	v_mul_f32_e32 v47, v47, v183
	v_mul_f32_e32 v42, v42, v190
	v_mul_f32_e32 v43, v43, v191
	v_mul_f32_e32 v38, v38, v194
	v_mul_f32_e32 v39, v39, v195
	v_mul_f32_e32 v36, v36, v192
	v_mul_f32_e32 v37, v37, v193
	v_mul_f32_e32 v64, v64, v184
	v_mul_f32_e32 v65, v65, v185
	v_mul_f32_e32 v60, v60, v180
	v_mul_f32_e32 v61, v61, v181
	v_mul_f32_e32 v56, v56, v188
	v_mul_f32_e32 v57, v57, v189
	v_mul_f32_e32 v66, v66, v186
	v_mul_f32_e32 v67, v67, v187
	v_mul_f32_e32 v62, v62, v182
	v_mul_f32_e32 v63, v63, v183
	v_mul_f32_e32 v58, v58, v190
	v_mul_f32_e32 v59, v59, v191
	v_mul_f32_e32 v54, v54, v194
	v_mul_f32_e32 v55, v55, v195
	v_mul_f32_e32 v52, v52, v192
	v_mul_f32_e32 v53, v53, v193
	v_mul_f32_e32 v16, v16, v184
	v_mul_f32_e32 v17, v17, v185
	v_mul_f32_e32 v12, v12, v180
	v_mul_f32_e32 v13, v13, v181
	v_mul_f32_e32 v8, v8, v188
	v_mul_f32_e32 v9, v9, v189
	v_mul_f32_e32 v18, v18, v186
	v_mul_f32_e32 v19, v19, v187
	v_mul_f32_e32 v14, v14, v182
	v_mul_f32_e32 v15, v15, v183
	v_mul_f32_e32 v10, v10, v190
	v_mul_f32_e32 v11, v11, v191
	v_mul_f32_e32 v6, v6, v194
	v_mul_f32_e32 v7, v7, v195
	v_mul_f32_e32 v4, v4, v192
	v_mul_f32_e32 v5, v5, v193
.LBB0_1748:
	v_exp_f32_e32 v84, v84
	v_exp_f32_e32 v85, v85
	v_exp_f32_e32 v86, v86
	v_exp_f32_e32 v87, v87
	v_exp_f32_e32 v88, v88
	v_exp_f32_e32 v89, v89
	v_exp_f32_e32 v90, v90
	v_exp_f32_e32 v91, v91
	v_exp_f32_e32 v92, v92
	v_exp_f32_e32 v93, v93
	v_add_f32_e32 v194, v68, v84
	v_add_f32_e32 v195, v69, v85
	v_exp_f32_e32 v94, v94
	v_exp_f32_e32 v95, v95
	v_add_f32_e32 v192, v70, v86
	v_add_f32_e32 v193, v71, v87
	v_add_f32_e32 v194, 0, v194
	v_add_f32_e32 v195, 0, v195
	v_exp_f32_e32 v96, v96
	v_exp_f32_e32 v97, v97
	v_add_f32_e32 v190, v72, v88
	v_add_f32_e32 v191, v73, v89
	v_add_f32_e32 v192, v192, v194
	v_add_f32_e32 v193, v193, v195
	v_exp_f32_e32 v98, v98
	v_exp_f32_e32 v99, v99
	v_add_f32_e32 v188, v74, v90
	v_add_f32_e32 v189, v75, v91
	v_add_f32_e32 v190, v190, v192
	v_add_f32_e32 v191, v191, v193
	v_add_f32_e32 v186, v76, v92
	v_add_f32_e32 v187, v77, v93
	v_add_f32_e32 v188, v188, v190
	v_add_f32_e32 v189, v189, v191
	v_add_f32_e32 v184, v78, v94
	v_add_f32_e32 v185, v79, v95
	v_add_f32_e32 v186, v186, v188
	v_add_f32_e32 v187, v187, v189
	v_add_f32_e32 v182, v80, v96
	v_add_f32_e32 v183, v81, v97
	v_add_f32_e32 v184, v184, v186
	v_add_f32_e32 v185, v185, v187
	v_add_f32_e32 v180, v82, v98
	v_add_f32_e32 v181, v83, v99
	v_add_f32_e32 v182, v182, v184
	v_add_f32_e32 v183, v183, v185
	s_nop 0
	v_add_f32_e32 v180, v180, v182
	v_add_f32_e32 v181, v181, v183
	s_nop 0
	v_pk_add_f32 v[180:181], v[180:181], v[180:181] op_sel:[0,1] op_sel_hi:[1,0]
	s_nop 0
	v_mov_b32_e32 v1, v180
	s_nop 1
	v_permlane32_swap_b32_e32 v180, v1
	v_add_f32_e32 v1, v180, v1
	v_cvt_pk_bf16_f32 v180, v68, v69
	v_cvt_pk_bf16_f32 v181, v70, v71
	v_cvt_pk_bf16_f32 v182, v72, v73
	v_cvt_pk_bf16_f32 v183, v74, v75
	v_cvt_pk_bf16_f32 v184, v76, v77
	v_cvt_pk_bf16_f32 v185, v78, v79
	v_cvt_pk_bf16_f32 v186, v80, v81
	v_cvt_pk_bf16_f32 v187, v82, v83
	v_cvt_pk_bf16_f32 v188, v84, v85
	v_cvt_pk_bf16_f32 v189, v86, v87
	v_cvt_pk_bf16_f32 v190, v88, v89
	v_cvt_pk_bf16_f32 v191, v90, v91
	v_cvt_pk_bf16_f32 v192, v92, v93
	v_cvt_pk_bf16_f32 v193, v94, v95
	v_cvt_pk_bf16_f32 v194, v96, v97
	v_cvt_pk_bf16_f32 v195, v98, v99
	ds_read_b64_tr_b16 v[196:197], v0 offset:0
	ds_read_b64_tr_b16 v[198:199], v0 offset:0x800
	ds_read_b64_tr_b16 v[200:201], v0 offset:0x1000
	ds_read_b64_tr_b16 v[202:203], v0 offset:0x1800
	ds_read_b64_tr_b16 v[204:205], v0 offset:0x2000
	ds_read_b64_tr_b16 v[206:207], v0 offset:0x2800
	ds_read_b64_tr_b16 v[208:209], v0 offset:0x3000
	ds_read_b64_tr_b16 v[210:211], v0 offset:0x3800
	s_waitcnt lgkmcnt(0)
	v_fmac_f32_e32 v1, v138, v178
	v_permlane32_swap_b32_e32 v180, v182
	v_permlane32_swap_b32_e32 v181, v183
	v_permlane32_swap_b32_e32 v184, v186
	v_permlane32_swap_b32_e32 v185, v187
	v_permlane32_swap_b32_e32 v188, v190
	v_permlane32_swap_b32_e32 v189, v191
	v_permlane32_swap_b32_e32 v192, v194
	v_permlane32_swap_b32_e32 v193, v195
	v_mfma_f32_32x32x16_bf16 v[20:35], v[180:183], v[196:199], v[20:35]
	ds_read_b64_tr_b16 v[196:197], v0 offset:0x200
	ds_read_b64_tr_b16 v[198:199], v0 offset:0xa00
	v_mfma_f32_32x32x16_bf16 v[20:35], v[184:187], v[200:203], v[20:35]
	ds_read_b64_tr_b16 v[200:201], v0 offset:0x1200
	ds_read_b64_tr_b16 v[202:203], v0 offset:0x1a00
	v_mfma_f32_32x32x16_bf16 v[20:35], v[188:191], v[204:207], v[20:35]
	ds_read_b64_tr_b16 v[204:205], v0 offset:0x2200
	ds_read_b64_tr_b16 v[206:207], v0 offset:0x2a00
	v_mfma_f32_32x32x16_bf16 v[20:35], v[192:195], v[208:211], v[20:35]
	ds_read_b64_tr_b16 v[208:209], v0 offset:0x3200
	ds_read_b64_tr_b16 v[210:211], v0 offset:0x3a00
	s_waitcnt lgkmcnt(0)
	v_mfma_f32_32x32x16_bf16 v[36:51], v[180:183], v[196:199], v[36:51]
	ds_read_b64_tr_b16 v[196:197], v0 offset:0x400
	ds_read_b64_tr_b16 v[198:199], v0 offset:0xc00
	v_mfma_f32_32x32x16_bf16 v[36:51], v[184:187], v[200:203], v[36:51]
	ds_read_b64_tr_b16 v[200:201], v0 offset:0x1400
	ds_read_b64_tr_b16 v[202:203], v0 offset:0x1c00
	v_mfma_f32_32x32x16_bf16 v[36:51], v[188:191], v[204:207], v[36:51]
	ds_read_b64_tr_b16 v[204:205], v0 offset:0x2400
	ds_read_b64_tr_b16 v[206:207], v0 offset:0x2c00
	v_mfma_f32_32x32x16_bf16 v[36:51], v[192:195], v[208:211], v[36:51]
	ds_read_b64_tr_b16 v[208:209], v0 offset:0x3400
	ds_read_b64_tr_b16 v[210:211], v0 offset:0x3c00
	s_waitcnt lgkmcnt(0)
	v_mfma_f32_32x32x16_bf16 v[52:67], v[180:183], v[196:199], v[52:67]
	ds_read_b64_tr_b16 v[196:197], v0 offset:0x600
	ds_read_b64_tr_b16 v[198:199], v0 offset:0xe00
	v_mfma_f32_32x32x16_bf16 v[52:67], v[184:187], v[200:203], v[52:67]
	ds_read_b64_tr_b16 v[200:201], v0 offset:0x1600
	ds_read_b64_tr_b16 v[202:203], v0 offset:0x1e00
	v_mfma_f32_32x32x16_bf16 v[52:67], v[188:191], v[204:207], v[52:67]
	ds_read_b64_tr_b16 v[204:205], v0 offset:0x2600
	ds_read_b64_tr_b16 v[206:207], v0 offset:0x2e00
	v_mfma_f32_32x32x16_bf16 v[52:67], v[192:195], v[208:211], v[52:67]
	ds_read_b64_tr_b16 v[208:209], v0 offset:0x3600
	ds_read_b64_tr_b16 v[210:211], v0 offset:0x3e00
	s_waitcnt lgkmcnt(0)
	v_mfma_f32_32x32x16_bf16 v[4:19], v[180:183], v[196:199], v[4:19]
	v_mov_b32_e32 v138, v1
	v_mfma_f32_32x32x16_bf16 v[4:19], v[184:187], v[200:203], v[4:19]
	v_mfma_f32_32x32x16_bf16 v[4:19], v[188:191], v[204:207], v[4:19]
	v_mfma_f32_32x32x16_bf16 v[4:19], v[192:195], v[208:211], v[4:19]

.LBB0_1771:
	s_andn2_b64 vcc, exec, s[20:21]
	s_cbranch_vccnz .LBB0_1777
	v_cmp_gt_f32_e32 vcc, 1.0, v178
	s_cbranch_vccz .LBB0_1776
	s_and_saveexec_b64 s[4:5], s[10:11]
	ds_write_b32 v176, v178
	s_or_b64 exec, exec, s[4:5]
	v_readlane_b32 s4, v254, 32
	s_waitcnt lgkmcnt(0)
	s_nop 1
	v_add_u32_e32 v1, s4, v177
	v_readlane_b32 s4, v254, 33
	s_nop 1
	v_add_u32_e32 v2, s4, v177
	v_readlane_b32 s4, v254, 31
	ds_read_b128 v[180:183], v1
	ds_read_b128 v[184:187], v2
	v_add_u32_e32 v1, s4, v177
	v_readlane_b32 s4, v254, 30
	ds_read_b128 v[188:191], v1
	s_waitcnt lgkmcnt(2)
	v_mul_f32_e32 v28, v28, v180
	v_mul_f32_e32 v29, v29, v181
	v_add_u32_e32 v1, s4, v177
	ds_read_b128 v[192:195], v1
	s_waitcnt lgkmcnt(2)
	v_mul_f32_e32 v32, v32, v184
	v_mul_f32_e32 v33, v33, v185
	s_waitcnt lgkmcnt(1)
	v_mul_f32_e32 v24, v24, v188
	v_mul_f32_e32 v25, v25, v189
	v_mul_f32_e32 v34, v34, v186
	v_mul_f32_e32 v35, v35, v187
	v_mul_f32_e32 v30, v30, v182
	v_mul_f32_e32 v31, v31, v183
	v_mul_f32_e32 v26, v26, v190
	v_mul_f32_e32 v27, v27, v191
	s_waitcnt lgkmcnt(0)
	v_mul_f32_e32 v22, v22, v194
	v_mul_f32_e32 v23, v23, v195
	v_mul_f32_e32 v20, v20, v192
	v_mul_f32_e32 v21, v21, v193
	v_mul_f32_e32 v48, v48, v184
	v_mul_f32_e32 v49, v49, v185
	v_mul_f32_e32 v44, v44, v180
	v_mul_f32_e32 v45, v45, v181
	v_mul_f32_e32 v40, v40, v188
	v_mul_f32_e32 v41, v41, v189
	v_mul_f32_e32 v50, v50, v186
	v_mul_f32_e32 v51, v51, v187
	v_mul_f32_e32 v46, v46, v182
	v_mul_f32_e32 v47, v47, v183
	v_mul_f32_e32 v42, v42, v190
	v_mul_f32_e32 v43, v43, v191
	v_mul_f32_e32 v38, v38, v194
	v_mul_f32_e32 v39, v39, v195
	v_mul_f32_e32 v36, v36, v192
	v_mul_f32_e32 v37, v37, v193
	v_mul_f32_e32 v64, v64, v184
	v_mul_f32_e32 v65, v65, v185
	v_mul_f32_e32 v60, v60, v180
	v_mul_f32_e32 v61, v61, v181
	v_mul_f32_e32 v56, v56, v188
	v_mul_f32_e32 v57, v57, v189
	v_mul_f32_e32 v66, v66, v186
	v_mul_f32_e32 v67, v67, v187
	v_mul_f32_e32 v62, v62, v182
	v_mul_f32_e32 v63, v63, v183
	v_mul_f32_e32 v58, v58, v190
	v_mul_f32_e32 v59, v59, v191
	v_mul_f32_e32 v54, v54, v194
	v_mul_f32_e32 v55, v55, v195
	v_mul_f32_e32 v52, v52, v192
	v_mul_f32_e32 v53, v53, v193
	v_mul_f32_e32 v16, v16, v184
	v_mul_f32_e32 v17, v17, v185
	v_mul_f32_e32 v12, v12, v180
	v_mul_f32_e32 v13, v13, v181
	v_mul_f32_e32 v8, v8, v188
	v_mul_f32_e32 v9, v9, v189
	v_mul_f32_e32 v18, v18, v186
	v_mul_f32_e32 v19, v19, v187
	v_mul_f32_e32 v14, v14, v182
	v_mul_f32_e32 v15, v15, v183
	v_mul_f32_e32 v10, v10, v190
	v_mul_f32_e32 v11, v11, v191
	v_mul_f32_e32 v6, v6, v194
	v_mul_f32_e32 v7, v7, v195
	v_mul_f32_e32 v4, v4, v192
	v_mul_f32_e32 v5, v5, v193
.LBB0_1776:
	v_exp_f32_e32 v84, v84
	v_exp_f32_e32 v85, v85
	v_exp_f32_e32 v86, v86
	v_exp_f32_e32 v87, v87
	v_exp_f32_e32 v88, v88
	v_exp_f32_e32 v89, v89
	v_exp_f32_e32 v90, v90
	v_exp_f32_e32 v91, v91
	v_exp_f32_e32 v92, v92
	v_exp_f32_e32 v93, v93
	v_add_f32_e32 v194, v68, v84
	v_add_f32_e32 v195, v69, v85
	v_exp_f32_e32 v94, v94
	v_exp_f32_e32 v95, v95
	v_add_f32_e32 v192, v70, v86
	v_add_f32_e32 v193, v71, v87
	v_add_f32_e32 v194, 0, v194
	v_add_f32_e32 v195, 0, v195
	v_exp_f32_e32 v96, v96
	v_exp_f32_e32 v97, v97
	v_add_f32_e32 v190, v72, v88
	v_add_f32_e32 v191, v73, v89
	v_add_f32_e32 v192, v192, v194
	v_add_f32_e32 v193, v193, v195
	v_exp_f32_e32 v98, v98
	v_exp_f32_e32 v99, v99
	v_add_f32_e32 v188, v74, v90
	v_add_f32_e32 v189, v75, v91
	v_add_f32_e32 v190, v190, v192
	v_add_f32_e32 v191, v191, v193
	v_add_f32_e32 v186, v76, v92
	v_add_f32_e32 v187, v77, v93
	v_add_f32_e32 v188, v188, v190
	v_add_f32_e32 v189, v189, v191
	v_add_f32_e32 v184, v78, v94
	v_add_f32_e32 v185, v79, v95
	v_add_f32_e32 v186, v186, v188
	v_add_f32_e32 v187, v187, v189
	v_add_f32_e32 v182, v80, v96
	v_add_f32_e32 v183, v81, v97
	v_add_f32_e32 v184, v184, v186
	v_add_f32_e32 v185, v185, v187
	v_add_f32_e32 v180, v82, v98
	v_add_f32_e32 v181, v83, v99
	v_add_f32_e32 v182, v182, v184
	v_add_f32_e32 v183, v183, v185
	s_nop 0
	v_add_f32_e32 v180, v180, v182
	v_add_f32_e32 v181, v181, v183
	s_nop 0
	v_pk_add_f32 v[180:181], v[180:181], v[180:181] op_sel:[0,1] op_sel_hi:[1,0]
	s_nop 0
	v_mov_b32_e32 v1, v180
	s_nop 1
	v_permlane32_swap_b32_e32 v180, v1
	v_add_f32_e32 v1, v180, v1
	v_cvt_pk_bf16_f32 v180, v68, v69
	v_cvt_pk_bf16_f32 v181, v70, v71
	v_cvt_pk_bf16_f32 v182, v72, v73
	v_cvt_pk_bf16_f32 v183, v74, v75
	v_cvt_pk_bf16_f32 v184, v76, v77
	v_cvt_pk_bf16_f32 v185, v78, v79
	v_cvt_pk_bf16_f32 v186, v80, v81
	v_cvt_pk_bf16_f32 v187, v82, v83
	v_cvt_pk_bf16_f32 v188, v84, v85
	v_cvt_pk_bf16_f32 v189, v86, v87
	v_cvt_pk_bf16_f32 v190, v88, v89
	v_cvt_pk_bf16_f32 v191, v90, v91
	v_cvt_pk_bf16_f32 v192, v92, v93
	v_cvt_pk_bf16_f32 v193, v94, v95
	v_cvt_pk_bf16_f32 v194, v96, v97
	v_cvt_pk_bf16_f32 v195, v98, v99
	ds_read_b64_tr_b16 v[196:197], v136 offset:0
	ds_read_b64_tr_b16 v[198:199], v136 offset:0x800
	ds_read_b64_tr_b16 v[200:201], v136 offset:0x1000
	ds_read_b64_tr_b16 v[202:203], v136 offset:0x1800
	ds_read_b64_tr_b16 v[204:205], v136 offset:0x2000
	ds_read_b64_tr_b16 v[206:207], v136 offset:0x2800
	ds_read_b64_tr_b16 v[208:209], v136 offset:0x3000
	ds_read_b64_tr_b16 v[210:211], v136 offset:0x3800
	s_waitcnt lgkmcnt(0)
	v_fmac_f32_e32 v1, v138, v178
	v_permlane32_swap_b32_e32 v180, v182
	v_permlane32_swap_b32_e32 v181, v183
	v_permlane32_swap_b32_e32 v184, v186
	v_permlane32_swap_b32_e32 v185, v187
	v_permlane32_swap_b32_e32 v188, v190
	v_permlane32_swap_b32_e32 v189, v191
	v_permlane32_swap_b32_e32 v192, v194
	v_permlane32_swap_b32_e32 v193, v195
	v_mfma_f32_32x32x16_bf16 v[20:35], v[180:183], v[196:199], v[20:35]
	ds_read_b64_tr_b16 v[196:197], v136 offset:0x200
	ds_read_b64_tr_b16 v[198:199], v136 offset:0xa00
	v_mfma_f32_32x32x16_bf16 v[20:35], v[184:187], v[200:203], v[20:35]
	ds_read_b64_tr_b16 v[200:201], v136 offset:0x1200
	ds_read_b64_tr_b16 v[202:203], v136 offset:0x1a00
	v_mfma_f32_32x32x16_bf16 v[20:35], v[188:191], v[204:207], v[20:35]
	ds_read_b64_tr_b16 v[204:205], v136 offset:0x2200
	ds_read_b64_tr_b16 v[206:207], v136 offset:0x2a00
	v_mfma_f32_32x32x16_bf16 v[20:35], v[192:195], v[208:211], v[20:35]
	ds_read_b64_tr_b16 v[208:209], v136 offset:0x3200
	ds_read_b64_tr_b16 v[210:211], v136 offset:0x3a00
	s_waitcnt lgkmcnt(0)
	v_mfma_f32_32x32x16_bf16 v[36:51], v[180:183], v[196:199], v[36:51]
	ds_read_b64_tr_b16 v[196:197], v136 offset:0x400
	ds_read_b64_tr_b16 v[198:199], v136 offset:0xc00
	v_mfma_f32_32x32x16_bf16 v[36:51], v[184:187], v[200:203], v[36:51]
	ds_read_b64_tr_b16 v[200:201], v136 offset:0x1400
	ds_read_b64_tr_b16 v[202:203], v136 offset:0x1c00
	v_mfma_f32_32x32x16_bf16 v[36:51], v[188:191], v[204:207], v[36:51]
	ds_read_b64_tr_b16 v[204:205], v136 offset:0x2400
	ds_read_b64_tr_b16 v[206:207], v136 offset:0x2c00
	v_mfma_f32_32x32x16_bf16 v[36:51], v[192:195], v[208:211], v[36:51]
	ds_read_b64_tr_b16 v[208:209], v136 offset:0x3400
	ds_read_b64_tr_b16 v[210:211], v136 offset:0x3c00
	s_waitcnt lgkmcnt(0)
	v_mfma_f32_32x32x16_bf16 v[52:67], v[180:183], v[196:199], v[52:67]
	ds_read_b64_tr_b16 v[196:197], v136 offset:0x600
	ds_read_b64_tr_b16 v[198:199], v136 offset:0xe00
	v_mfma_f32_32x32x16_bf16 v[52:67], v[184:187], v[200:203], v[52:67]
	ds_read_b64_tr_b16 v[200:201], v136 offset:0x1600
	ds_read_b64_tr_b16 v[202:203], v136 offset:0x1e00
	v_mfma_f32_32x32x16_bf16 v[52:67], v[188:191], v[204:207], v[52:67]
	ds_read_b64_tr_b16 v[204:205], v136 offset:0x2600
	ds_read_b64_tr_b16 v[206:207], v136 offset:0x2e00
	v_mfma_f32_32x32x16_bf16 v[52:67], v[192:195], v[208:211], v[52:67]
	ds_read_b64_tr_b16 v[208:209], v136 offset:0x3600
	ds_read_b64_tr_b16 v[210:211], v136 offset:0x3e00
	s_waitcnt lgkmcnt(0)
	v_mfma_f32_32x32x16_bf16 v[4:19], v[180:183], v[196:199], v[4:19]
	v_mov_b32_e32 v138, v1
	v_mfma_f32_32x32x16_bf16 v[4:19], v[184:187], v[200:203], v[4:19]
	v_mfma_f32_32x32x16_bf16 v[4:19], v[188:191], v[204:207], v[4:19]
	v_mfma_f32_32x32x16_bf16 v[4:19], v[192:195], v[208:211], v[4:19]

.LBB0_1795:
	s_andn2_b64 vcc, exec, s[16:17]
	s_cbranch_vccnz .LBB0_1801
	v_cmp_gt_f32_e32 vcc, 1.0, v178
	s_cbranch_vccz .LBB0_1800
	s_and_saveexec_b64 s[4:5], s[10:11]
	ds_write_b32 v176, v178
	s_or_b64 exec, exec, s[4:5]
	v_readlane_b32 s4, v254, 32
	s_waitcnt lgkmcnt(0)
	s_nop 1
	v_add_u32_e32 v1, s4, v177
	v_readlane_b32 s4, v254, 33
	s_nop 1
	v_add_u32_e32 v2, s4, v177
	v_readlane_b32 s4, v254, 31
	ds_read_b128 v[180:183], v1
	ds_read_b128 v[184:187], v2
	v_add_u32_e32 v1, s4, v177
	v_readlane_b32 s4, v254, 30
	ds_read_b128 v[188:191], v1
	s_waitcnt lgkmcnt(2)
	v_mul_f32_e32 v28, v28, v180
	v_mul_f32_e32 v29, v29, v181
	v_add_u32_e32 v1, s4, v177
	ds_read_b128 v[192:195], v1
	s_waitcnt lgkmcnt(2)
	v_mul_f32_e32 v32, v32, v184
	v_mul_f32_e32 v33, v33, v185
	s_waitcnt lgkmcnt(1)
	v_mul_f32_e32 v24, v24, v188
	v_mul_f32_e32 v25, v25, v189
	v_mul_f32_e32 v34, v34, v186
	v_mul_f32_e32 v35, v35, v187
	v_mul_f32_e32 v30, v30, v182
	v_mul_f32_e32 v31, v31, v183
	v_mul_f32_e32 v26, v26, v190
	v_mul_f32_e32 v27, v27, v191
	s_waitcnt lgkmcnt(0)
	v_mul_f32_e32 v22, v22, v194
	v_mul_f32_e32 v23, v23, v195
	v_mul_f32_e32 v20, v20, v192
	v_mul_f32_e32 v21, v21, v193
	v_mul_f32_e32 v48, v48, v184
	v_mul_f32_e32 v49, v49, v185
	v_mul_f32_e32 v44, v44, v180
	v_mul_f32_e32 v45, v45, v181
	v_mul_f32_e32 v40, v40, v188
	v_mul_f32_e32 v41, v41, v189
	v_mul_f32_e32 v50, v50, v186
	v_mul_f32_e32 v51, v51, v187
	v_mul_f32_e32 v46, v46, v182
	v_mul_f32_e32 v47, v47, v183
	v_mul_f32_e32 v42, v42, v190
	v_mul_f32_e32 v43, v43, v191
	v_mul_f32_e32 v38, v38, v194
	v_mul_f32_e32 v39, v39, v195
	v_mul_f32_e32 v36, v36, v192
	v_mul_f32_e32 v37, v37, v193
	v_mul_f32_e32 v64, v64, v184
	v_mul_f32_e32 v65, v65, v185
	v_mul_f32_e32 v60, v60, v180
	v_mul_f32_e32 v61, v61, v181
	v_mul_f32_e32 v56, v56, v188
	v_mul_f32_e32 v57, v57, v189
	v_mul_f32_e32 v66, v66, v186
	v_mul_f32_e32 v67, v67, v187
	v_mul_f32_e32 v62, v62, v182
	v_mul_f32_e32 v63, v63, v183
	v_mul_f32_e32 v58, v58, v190
	v_mul_f32_e32 v59, v59, v191
	v_mul_f32_e32 v54, v54, v194
	v_mul_f32_e32 v55, v55, v195
	v_mul_f32_e32 v52, v52, v192
	v_mul_f32_e32 v53, v53, v193
	v_mul_f32_e32 v16, v16, v184
	v_mul_f32_e32 v17, v17, v185
	v_mul_f32_e32 v12, v12, v180
	v_mul_f32_e32 v13, v13, v181
	v_mul_f32_e32 v8, v8, v188
	v_mul_f32_e32 v9, v9, v189
	v_mul_f32_e32 v18, v18, v186
	v_mul_f32_e32 v19, v19, v187
	v_mul_f32_e32 v14, v14, v182
	v_mul_f32_e32 v15, v15, v183
	v_mul_f32_e32 v10, v10, v190
	v_mul_f32_e32 v11, v11, v191
	v_mul_f32_e32 v6, v6, v194
	v_mul_f32_e32 v7, v7, v195
	v_mul_f32_e32 v4, v4, v192
	v_mul_f32_e32 v5, v5, v193

.LBB0_1814:
	v_mul_f32_e32 v0, 0xbe0293ee, v154
	v_fma_f32 v84, v4, s2, v0
	v_fma_f32 v85, v5, s2, v0
	v_fma_f32 v4, v24, s2, v0
	v_fma_f32 v5, v25, s2, v0
	v_fma_f32 v20, v20, s2, v0
	v_fma_f32 v21, v21, s2, v0
	v_exp_f32_e32 v72, v4
	v_exp_f32_e32 v73, v5
	v_fma_f32 v4, v26, s2, v0
	v_fma_f32 v5, v27, s2, v0
	v_exp_f32_e32 v68, v20
	v_exp_f32_e32 v74, v4
	v_exp_f32_e32 v75, v5
	v_fma_f32 v4, v28, s2, v0
	v_fma_f32 v5, v29, s2, v0
	v_exp_f32_e32 v69, v21
	v_exp_f32_e32 v76, v4
	v_exp_f32_e32 v77, v5
	v_fma_f32 v4, v30, s2, v0
	v_fma_f32 v5, v31, s2, v0
	v_fma_f32 v20, v22, s2, v0
	v_fma_f32 v21, v23, s2, v0
	v_exp_f32_e32 v78, v4
	v_exp_f32_e32 v79, v5
	v_fma_f32 v4, v32, s2, v0
	v_fma_f32 v5, v33, s2, v0
	v_exp_f32_e32 v70, v20
	v_exp_f32_e32 v80, v4
	v_exp_f32_e32 v81, v5
	v_fma_f32 v4, v34, s2, v0
	v_fma_f32 v5, v35, s2, v0
	v_exp_f32_e32 v71, v21
	v_exp_f32_e32 v82, v4
	v_exp_f32_e32 v83, v5
	v_fma_f32 v86, v6, s2, v0
	v_fma_f32 v87, v7, s2, v0
	v_fma_f32 v88, v8, s2, v0
	v_fma_f32 v89, v9, s2, v0
	v_fma_f32 v90, v10, s2, v0
	v_fma_f32 v91, v11, s2, v0
	v_fma_f32 v92, v12, s2, v0
	v_fma_f32 v93, v13, s2, v0
	v_fma_f32 v94, v14, s2, v0
	v_fma_f32 v95, v15, s2, v0
	v_fma_f32 v96, v16, s2, v0
	v_fma_f32 v97, v17, s2, v0
	v_fma_f32 v98, v18, s2, v0
	v_fma_f32 v99, v19, s2, v0
	s_branch .LBB0_1816

.LBB0_1816:
	s_waitcnt vmcnt(0) lgkmcnt(0)
	s_barrier
	v_readlane_b32 s1, v254, 30
	v_cmp_eq_u32_e64 s[8:9], 0, v140
	v_lshlrev_b32_e32 v140, 4, v140
	v_lshl_add_u32 v141, v141, 2, s1
	s_andn2_b64 vcc, exec, s[10:11]
	s_cbranch_vccnz .LBB0_1821
	v_cmp_gt_f32_e32 vcc, 1.0, v155
	s_cbranch_vccz .LBB0_1822
	s_and_saveexec_b64 s[4:5], s[8:9]
	ds_write_b32 v141, v155
	s_or_b64 exec, exec, s[4:5]
	v_readlane_b32 s1, v254, 30
	s_waitcnt lgkmcnt(0)
	s_nop 1
	v_add_u32_e32 v0, s1, v140
	v_readlane_b32 s1, v254, 32
	s_nop 1
	v_add_u32_e32 v1, s1, v140
	v_readlane_b32 s1, v254, 33
	s_nop 1
	v_add_u32_e32 v2, s1, v140
	v_readlane_b32 s1, v254, 31
	ds_read_b128 v[4:7], v1
	ds_read_b128 v[8:11], v2
	v_add_u32_e32 v1, s1, v140
	ds_read_b128 v[20:23], v1
	ds_read_b128 v[24:27], v0
	s_waitcnt lgkmcnt(3)
	v_mul_f32_e32 v14, 0, v6
	v_mul_f32_e32 v15, 0, v7
	s_waitcnt lgkmcnt(2)
	v_mul_f32_e32 v18, 0, v10
	v_mul_f32_e32 v19, 0, v11
	s_waitcnt lgkmcnt(1)
	v_mul_f32_e32 v10, 0, v22
	v_mul_f32_e32 v11, 0, v23
	s_waitcnt lgkmcnt(0)
	v_mul_f32_e32 v6, 0, v26
	v_mul_f32_e32 v7, 0, v27
	v_mul_f32_e32 v16, 0, v8
	v_mul_f32_e32 v17, 0, v9
	v_mul_f32_e32 v12, 0, v4
	v_mul_f32_e32 v13, 0, v5
	v_mul_f32_e32 v8, 0, v20
	v_mul_f32_e32 v9, 0, v21
	v_mul_f32_e32 v4, 0, v24
	v_mul_f32_e32 v5, 0, v25
	s_branch .LBB0_1823

.LBB0_1823:
	v_exp_f32_e32 v84, v84
	v_exp_f32_e32 v85, v85
	v_exp_f32_e32 v86, v86
	v_exp_f32_e32 v87, v87
	v_exp_f32_e32 v88, v88
	v_exp_f32_e32 v89, v89
	v_exp_f32_e32 v90, v90
	v_exp_f32_e32 v91, v91
	v_exp_f32_e32 v92, v92
	v_exp_f32_e32 v93, v93
	v_add_f32_e32 v32, v68, v84
	v_add_f32_e32 v33, v69, v85
	v_exp_f32_e32 v94, v94
	v_exp_f32_e32 v95, v95
	v_add_f32_e32 v30, v70, v86
	v_add_f32_e32 v31, v71, v87
	v_add_f32_e32 v32, 0, v32
	v_add_f32_e32 v33, 0, v33
	v_exp_f32_e32 v96, v96
	v_exp_f32_e32 v97, v97
	v_add_f32_e32 v28, v72, v88
	v_add_f32_e32 v29, v73, v89
	v_add_f32_e32 v30, v30, v32
	v_add_f32_e32 v31, v31, v33
	v_exp_f32_e32 v98, v98
	v_exp_f32_e32 v99, v99
	v_add_f32_e32 v26, v74, v90
	v_add_f32_e32 v27, v75, v91
	v_add_f32_e32 v28, v28, v30
	v_add_f32_e32 v29, v29, v31
	v_cvt_pk_bf16_f32 v170, v68, v69
	v_cvt_pk_bf16_f32 v171, v70, v71
	v_cvt_pk_bf16_f32 v172, v72, v73
	v_cvt_pk_bf16_f32 v173, v74, v75
	v_cvt_pk_bf16_f32 v174, v76, v77
	v_cvt_pk_bf16_f32 v175, v78, v79
	v_cvt_pk_bf16_f32 v176, v80, v81
	v_cvt_pk_bf16_f32 v177, v82, v83
	v_cvt_pk_bf16_f32 v178, v84, v85
	v_cvt_pk_bf16_f32 v179, v86, v87
	v_cvt_pk_bf16_f32 v180, v88, v89
	v_cvt_pk_bf16_f32 v181, v90, v91
	v_cvt_pk_bf16_f32 v182, v92, v93
	v_cvt_pk_bf16_f32 v183, v94, v95
	v_cvt_pk_bf16_f32 v184, v96, v97
	v_cvt_pk_bf16_f32 v185, v98, v99
	ds_read_b64_tr_b16 v[36:37], v136 offset:0
	v_add_f32_e32 v24, v76, v92
	v_add_f32_e32 v25, v77, v93
	v_add_f32_e32 v26, v26, v28
	v_add_f32_e32 v27, v27, v29
	ds_read_b64_tr_b16 v[38:39], v136 offset:0x800
	v_add_f32_e32 v22, v78, v94
	v_add_f32_e32 v23, v79, v95
	v_add_f32_e32 v24, v24, v26
	v_add_f32_e32 v25, v25, v27
	ds_read_b64_tr_b16 v[40:41], v136 offset:0x1000
	v_add_f32_e32 v20, v80, v96
	v_add_f32_e32 v21, v81, v97
	v_add_f32_e32 v22, v22, v24
	v_add_f32_e32 v23, v23, v25
	ds_read_b64_tr_b16 v[42:43], v136 offset:0x1800
	v_add_f32_e32 v0, v82, v98
	v_add_f32_e32 v1, v83, v99
	v_add_f32_e32 v20, v20, v22
	v_add_f32_e32 v21, v21, v23
	ds_read_b64_tr_b16 v[44:45], v136 offset:0x2000
	ds_read_b64_tr_b16 v[46:47], v136 offset:0x2800
	ds_read_b64_tr_b16 v[48:49], v136 offset:0x3000
	ds_read_b64_tr_b16 v[50:51], v136 offset:0x3800
	s_waitcnt lgkmcnt(0)
	s_nop 0
	v_add_f32_e32 v0, v0, v20
	v_add_f32_e32 v1, v1, v21
	v_permlane32_swap_b32_e32 v170, v172
	v_pk_add_f32 v[0:1], v[0:1], v[0:1] op_sel:[0,1] op_sel_hi:[1,0]
	v_permlane32_swap_b32_e32 v171, v173
	v_mov_b32_e32 v1, v0
	s_nop 1
	v_permlane32_swap_b32_e32 v0, v1
	v_add_f32_e32 v138, v0, v1
	v_fmac_f32_e32 v138, 0, v155
	v_permlane32_swap_b32_e32 v174, v176
	v_permlane32_swap_b32_e32 v175, v177
	v_permlane32_swap_b32_e32 v178, v180
	v_permlane32_swap_b32_e32 v179, v181
	v_permlane32_swap_b32_e32 v182, v184
	v_permlane32_swap_b32_e32 v183, v185
	v_mfma_f32_32x32x16_bf16 v[20:35], v[170:173], v[36:39], v[4:19]
	ds_read_b64_tr_b16 v[52:53], v136 offset:0x200
	ds_read_b64_tr_b16 v[54:55], v136 offset:0xa00
	ds_read_b64_tr_b16 v[56:57], v136 offset:0x1200
	ds_read_b64_tr_b16 v[58:59], v136 offset:0x1a00
	ds_read_b64_tr_b16 v[60:61], v136 offset:0x2200
	ds_read_b64_tr_b16 v[62:63], v136 offset:0x2a00
	ds_read_b64_tr_b16 v[64:65], v136 offset:0x3200
	v_mfma_f32_32x32x16_bf16 v[20:35], v[174:177], v[40:43], v[20:35]
	ds_read_b64_tr_b16 v[66:67], v136 offset:0x3a00
	s_waitcnt lgkmcnt(0)
	v_mfma_f32_32x32x16_bf16 v[20:35], v[178:181], v[44:47], v[20:35]
	v_mfma_f32_32x32x16_bf16 v[20:35], v[182:185], v[48:51], v[20:35]
	v_mfma_f32_32x32x16_bf16 v[36:51], v[170:173], v[52:55], v[4:19]
	ds_read_b64_tr_b16 v[186:187], v136 offset:0x400
	ds_read_b64_tr_b16 v[188:189], v136 offset:0xc00
	ds_read_b64_tr_b16 v[190:191], v136 offset:0x1400
	ds_read_b64_tr_b16 v[192:193], v136 offset:0x1c00
	ds_read_b64_tr_b16 v[194:195], v136 offset:0x2400
	ds_read_b64_tr_b16 v[196:197], v136 offset:0x2c00
	ds_read_b64_tr_b16 v[198:199], v136 offset:0x3400
	v_mfma_f32_32x32x16_bf16 v[36:51], v[174:177], v[56:59], v[36:51]
	ds_read_b64_tr_b16 v[200:201], v136 offset:0x3c00
	s_waitcnt lgkmcnt(0)
	v_mfma_f32_32x32x16_bf16 v[36:51], v[178:181], v[60:63], v[36:51]
	v_mfma_f32_32x32x16_bf16 v[36:51], v[182:185], v[64:67], v[36:51]
	v_mfma_f32_32x32x16_bf16 v[52:67], v[170:173], v[186:189], v[4:19]
	ds_read_b64_tr_b16 v[186:187], v136 offset:0x600
	ds_read_b64_tr_b16 v[188:189], v136 offset:0xe00
	v_mfma_f32_32x32x16_bf16 v[52:67], v[174:177], v[190:193], v[52:67]
	ds_read_b64_tr_b16 v[190:191], v136 offset:0x1600
	ds_read_b64_tr_b16 v[192:193], v136 offset:0x1e00
	v_mfma_f32_32x32x16_bf16 v[52:67], v[178:181], v[194:197], v[52:67]
	ds_read_b64_tr_b16 v[194:195], v136 offset:0x2600
	ds_read_b64_tr_b16 v[196:197], v136 offset:0x2e00
	v_mfma_f32_32x32x16_bf16 v[52:67], v[182:185], v[198:201], v[52:67]
	ds_read_b64_tr_b16 v[198:199], v136 offset:0x3600
	ds_read_b64_tr_b16 v[200:201], v136 offset:0x3e00
	s_waitcnt lgkmcnt(0)
	v_mfma_f32_32x32x16_bf16 v[4:19], v[170:173], v[186:189], v[4:19]
	v_mfma_f32_32x32x16_bf16 v[4:19], v[174:177], v[190:193], v[4:19]
	v_mfma_f32_32x32x16_bf16 v[4:19], v[178:181], v[194:197], v[4:19]
	v_mfma_f32_32x32x16_bf16 v[4:19], v[182:185], v[198:201], v[4:19]

.LBB0_1831:
	v_mul_f32_e32 v2, 0xbe0293ee, v154
	v_cndmask_b32_e64 v2, v168, v2, s[98:99]
	v_fma_f32 v68, v68, s2, v2
	v_fma_f32 v69, v69, s2, v2
	v_fma_f32 v70, v70, s2, v2
	v_fma_f32 v71, v71, s2, v2
	v_fma_f32 v72, v72, s2, v2
	v_fma_f32 v73, v73, s2, v2
	v_fma_f32 v74, v74, s2, v2
	v_fma_f32 v75, v75, s2, v2
	v_fma_f32 v76, v76, s2, v2
	v_fma_f32 v77, v77, s2, v2
	v_fma_f32 v78, v78, s2, v2
	v_fma_f32 v79, v79, s2, v2
	v_fma_f32 v80, v80, s2, v2
	v_fma_f32 v81, v81, s2, v2
	v_fma_f32 v82, v82, s2, v2
	v_fma_f32 v83, v83, s2, v2
	v_exp_f32_e32 v68, v68
	v_exp_f32_e32 v69, v69
	v_exp_f32_e32 v70, v70
	v_exp_f32_e32 v71, v71
	v_exp_f32_e32 v72, v72
	v_exp_f32_e32 v73, v73
	v_exp_f32_e32 v74, v74
	v_exp_f32_e32 v75, v75
	v_exp_f32_e32 v76, v76
	v_exp_f32_e32 v77, v77
	v_exp_f32_e32 v78, v78
	v_exp_f32_e32 v79, v79
	v_exp_f32_e32 v80, v80
	v_exp_f32_e32 v81, v81
	v_exp_f32_e32 v82, v82
	v_exp_f32_e32 v83, v83
	v_fma_f32 v86, v86, s2, v2
	v_fma_f32 v87, v87, s2, v2
	v_fma_f32 v84, v84, s2, v2
	v_fma_f32 v85, v85, s2, v2
	v_fma_f32 v88, v88, s2, v2
	v_fma_f32 v89, v89, s2, v2
	v_fma_f32 v90, v90, s2, v2
	v_fma_f32 v91, v91, s2, v2
	v_fma_f32 v92, v92, s2, v2
	v_fma_f32 v93, v93, s2, v2
	v_fma_f32 v94, v94, s2, v2
	v_fma_f32 v95, v95, s2, v2
	v_fma_f32 v96, v96, s2, v2
	v_fma_f32 v97, v97, s2, v2
	v_fma_f32 v98, v98, s2, v2
	v_fma_f32 v99, v99, s2, v2

.LBB0_1838:
	s_andn2_b64 vcc, exec, s[12:13]
	s_cbranch_vccnz .LBB0_1844
	v_cmp_gt_f32_e32 vcc, 1.0, v155
	s_cbranch_vccz .LBB0_1843
	s_and_saveexec_b64 s[4:5], s[8:9]
	ds_write_b32 v141, v155
	s_or_b64 exec, exec, s[4:5]
	v_readlane_b32 s1, v254, 32
	s_waitcnt lgkmcnt(0)
	s_nop 1
	v_add_u32_e32 v1, s1, v140
	v_readlane_b32 s1, v254, 33
	s_nop 1
	v_add_u32_e32 v2, s1, v140
	v_readlane_b32 s1, v254, 31
	ds_read_b128 v[170:173], v1
	ds_read_b128 v[174:177], v2
	v_add_u32_e32 v1, s1, v140
	v_readlane_b32 s1, v254, 30
	ds_read_b128 v[178:181], v1
	s_waitcnt lgkmcnt(2)
	v_mul_f32_e32 v28, v28, v170
	v_mul_f32_e32 v29, v29, v171
	v_add_u32_e32 v1, s1, v140
	ds_read_b128 v[182:185], v1
	s_waitcnt lgkmcnt(2)
	v_mul_f32_e32 v32, v32, v174
	v_mul_f32_e32 v33, v33, v175
	s_waitcnt lgkmcnt(1)
	v_mul_f32_e32 v24, v24, v178
	v_mul_f32_e32 v25, v25, v179
	v_mul_f32_e32 v34, v34, v176
	v_mul_f32_e32 v35, v35, v177
	v_mul_f32_e32 v30, v30, v172
	v_mul_f32_e32 v31, v31, v173
	v_mul_f32_e32 v26, v26, v180
	v_mul_f32_e32 v27, v27, v181
	s_waitcnt lgkmcnt(0)
	v_mul_f32_e32 v22, v22, v184
	v_mul_f32_e32 v23, v23, v185
	v_mul_f32_e32 v20, v20, v182
	v_mul_f32_e32 v21, v21, v183
	v_mul_f32_e32 v48, v48, v174
	v_mul_f32_e32 v49, v49, v175
	v_mul_f32_e32 v44, v44, v170
	v_mul_f32_e32 v45, v45, v171
	v_mul_f32_e32 v40, v40, v178
	v_mul_f32_e32 v41, v41, v179
	v_mul_f32_e32 v50, v50, v176
	v_mul_f32_e32 v51, v51, v177
	v_mul_f32_e32 v46, v46, v172
	v_mul_f32_e32 v47, v47, v173
	v_mul_f32_e32 v42, v42, v180
	v_mul_f32_e32 v43, v43, v181
	v_mul_f32_e32 v38, v38, v184
	v_mul_f32_e32 v39, v39, v185
	v_mul_f32_e32 v36, v36, v182
	v_mul_f32_e32 v37, v37, v183
	v_mul_f32_e32 v64, v64, v174
	v_mul_f32_e32 v65, v65, v175
	v_mul_f32_e32 v60, v60, v170
	v_mul_f32_e32 v61, v61, v171
	v_mul_f32_e32 v56, v56, v178
	v_mul_f32_e32 v57, v57, v179
	v_mul_f32_e32 v66, v66, v176
	v_mul_f32_e32 v67, v67, v177
	v_mul_f32_e32 v62, v62, v172
	v_mul_f32_e32 v63, v63, v173
	v_mul_f32_e32 v58, v58, v180
	v_mul_f32_e32 v59, v59, v181
	v_mul_f32_e32 v54, v54, v184
	v_mul_f32_e32 v55, v55, v185
	v_mul_f32_e32 v52, v52, v182
	v_mul_f32_e32 v53, v53, v183
	v_mul_f32_e32 v16, v16, v174
	v_mul_f32_e32 v17, v17, v175
	v_mul_f32_e32 v12, v12, v170
	v_mul_f32_e32 v13, v13, v171
	v_mul_f32_e32 v8, v8, v178
	v_mul_f32_e32 v9, v9, v179
	v_mul_f32_e32 v18, v18, v176
	v_mul_f32_e32 v19, v19, v177
	v_mul_f32_e32 v14, v14, v172
	v_mul_f32_e32 v15, v15, v173
	v_mul_f32_e32 v10, v10, v180
	v_mul_f32_e32 v11, v11, v181
	v_mul_f32_e32 v6, v6, v184
	v_mul_f32_e32 v7, v7, v185
	v_mul_f32_e32 v4, v4, v182
	v_mul_f32_e32 v5, v5, v183
.LBB0_1843:
	v_exp_f32_e32 v84, v84
	v_exp_f32_e32 v85, v85
	v_exp_f32_e32 v86, v86
	v_exp_f32_e32 v87, v87
	v_exp_f32_e32 v88, v88
	v_exp_f32_e32 v89, v89
	v_exp_f32_e32 v90, v90
	v_exp_f32_e32 v91, v91
	v_exp_f32_e32 v92, v92
	v_exp_f32_e32 v93, v93
	v_add_f32_e32 v184, v68, v84
	v_add_f32_e32 v185, v69, v85
	v_exp_f32_e32 v94, v94
	v_exp_f32_e32 v95, v95
	v_add_f32_e32 v182, v70, v86
	v_add_f32_e32 v183, v71, v87
	v_add_f32_e32 v184, 0, v184
	v_add_f32_e32 v185, 0, v185
	v_exp_f32_e32 v96, v96
	v_exp_f32_e32 v97, v97
	v_add_f32_e32 v180, v72, v88
	v_add_f32_e32 v181, v73, v89
	v_add_f32_e32 v182, v182, v184
	v_add_f32_e32 v183, v183, v185
	v_exp_f32_e32 v98, v98
	v_exp_f32_e32 v99, v99
	v_add_f32_e32 v178, v74, v90
	v_add_f32_e32 v179, v75, v91
	v_add_f32_e32 v180, v180, v182
	v_add_f32_e32 v181, v181, v183
	v_add_f32_e32 v176, v76, v92
	v_add_f32_e32 v177, v77, v93
	v_add_f32_e32 v178, v178, v180
	v_add_f32_e32 v179, v179, v181
	v_add_f32_e32 v174, v78, v94
	v_add_f32_e32 v175, v79, v95
	v_add_f32_e32 v176, v176, v178
	v_add_f32_e32 v177, v177, v179
	v_add_f32_e32 v172, v80, v96
	v_add_f32_e32 v173, v81, v97
	v_add_f32_e32 v174, v174, v176
	v_add_f32_e32 v175, v175, v177
	v_add_f32_e32 v170, v82, v98
	v_add_f32_e32 v171, v83, v99
	v_add_f32_e32 v172, v172, v174
	v_add_f32_e32 v173, v173, v175
	s_nop 0
	v_add_f32_e32 v170, v170, v172
	v_add_f32_e32 v171, v171, v173
	s_nop 0
	v_pk_add_f32 v[170:171], v[170:171], v[170:171] op_sel:[0,1] op_sel_hi:[1,0]
	s_nop 0
	v_mov_b32_e32 v1, v170
	s_nop 1
	v_permlane32_swap_b32_e32 v170, v1
	v_add_f32_e32 v1, v170, v1
	v_cvt_pk_bf16_f32 v170, v68, v69
	v_cvt_pk_bf16_f32 v171, v70, v71
	v_cvt_pk_bf16_f32 v172, v72, v73
	v_cvt_pk_bf16_f32 v173, v74, v75
	v_cvt_pk_bf16_f32 v174, v76, v77
	v_cvt_pk_bf16_f32 v175, v78, v79
	v_cvt_pk_bf16_f32 v176, v80, v81
	v_cvt_pk_bf16_f32 v177, v82, v83
	v_cvt_pk_bf16_f32 v178, v84, v85
	v_cvt_pk_bf16_f32 v179, v86, v87
	v_cvt_pk_bf16_f32 v180, v88, v89
	v_cvt_pk_bf16_f32 v181, v90, v91
	v_cvt_pk_bf16_f32 v182, v92, v93
	v_cvt_pk_bf16_f32 v183, v94, v95
	v_cvt_pk_bf16_f32 v184, v96, v97
	v_cvt_pk_bf16_f32 v185, v98, v99
	ds_read_b64_tr_b16 v[186:187], v0 offset:0
	ds_read_b64_tr_b16 v[188:189], v0 offset:0x800
	ds_read_b64_tr_b16 v[190:191], v0 offset:0x1000
	ds_read_b64_tr_b16 v[192:193], v0 offset:0x1800
	ds_read_b64_tr_b16 v[194:195], v0 offset:0x2000
	ds_read_b64_tr_b16 v[196:197], v0 offset:0x2800
	ds_read_b64_tr_b16 v[198:199], v0 offset:0x3000
	ds_read_b64_tr_b16 v[200:201], v0 offset:0x3800
	s_waitcnt lgkmcnt(0)
	v_fmac_f32_e32 v1, v138, v155
	v_permlane32_swap_b32_e32 v170, v172
	v_permlane32_swap_b32_e32 v171, v173
	v_permlane32_swap_b32_e32 v174, v176
	v_permlane32_swap_b32_e32 v175, v177
	v_permlane32_swap_b32_e32 v178, v180
	v_permlane32_swap_b32_e32 v179, v181
	v_permlane32_swap_b32_e32 v182, v184
	v_permlane32_swap_b32_e32 v183, v185
	v_mfma_f32_32x32x16_bf16 v[20:35], v[170:173], v[186:189], v[20:35]
	ds_read_b64_tr_b16 v[186:187], v0 offset:0x200
	ds_read_b64_tr_b16 v[188:189], v0 offset:0xa00
	v_mfma_f32_32x32x16_bf16 v[20:35], v[174:177], v[190:193], v[20:35]
	ds_read_b64_tr_b16 v[190:191], v0 offset:0x1200
	ds_read_b64_tr_b16 v[192:193], v0 offset:0x1a00
	v_mfma_f32_32x32x16_bf16 v[20:35], v[178:181], v[194:197], v[20:35]
	ds_read_b64_tr_b16 v[194:195], v0 offset:0x2200
	ds_read_b64_tr_b16 v[196:197], v0 offset:0x2a00
	v_mfma_f32_32x32x16_bf16 v[20:35], v[182:185], v[198:201], v[20:35]
	ds_read_b64_tr_b16 v[198:199], v0 offset:0x3200
	ds_read_b64_tr_b16 v[200:201], v0 offset:0x3a00
	s_waitcnt lgkmcnt(0)
	v_mfma_f32_32x32x16_bf16 v[36:51], v[170:173], v[186:189], v[36:51]
	ds_read_b64_tr_b16 v[186:187], v0 offset:0x400
	ds_read_b64_tr_b16 v[188:189], v0 offset:0xc00
	v_mfma_f32_32x32x16_bf16 v[36:51], v[174:177], v[190:193], v[36:51]
	ds_read_b64_tr_b16 v[190:191], v0 offset:0x1400
	ds_read_b64_tr_b16 v[192:193], v0 offset:0x1c00
	v_mfma_f32_32x32x16_bf16 v[36:51], v[178:181], v[194:197], v[36:51]
	ds_read_b64_tr_b16 v[194:195], v0 offset:0x2400
	ds_read_b64_tr_b16 v[196:197], v0 offset:0x2c00
	v_mfma_f32_32x32x16_bf16 v[36:51], v[182:185], v[198:201], v[36:51]
	ds_read_b64_tr_b16 v[198:199], v0 offset:0x3400
	ds_read_b64_tr_b16 v[200:201], v0 offset:0x3c00
	s_waitcnt lgkmcnt(0)
	v_mfma_f32_32x32x16_bf16 v[52:67], v[170:173], v[186:189], v[52:67]
	ds_read_b64_tr_b16 v[186:187], v0 offset:0x600
	ds_read_b64_tr_b16 v[188:189], v0 offset:0xe00
	v_mfma_f32_32x32x16_bf16 v[52:67], v[174:177], v[190:193], v[52:67]
	ds_read_b64_tr_b16 v[190:191], v0 offset:0x1600
	ds_read_b64_tr_b16 v[192:193], v0 offset:0x1e00
	v_mfma_f32_32x32x16_bf16 v[52:67], v[178:181], v[194:197], v[52:67]
	ds_read_b64_tr_b16 v[194:195], v0 offset:0x2600
	ds_read_b64_tr_b16 v[196:197], v0 offset:0x2e00
	v_mfma_f32_32x32x16_bf16 v[52:67], v[182:185], v[198:201], v[52:67]
	ds_read_b64_tr_b16 v[198:199], v0 offset:0x3600
	ds_read_b64_tr_b16 v[200:201], v0 offset:0x3e00
	s_waitcnt lgkmcnt(0)
	v_mfma_f32_32x32x16_bf16 v[4:19], v[170:173], v[186:189], v[4:19]
	v_mov_b32_e32 v138, v1
	v_mfma_f32_32x32x16_bf16 v[4:19], v[174:177], v[190:193], v[4:19]
	v_mfma_f32_32x32x16_bf16 v[4:19], v[178:181], v[194:197], v[4:19]
	v_mfma_f32_32x32x16_bf16 v[4:19], v[182:185], v[198:201], v[4:19]

.LBB0_1864:
	s_andn2_b64 vcc, exec, s[18:19]
	s_cbranch_vccnz .LBB0_1870
	v_cmp_gt_f32_e32 vcc, 1.0, v155
	s_cbranch_vccz .LBB0_1869
	s_and_saveexec_b64 s[4:5], s[8:9]
	ds_write_b32 v141, v155
	s_or_b64 exec, exec, s[4:5]
	v_readlane_b32 s4, v254, 32
	s_waitcnt lgkmcnt(0)
	s_nop 1
	v_add_u32_e32 v1, s4, v140
	v_readlane_b32 s4, v254, 33
	s_nop 1
	v_add_u32_e32 v2, s4, v140
	v_readlane_b32 s4, v254, 31
	ds_read_b128 v[170:173], v1
	ds_read_b128 v[174:177], v2
	v_add_u32_e32 v1, s4, v140
	v_readlane_b32 s4, v254, 30
	ds_read_b128 v[178:181], v1
	s_waitcnt lgkmcnt(2)
	v_mul_f32_e32 v28, v28, v170
	v_mul_f32_e32 v29, v29, v171
	v_add_u32_e32 v1, s4, v140
	ds_read_b128 v[182:185], v1
	s_waitcnt lgkmcnt(2)
	v_mul_f32_e32 v32, v32, v174
	v_mul_f32_e32 v33, v33, v175
	s_waitcnt lgkmcnt(1)
	v_mul_f32_e32 v24, v24, v178
	v_mul_f32_e32 v25, v25, v179
	v_mul_f32_e32 v34, v34, v176
	v_mul_f32_e32 v35, v35, v177
	v_mul_f32_e32 v30, v30, v172
	v_mul_f32_e32 v31, v31, v173
	v_mul_f32_e32 v26, v26, v180
	v_mul_f32_e32 v27, v27, v181
	s_waitcnt lgkmcnt(0)
	v_mul_f32_e32 v22, v22, v184
	v_mul_f32_e32 v23, v23, v185
	v_mul_f32_e32 v20, v20, v182
	v_mul_f32_e32 v21, v21, v183
	v_mul_f32_e32 v48, v48, v174
	v_mul_f32_e32 v49, v49, v175
	v_mul_f32_e32 v44, v44, v170
	v_mul_f32_e32 v45, v45, v171
	v_mul_f32_e32 v40, v40, v178
	v_mul_f32_e32 v41, v41, v179
	v_mul_f32_e32 v50, v50, v176
	v_mul_f32_e32 v51, v51, v177
	v_mul_f32_e32 v46, v46, v172
	v_mul_f32_e32 v47, v47, v173
	v_mul_f32_e32 v42, v42, v180
	v_mul_f32_e32 v43, v43, v181
	v_mul_f32_e32 v38, v38, v184
	v_mul_f32_e32 v39, v39, v185
	v_mul_f32_e32 v36, v36, v182
	v_mul_f32_e32 v37, v37, v183
	v_mul_f32_e32 v64, v64, v174
	v_mul_f32_e32 v65, v65, v175
	v_mul_f32_e32 v60, v60, v170
	v_mul_f32_e32 v61, v61, v171
	v_mul_f32_e32 v56, v56, v178
	v_mul_f32_e32 v57, v57, v179
	v_mul_f32_e32 v66, v66, v176
	v_mul_f32_e32 v67, v67, v177
	v_mul_f32_e32 v62, v62, v172
	v_mul_f32_e32 v63, v63, v173
	v_mul_f32_e32 v58, v58, v180
	v_mul_f32_e32 v59, v59, v181
	v_mul_f32_e32 v54, v54, v184
	v_mul_f32_e32 v55, v55, v185
	v_mul_f32_e32 v52, v52, v182
	v_mul_f32_e32 v53, v53, v183
	v_mul_f32_e32 v16, v16, v174
	v_mul_f32_e32 v17, v17, v175
	v_mul_f32_e32 v12, v12, v170
	v_mul_f32_e32 v13, v13, v171
	v_mul_f32_e32 v8, v8, v178
	v_mul_f32_e32 v9, v9, v179
	v_mul_f32_e32 v18, v18, v176
	v_mul_f32_e32 v19, v19, v177
	v_mul_f32_e32 v14, v14, v172
	v_mul_f32_e32 v15, v15, v173
	v_mul_f32_e32 v10, v10, v180
	v_mul_f32_e32 v11, v11, v181
	v_mul_f32_e32 v6, v6, v184
	v_mul_f32_e32 v7, v7, v185
	v_mul_f32_e32 v4, v4, v182
	v_mul_f32_e32 v5, v5, v183
.LBB0_1869:
	v_exp_f32_e32 v84, v84
	v_exp_f32_e32 v85, v85
	v_exp_f32_e32 v86, v86
	v_exp_f32_e32 v87, v87
	v_exp_f32_e32 v88, v88
	v_exp_f32_e32 v89, v89
	v_exp_f32_e32 v90, v90
	v_exp_f32_e32 v91, v91
	v_exp_f32_e32 v92, v92
	v_exp_f32_e32 v93, v93
	v_add_f32_e32 v184, v68, v84
	v_add_f32_e32 v185, v69, v85
	v_exp_f32_e32 v94, v94
	v_exp_f32_e32 v95, v95
	v_add_f32_e32 v182, v70, v86
	v_add_f32_e32 v183, v71, v87
	v_add_f32_e32 v184, 0, v184
	v_add_f32_e32 v185, 0, v185
	v_exp_f32_e32 v96, v96
	v_exp_f32_e32 v97, v97
	v_add_f32_e32 v180, v72, v88
	v_add_f32_e32 v181, v73, v89
	v_add_f32_e32 v182, v182, v184
	v_add_f32_e32 v183, v183, v185
	v_exp_f32_e32 v98, v98
	v_exp_f32_e32 v99, v99
	v_add_f32_e32 v178, v74, v90
	v_add_f32_e32 v179, v75, v91
	v_add_f32_e32 v180, v180, v182
	v_add_f32_e32 v181, v181, v183
	v_add_f32_e32 v176, v76, v92
	v_add_f32_e32 v177, v77, v93
	v_add_f32_e32 v178, v178, v180
	v_add_f32_e32 v179, v179, v181
	v_add_f32_e32 v174, v78, v94
	v_add_f32_e32 v175, v79, v95
	v_add_f32_e32 v176, v176, v178
	v_add_f32_e32 v177, v177, v179
	v_add_f32_e32 v172, v80, v96
	v_add_f32_e32 v173, v81, v97
	v_add_f32_e32 v174, v174, v176
	v_add_f32_e32 v175, v175, v177
	v_add_f32_e32 v170, v82, v98
	v_add_f32_e32 v171, v83, v99
	v_add_f32_e32 v172, v172, v174
	v_add_f32_e32 v173, v173, v175
	s_nop 0
	v_add_f32_e32 v170, v170, v172
	v_add_f32_e32 v171, v171, v173
	s_nop 0
	v_pk_add_f32 v[170:171], v[170:171], v[170:171] op_sel:[0,1] op_sel_hi:[1,0]
	s_nop 0
	v_mov_b32_e32 v1, v170
	s_nop 1
	v_permlane32_swap_b32_e32 v170, v1
	v_add_f32_e32 v1, v170, v1
	v_cvt_pk_bf16_f32 v170, v68, v69
	v_cvt_pk_bf16_f32 v171, v70, v71
	v_cvt_pk_bf16_f32 v172, v72, v73
	v_cvt_pk_bf16_f32 v173, v74, v75
	v_cvt_pk_bf16_f32 v174, v76, v77
	v_cvt_pk_bf16_f32 v175, v78, v79
	v_cvt_pk_bf16_f32 v176, v80, v81
	v_cvt_pk_bf16_f32 v177, v82, v83
	v_cvt_pk_bf16_f32 v178, v84, v85
	v_cvt_pk_bf16_f32 v179, v86, v87
	v_cvt_pk_bf16_f32 v180, v88, v89
	v_cvt_pk_bf16_f32 v181, v90, v91
	v_cvt_pk_bf16_f32 v182, v92, v93
	v_cvt_pk_bf16_f32 v183, v94, v95
	v_cvt_pk_bf16_f32 v184, v96, v97
	v_cvt_pk_bf16_f32 v185, v98, v99
	ds_read_b64_tr_b16 v[186:187], v136 offset:0
	ds_read_b64_tr_b16 v[188:189], v136 offset:0x800
	ds_read_b64_tr_b16 v[190:191], v136 offset:0x1000
	ds_read_b64_tr_b16 v[192:193], v136 offset:0x1800
	ds_read_b64_tr_b16 v[194:195], v136 offset:0x2000
	ds_read_b64_tr_b16 v[196:197], v136 offset:0x2800
	ds_read_b64_tr_b16 v[198:199], v136 offset:0x3000
	ds_read_b64_tr_b16 v[200:201], v136 offset:0x3800
	s_waitcnt lgkmcnt(0)
	v_fmac_f32_e32 v1, v138, v155
	v_permlane32_swap_b32_e32 v170, v172
	v_permlane32_swap_b32_e32 v171, v173
	v_permlane32_swap_b32_e32 v174, v176
	v_permlane32_swap_b32_e32 v175, v177
	v_permlane32_swap_b32_e32 v178, v180
	v_permlane32_swap_b32_e32 v179, v181
	v_permlane32_swap_b32_e32 v182, v184
	v_permlane32_swap_b32_e32 v183, v185
	v_mfma_f32_32x32x16_bf16 v[20:35], v[170:173], v[186:189], v[20:35]
	ds_read_b64_tr_b16 v[186:187], v136 offset:0x200
	ds_read_b64_tr_b16 v[188:189], v136 offset:0xa00
	v_mfma_f32_32x32x16_bf16 v[20:35], v[174:177], v[190:193], v[20:35]
	ds_read_b64_tr_b16 v[190:191], v136 offset:0x1200
	ds_read_b64_tr_b16 v[192:193], v136 offset:0x1a00
	v_mfma_f32_32x32x16_bf16 v[20:35], v[178:181], v[194:197], v[20:35]
	ds_read_b64_tr_b16 v[194:195], v136 offset:0x2200
	ds_read_b64_tr_b16 v[196:197], v136 offset:0x2a00
	v_mfma_f32_32x32x16_bf16 v[20:35], v[182:185], v[198:201], v[20:35]
	ds_read_b64_tr_b16 v[198:199], v136 offset:0x3200
	ds_read_b64_tr_b16 v[200:201], v136 offset:0x3a00
	s_waitcnt lgkmcnt(0)
	v_mfma_f32_32x32x16_bf16 v[36:51], v[170:173], v[186:189], v[36:51]
	ds_read_b64_tr_b16 v[186:187], v136 offset:0x400
	ds_read_b64_tr_b16 v[188:189], v136 offset:0xc00
	v_mfma_f32_32x32x16_bf16 v[36:51], v[174:177], v[190:193], v[36:51]
	ds_read_b64_tr_b16 v[190:191], v136 offset:0x1400
	ds_read_b64_tr_b16 v[192:193], v136 offset:0x1c00
	v_mfma_f32_32x32x16_bf16 v[36:51], v[178:181], v[194:197], v[36:51]
	ds_read_b64_tr_b16 v[194:195], v136 offset:0x2400
	ds_read_b64_tr_b16 v[196:197], v136 offset:0x2c00
	v_mfma_f32_32x32x16_bf16 v[36:51], v[182:185], v[198:201], v[36:51]
	ds_read_b64_tr_b16 v[198:199], v136 offset:0x3400
	ds_read_b64_tr_b16 v[200:201], v136 offset:0x3c00
	s_waitcnt lgkmcnt(0)
	v_mfma_f32_32x32x16_bf16 v[52:67], v[170:173], v[186:189], v[52:67]
	ds_read_b64_tr_b16 v[186:187], v136 offset:0x600
	ds_read_b64_tr_b16 v[188:189], v136 offset:0xe00
	v_mfma_f32_32x32x16_bf16 v[52:67], v[174:177], v[190:193], v[52:67]
	ds_read_b64_tr_b16 v[190:191], v136 offset:0x1600
	ds_read_b64_tr_b16 v[192:193], v136 offset:0x1e00
	v_mfma_f32_32x32x16_bf16 v[52:67], v[178:181], v[194:197], v[52:67]
	ds_read_b64_tr_b16 v[194:195], v136 offset:0x2600
	ds_read_b64_tr_b16 v[196:197], v136 offset:0x2e00
	v_mfma_f32_32x32x16_bf16 v[52:67], v[182:185], v[198:201], v[52:67]
	ds_read_b64_tr_b16 v[198:199], v136 offset:0x3600
	ds_read_b64_tr_b16 v[200:201], v136 offset:0x3e00
	s_waitcnt lgkmcnt(0)
	v_mfma_f32_32x32x16_bf16 v[4:19], v[170:173], v[186:189], v[4:19]
	v_mov_b32_e32 v138, v1
	v_mfma_f32_32x32x16_bf16 v[4:19], v[174:177], v[190:193], v[4:19]
	v_mfma_f32_32x32x16_bf16 v[4:19], v[178:181], v[194:197], v[4:19]
	v_mfma_f32_32x32x16_bf16 v[4:19], v[182:185], v[198:201], v[4:19]

.LBB0_1888:
	s_andn2_b64 vcc, exec, s[12:13]
	s_cbranch_vccnz .LBB0_1894
	v_cmp_gt_f32_e32 vcc, 1.0, v155
	s_cbranch_vccz .LBB0_1893
	s_and_saveexec_b64 s[4:5], s[8:9]
	ds_write_b32 v141, v155
	s_or_b64 exec, exec, s[4:5]
	v_readlane_b32 s3, v254, 32
	s_waitcnt lgkmcnt(0)
	s_nop 1
	v_add_u32_e32 v1, s3, v140
	v_readlane_b32 s3, v254, 33
	s_nop 1
	v_add_u32_e32 v2, s3, v140
	v_readlane_b32 s3, v254, 31
	ds_read_b128 v[170:173], v1
	ds_read_b128 v[174:177], v2
	v_add_u32_e32 v1, s3, v140
	v_readlane_b32 s3, v254, 30
	ds_read_b128 v[178:181], v1
	s_waitcnt lgkmcnt(2)
	v_mul_f32_e32 v28, v28, v170
	v_mul_f32_e32 v29, v29, v171
	v_add_u32_e32 v1, s3, v140
	ds_read_b128 v[182:185], v1
	s_waitcnt lgkmcnt(2)
	v_mul_f32_e32 v32, v32, v174
	v_mul_f32_e32 v33, v33, v175
	s_waitcnt lgkmcnt(1)
	v_mul_f32_e32 v24, v24, v178
	v_mul_f32_e32 v25, v25, v179
	v_mul_f32_e32 v34, v34, v176
	v_mul_f32_e32 v35, v35, v177
	v_mul_f32_e32 v30, v30, v172
	v_mul_f32_e32 v31, v31, v173
	v_mul_f32_e32 v26, v26, v180
	v_mul_f32_e32 v27, v27, v181
	s_waitcnt lgkmcnt(0)
	v_mul_f32_e32 v22, v22, v184
	v_mul_f32_e32 v23, v23, v185
	v_mul_f32_e32 v20, v20, v182
	v_mul_f32_e32 v21, v21, v183
	v_mul_f32_e32 v48, v48, v174
	v_mul_f32_e32 v49, v49, v175
	v_mul_f32_e32 v44, v44, v170
	v_mul_f32_e32 v45, v45, v171
	v_mul_f32_e32 v40, v40, v178
	v_mul_f32_e32 v41, v41, v179
	v_mul_f32_e32 v50, v50, v176
	v_mul_f32_e32 v51, v51, v177
	v_mul_f32_e32 v46, v46, v172
	v_mul_f32_e32 v47, v47, v173
	v_mul_f32_e32 v42, v42, v180
	v_mul_f32_e32 v43, v43, v181
	v_mul_f32_e32 v38, v38, v184
	v_mul_f32_e32 v39, v39, v185
	v_mul_f32_e32 v36, v36, v182
	v_mul_f32_e32 v37, v37, v183
	v_mul_f32_e32 v64, v64, v174
	v_mul_f32_e32 v65, v65, v175
	v_mul_f32_e32 v60, v60, v170
	v_mul_f32_e32 v61, v61, v171
	v_mul_f32_e32 v56, v56, v178
	v_mul_f32_e32 v57, v57, v179
	v_mul_f32_e32 v66, v66, v176
	v_mul_f32_e32 v67, v67, v177
	v_mul_f32_e32 v62, v62, v172
	v_mul_f32_e32 v63, v63, v173
	v_mul_f32_e32 v58, v58, v180
	v_mul_f32_e32 v59, v59, v181
	v_mul_f32_e32 v54, v54, v184
	v_mul_f32_e32 v55, v55, v185
	v_mul_f32_e32 v52, v52, v182
	v_mul_f32_e32 v53, v53, v183
	v_mul_f32_e32 v16, v16, v174
	v_mul_f32_e32 v17, v17, v175
	v_mul_f32_e32 v12, v12, v170
	v_mul_f32_e32 v13, v13, v171
	v_mul_f32_e32 v8, v8, v178
	v_mul_f32_e32 v9, v9, v179
	v_mul_f32_e32 v18, v18, v176
	v_mul_f32_e32 v19, v19, v177
	v_mul_f32_e32 v14, v14, v172
	v_mul_f32_e32 v15, v15, v173
	v_mul_f32_e32 v10, v10, v180
	v_mul_f32_e32 v11, v11, v181
	v_mul_f32_e32 v6, v6, v184
	v_mul_f32_e32 v7, v7, v185
	v_mul_f32_e32 v4, v4, v182
	v_mul_f32_e32 v5, v5, v183

.LBB0_1923:
	v_readlane_b32 s1, v254, 30
	v_cmp_eq_u32_e64 s[78:79], 0, v139
	v_lshlrev_b32_e32 v175, 4, v139
	v_lshl_add_u32 v174, v138, 2, s1
	v_cmp_gt_f32_e32 vcc, 1.0, v1
	s_cbranch_vccz .LBB0_1927
	s_and_saveexec_b64 s[4:5], s[78:79]
	ds_write_b32 v174, v1
	s_or_b64 exec, exec, s[4:5]
	v_readlane_b32 s1, v254, 30
	s_waitcnt lgkmcnt(0)
	s_nop 1
	v_add_u32_e32 v0, s1, v175
	v_readlane_b32 s1, v254, 32
	s_nop 1
	v_add_u32_e32 v4, s1, v175
	v_readlane_b32 s1, v254, 33
	s_nop 1
	v_add_u32_e32 v8, s1, v175
	v_readlane_b32 s1, v254, 31
	ds_read_b128 v[4:7], v4
	ds_read_b128 v[8:11], v8
	v_add_u32_e32 v12, s1, v175
	ds_read_b128 v[52:55], v12
	ds_read_b128 v[56:59], v0
	s_waitcnt lgkmcnt(3)
	v_mul_f32_e32 v14, 0, v6
	v_mul_f32_e32 v15, 0, v7
	s_waitcnt lgkmcnt(2)
	v_mul_f32_e32 v18, 0, v10
	v_mul_f32_e32 v19, 0, v11
	s_waitcnt lgkmcnt(1)
	v_mul_f32_e32 v10, 0, v54
	v_mul_f32_e32 v11, 0, v55
	s_waitcnt lgkmcnt(0)
	v_mul_f32_e32 v6, 0, v58
	v_mul_f32_e32 v7, 0, v59
	v_mul_f32_e32 v16, 0, v8
	v_mul_f32_e32 v17, 0, v9
	v_mul_f32_e32 v12, 0, v4
	v_mul_f32_e32 v13, 0, v5
	v_mul_f32_e32 v8, 0, v52
	v_mul_f32_e32 v9, 0, v53
	v_mul_f32_e32 v4, 0, v56
	v_mul_f32_e32 v5, 0, v57
	s_branch .LBB0_1928

.LBB0_1928:
	v_mul_f32_e32 v0, 0xbe0293ee, v173
	v_fma_f32 v36, v36, s2, v0
	v_fma_f32 v37, v37, s2, v0
	v_fma_f32 v20, v20, s2, v0
	v_fma_f32 v21, v21, s2, v0
	v_fma_f32 v38, v38, s2, v0
	v_fma_f32 v39, v39, s2, v0
	v_exp_f32_e32 v36, v36
	v_exp_f32_e32 v37, v37
	v_exp_f32_e32 v20, v20
	v_exp_f32_e32 v21, v21
	v_fma_f32 v22, v22, s2, v0
	v_fma_f32 v23, v23, s2, v0
	v_fma_f32 v40, v40, s2, v0
	v_fma_f32 v41, v41, s2, v0
	v_exp_f32_e32 v38, v38
	v_exp_f32_e32 v39, v39
	v_exp_f32_e32 v22, v22
	v_exp_f32_e32 v23, v23
	v_fma_f32 v24, v24, s2, v0
	v_fma_f32 v25, v25, s2, v0
	v_fma_f32 v42, v42, s2, v0
	v_fma_f32 v43, v43, s2, v0
	v_exp_f32_e32 v40, v40
	v_exp_f32_e32 v41, v41
	v_exp_f32_e32 v24, v24
	v_exp_f32_e32 v25, v25
	v_fma_f32 v26, v26, s2, v0
	v_fma_f32 v27, v27, s2, v0
	v_fma_f32 v44, v44, s2, v0
	v_fma_f32 v45, v45, s2, v0
	v_exp_f32_e32 v42, v42
	v_exp_f32_e32 v43, v43
	v_exp_f32_e32 v26, v26
	v_exp_f32_e32 v27, v27
	v_fma_f32 v28, v28, s2, v0
	v_fma_f32 v29, v29, s2, v0
	v_fma_f32 v46, v46, s2, v0
	v_fma_f32 v47, v47, s2, v0
	v_fma_f32 v48, v48, s2, v0
	v_fma_f32 v49, v49, s2, v0
	v_fma_f32 v50, v50, s2, v0
	v_fma_f32 v51, v51, s2, v0
	v_exp_f32_e32 v44, v44
	v_exp_f32_e32 v45, v45
	v_exp_f32_e32 v28, v28
	v_exp_f32_e32 v29, v29
	v_fma_f32 v30, v30, s2, v0
	v_fma_f32 v31, v31, s2, v0
	v_fma_f32 v32, v32, s2, v0
	v_fma_f32 v33, v33, s2, v0
	v_fma_f32 v34, v34, s2, v0
	v_fma_f32 v35, v35, s2, v0
	v_add_f32_e32 v66, v20, v36
	v_add_f32_e32 v67, v21, v37
	v_exp_f32_e32 v46, v46
	v_exp_f32_e32 v47, v47
	v_exp_f32_e32 v48, v48
	v_exp_f32_e32 v49, v49
	v_exp_f32_e32 v50, v50
	v_exp_f32_e32 v51, v51
	v_exp_f32_e32 v30, v30
	v_exp_f32_e32 v31, v31
	v_exp_f32_e32 v32, v32
	v_exp_f32_e32 v33, v33
	v_exp_f32_e32 v34, v34
	v_exp_f32_e32 v35, v35
	v_add_f32_e32 v64, v22, v38
	v_add_f32_e32 v65, v23, v39
	v_add_f32_e32 v66, 0, v66
	v_add_f32_e32 v67, 0, v67
	v_cvt_pk_bf16_f32 v70, v20, v21
	v_cvt_pk_bf16_f32 v71, v22, v23
	v_cvt_pk_bf16_f32 v72, v24, v25
	v_cvt_pk_bf16_f32 v73, v26, v27
	v_cvt_pk_bf16_f32 v74, v28, v29
	v_cvt_pk_bf16_f32 v75, v30, v31
	v_cvt_pk_bf16_f32 v76, v32, v33
	v_cvt_pk_bf16_f32 v77, v34, v35
	v_cvt_pk_bf16_f32 v78, v36, v37
	v_cvt_pk_bf16_f32 v79, v38, v39
	v_cvt_pk_bf16_f32 v80, v40, v41
	v_cvt_pk_bf16_f32 v81, v42, v43
	v_cvt_pk_bf16_f32 v82, v44, v45
	v_cvt_pk_bf16_f32 v83, v46, v47
	v_cvt_pk_bf16_f32 v84, v48, v49
	v_cvt_pk_bf16_f32 v85, v50, v51
	ds_read_b64_tr_b16 v[36:37], v136 offset:0
	v_add_f32_e32 v62, v24, v40
	v_add_f32_e32 v63, v25, v41
	v_add_f32_e32 v64, v64, v66
	v_add_f32_e32 v65, v65, v67
	ds_read_b64_tr_b16 v[38:39], v136 offset:0x800
	v_add_f32_e32 v60, v26, v42
	v_add_f32_e32 v61, v27, v43
	v_add_f32_e32 v62, v62, v64
	v_add_f32_e32 v63, v63, v65
	ds_read_b64_tr_b16 v[40:41], v136 offset:0x1000
	v_add_f32_e32 v58, v28, v44
	v_add_f32_e32 v59, v29, v45
	v_add_f32_e32 v60, v60, v62
	v_add_f32_e32 v61, v61, v63
	ds_read_b64_tr_b16 v[42:43], v136 offset:0x1800
	v_add_f32_e32 v56, v30, v46
	v_add_f32_e32 v57, v31, v47
	v_add_f32_e32 v58, v58, v60
	v_add_f32_e32 v59, v59, v61
	ds_read_b64_tr_b16 v[44:45], v136 offset:0x2000
	v_add_f32_e32 v54, v32, v48
	v_add_f32_e32 v55, v33, v49
	v_add_f32_e32 v56, v56, v58
	v_add_f32_e32 v57, v57, v59
	ds_read_b64_tr_b16 v[46:47], v136 offset:0x2800
	v_add_f32_e32 v52, v34, v50
	v_add_f32_e32 v53, v35, v51
	v_add_f32_e32 v54, v54, v56
	v_add_f32_e32 v55, v55, v57
	ds_read_b64_tr_b16 v[48:49], v136 offset:0x3000
	ds_read_b64_tr_b16 v[50:51], v136 offset:0x3800
	s_waitcnt lgkmcnt(0)
	v_permlane32_swap_b32_e32 v70, v72
	v_add_f32_e32 v52, v52, v54
	v_add_f32_e32 v53, v53, v55
	v_permlane32_swap_b32_e32 v71, v73
	v_add_f32_e32 v68, v52, v53
	v_add_f32_e32 v69, v53, v52
	v_permlane32_swap_b32_e32 v74, v76
	v_mov_b32_e32 v69, v68
	s_nop 1
	v_permlane32_swap_b32_e32 v68, v69
	v_permlane32_swap_b32_e32 v75, v77
	v_permlane32_swap_b32_e32 v78, v80
	v_permlane32_swap_b32_e32 v79, v81
	v_permlane32_swap_b32_e32 v82, v84
	v_permlane32_swap_b32_e32 v83, v85
	v_mfma_f32_32x32x16_bf16 v[20:35], v[70:73], v[36:39], v[4:19]
	ds_read_b64_tr_b16 v[52:53], v136 offset:0x200
	ds_read_b64_tr_b16 v[54:55], v136 offset:0xa00
	ds_read_b64_tr_b16 v[56:57], v136 offset:0x1200
	ds_read_b64_tr_b16 v[58:59], v136 offset:0x1a00
	ds_read_b64_tr_b16 v[60:61], v136 offset:0x2200
	ds_read_b64_tr_b16 v[62:63], v136 offset:0x2a00
	ds_read_b64_tr_b16 v[64:65], v136 offset:0x3200
	v_mfma_f32_32x32x16_bf16 v[20:35], v[74:77], v[40:43], v[20:35]
	ds_read_b64_tr_b16 v[66:67], v136 offset:0x3a00
	s_waitcnt lgkmcnt(0)
	v_mfma_f32_32x32x16_bf16 v[20:35], v[78:81], v[44:47], v[20:35]
	v_mfma_f32_32x32x16_bf16 v[20:35], v[82:85], v[48:51], v[20:35]
	v_mfma_f32_32x32x16_bf16 v[36:51], v[70:73], v[52:55], v[4:19]
	ds_read_b64_tr_b16 v[86:87], v136 offset:0x400
	ds_read_b64_tr_b16 v[88:89], v136 offset:0xc00
	ds_read_b64_tr_b16 v[90:91], v136 offset:0x1400
	ds_read_b64_tr_b16 v[92:93], v136 offset:0x1c00
	ds_read_b64_tr_b16 v[94:95], v136 offset:0x2400
	ds_read_b64_tr_b16 v[96:97], v136 offset:0x2c00
	ds_read_b64_tr_b16 v[176:177], v136 offset:0x3400
	v_mfma_f32_32x32x16_bf16 v[36:51], v[74:77], v[56:59], v[36:51]
	ds_read_b64_tr_b16 v[178:179], v136 offset:0x3c00
	s_waitcnt lgkmcnt(0)
	v_mfma_f32_32x32x16_bf16 v[36:51], v[78:81], v[60:63], v[36:51]
	v_mfma_f32_32x32x16_bf16 v[36:51], v[82:85], v[64:67], v[36:51]
	v_mfma_f32_32x32x16_bf16 v[52:67], v[70:73], v[86:89], v[4:19]
	ds_read_b64_tr_b16 v[86:87], v136 offset:0x600
	ds_read_b64_tr_b16 v[88:89], v136 offset:0xe00
	v_mfma_f32_32x32x16_bf16 v[52:67], v[74:77], v[90:93], v[52:67]
	ds_read_b64_tr_b16 v[90:91], v136 offset:0x1600
	ds_read_b64_tr_b16 v[92:93], v136 offset:0x1e00
	v_mfma_f32_32x32x16_bf16 v[52:67], v[78:81], v[94:97], v[52:67]
	ds_read_b64_tr_b16 v[94:95], v136 offset:0x2600
	ds_read_b64_tr_b16 v[96:97], v136 offset:0x2e00
	v_mfma_f32_32x32x16_bf16 v[52:67], v[82:85], v[176:179], v[52:67]
	ds_read_b64_tr_b16 v[176:177], v136 offset:0x3600
	ds_read_b64_tr_b16 v[178:179], v136 offset:0x3e00
	s_waitcnt lgkmcnt(0)
	v_mfma_f32_32x32x16_bf16 v[4:19], v[70:73], v[86:89], v[4:19]
	v_cndmask_b32_e64 v70, 0, 1, s[8:9]
	s_mov_b64 s[86:87], -1
	v_cmp_ne_u32_e64 s[80:81], 1, v70
	s_andn2_b64 vcc, exec, s[8:9]
	v_mfma_f32_32x32x16_bf16 v[4:19], v[74:77], v[90:93], v[4:19]
	v_mfma_f32_32x32x16_bf16 v[4:19], v[78:81], v[94:97], v[4:19]
	v_mfma_f32_32x32x16_bf16 v[4:19], v[82:85], v[176:179], v[4:19]
	s_cbranch_vccnz .LBB0_1930
	s_waitcnt vmcnt(2) lgkmcnt(0)
	s_mov_b64 s[86:87], 0

.LBB0_1948:
	v_cmp_gt_f32_e32 vcc, 1.0, v177
	s_cbranch_vccz .LBB0_1952
	s_and_saveexec_b64 s[4:5], s[78:79]
	ds_write_b32 v174, v177
	s_or_b64 exec, exec, s[4:5]
	v_readlane_b32 s1, v254, 32
	s_waitcnt lgkmcnt(0)
	s_nop 1
	v_add_u32_e32 v1, s1, v175
	v_readlane_b32 s1, v254, 33
	s_nop 1
	v_add_u32_e32 v182, s1, v175
	v_readlane_b32 s1, v254, 31
	ds_read_b128 v[178:181], v1
	ds_read_b128 v[182:185], v182
	v_add_u32_e32 v1, s1, v175
	v_readlane_b32 s1, v254, 30
	ds_read_b128 v[186:189], v1
	s_waitcnt lgkmcnt(2)
	v_mul_f32_e32 v28, v28, v178
	v_mul_f32_e32 v29, v29, v179
	v_add_u32_e32 v1, s1, v175
	ds_read_b128 v[190:193], v1
	s_waitcnt lgkmcnt(2)
	v_mul_f32_e32 v32, v32, v182
	v_mul_f32_e32 v33, v33, v183
	s_waitcnt lgkmcnt(1)
	v_mul_f32_e32 v24, v24, v186
	v_mul_f32_e32 v25, v25, v187
	v_mul_f32_e32 v34, v34, v184
	v_mul_f32_e32 v35, v35, v185
	v_mul_f32_e32 v30, v30, v180
	v_mul_f32_e32 v31, v31, v181
	v_mul_f32_e32 v26, v26, v188
	v_mul_f32_e32 v27, v27, v189
	s_waitcnt lgkmcnt(0)
	v_mul_f32_e32 v22, v22, v192
	v_mul_f32_e32 v23, v23, v193
	v_mul_f32_e32 v20, v20, v190
	v_mul_f32_e32 v21, v21, v191
	v_mul_f32_e32 v48, v48, v182
	v_mul_f32_e32 v49, v49, v183
	v_mul_f32_e32 v44, v44, v178
	v_mul_f32_e32 v45, v45, v179
	v_mul_f32_e32 v40, v40, v186
	v_mul_f32_e32 v41, v41, v187
	v_mul_f32_e32 v50, v50, v184
	v_mul_f32_e32 v51, v51, v185
	v_mul_f32_e32 v46, v46, v180
	v_mul_f32_e32 v47, v47, v181
	v_mul_f32_e32 v42, v42, v188
	v_mul_f32_e32 v43, v43, v189
	v_mul_f32_e32 v38, v38, v192
	v_mul_f32_e32 v39, v39, v193
	v_mul_f32_e32 v36, v36, v190
	v_mul_f32_e32 v37, v37, v191
	v_mul_f32_e32 v64, v64, v182
	v_mul_f32_e32 v65, v65, v183
	v_mul_f32_e32 v60, v60, v178
	v_mul_f32_e32 v61, v61, v179
	v_mul_f32_e32 v56, v56, v186
	v_mul_f32_e32 v57, v57, v187
	v_mul_f32_e32 v66, v66, v184
	v_mul_f32_e32 v67, v67, v185
	v_mul_f32_e32 v62, v62, v180
	v_mul_f32_e32 v63, v63, v181
	v_mul_f32_e32 v58, v58, v188
	v_mul_f32_e32 v59, v59, v189
	v_mul_f32_e32 v54, v54, v192
	v_mul_f32_e32 v55, v55, v193
	v_mul_f32_e32 v52, v52, v190
	v_mul_f32_e32 v53, v53, v191
	v_mul_f32_e32 v16, v16, v182
	v_mul_f32_e32 v17, v17, v183
	v_mul_f32_e32 v12, v12, v178
	v_mul_f32_e32 v13, v13, v179
	v_mul_f32_e32 v8, v8, v186
	v_mul_f32_e32 v9, v9, v187
	v_mul_f32_e32 v18, v18, v184
	v_mul_f32_e32 v19, v19, v185
	v_mul_f32_e32 v14, v14, v180
	v_mul_f32_e32 v15, v15, v181
	v_mul_f32_e32 v10, v10, v188
	v_mul_f32_e32 v11, v11, v189
	v_mul_f32_e32 v6, v6, v192
	v_mul_f32_e32 v7, v7, v193
	v_mul_f32_e32 v4, v4, v190
	v_mul_f32_e32 v5, v5, v191
.LBB0_1952:
	v_mov_b32_e32 v1, v0
	v_fma_f32 v84, v84, s2, v0
	v_fma_f32 v85, v85, s2, v1
	v_fma_f32 v68, v68, s2, v0
	v_fma_f32 v69, v69, s2, v1
	v_fma_f32 v86, v86, s2, v0
	v_fma_f32 v87, v87, s2, v1
	v_fma_f32 v88, v88, s2, v0
	v_fma_f32 v89, v89, s2, v1
	v_fma_f32 v90, v90, s2, v0
	v_fma_f32 v91, v91, s2, v1
	v_fma_f32 v92, v92, s2, v0
	v_fma_f32 v93, v93, s2, v1
	v_fma_f32 v94, v94, s2, v0
	v_fma_f32 v95, v95, s2, v1
	v_fma_f32 v96, v96, s2, v0
	v_fma_f32 v97, v97, s2, v1
	v_fma_f32 v98, v98, s2, v0
	v_fma_f32 v99, v99, s2, v1
	v_exp_f32_e32 v84, v84
	v_exp_f32_e32 v85, v85
	v_exp_f32_e32 v68, v68
	v_exp_f32_e32 v69, v69
	v_fma_f32 v70, v70, s2, v0
	v_fma_f32 v71, v71, s2, v1
	v_fma_f32 v72, v72, s2, v0
	v_fma_f32 v73, v73, s2, v1
	v_fma_f32 v74, v74, s2, v0
	v_fma_f32 v75, v75, s2, v1
	v_fma_f32 v76, v76, s2, v0
	v_fma_f32 v77, v77, s2, v1
	v_fma_f32 v78, v78, s2, v0
	v_fma_f32 v79, v79, s2, v1
	v_fma_f32 v80, v80, s2, v0
	v_fma_f32 v81, v81, s2, v1
	v_fma_f32 v0, v82, s2, v0
	v_fma_f32 v1, v83, s2, v1
	v_exp_f32_e32 v86, v86
	v_exp_f32_e32 v87, v87
	v_exp_f32_e32 v88, v88
	v_exp_f32_e32 v89, v89
	v_exp_f32_e32 v90, v90
	v_exp_f32_e32 v91, v91
	v_exp_f32_e32 v92, v92
	v_exp_f32_e32 v93, v93
	v_exp_f32_e32 v94, v94
	v_exp_f32_e32 v95, v95
	v_exp_f32_e32 v96, v96
	v_exp_f32_e32 v97, v97
	v_exp_f32_e32 v98, v98
	v_exp_f32_e32 v99, v99
	v_exp_f32_e32 v70, v70
	v_exp_f32_e32 v71, v71
	v_exp_f32_e32 v72, v72
	v_exp_f32_e32 v73, v73
	v_exp_f32_e32 v74, v74
	v_exp_f32_e32 v75, v75
	v_exp_f32_e32 v76, v76
	v_exp_f32_e32 v77, v77
	v_exp_f32_e32 v78, v78
	v_exp_f32_e32 v79, v79
	v_exp_f32_e32 v80, v80
	v_exp_f32_e32 v81, v81
	v_exp_f32_e32 v82, v0
	v_exp_f32_e32 v83, v1
	v_add_f32_e32 v190, v68, v84
	v_add_f32_e32 v191, v69, v85
	v_add_f32_e32 v178, v80, v96
	v_add_f32_e32 v179, v81, v97
	v_add_f32_e32 v180, v78, v94
	v_add_f32_e32 v181, v79, v95
	v_add_f32_e32 v0, v82, v98
	v_add_f32_e32 v1, v83, v99
	v_add_f32_e32 v182, v76, v92
	v_add_f32_e32 v183, v77, v93
	v_add_f32_e32 v184, v74, v90
	v_add_f32_e32 v185, v75, v91
	v_add_f32_e32 v186, v72, v88
	v_add_f32_e32 v187, v73, v89
	v_add_f32_e32 v188, v70, v86
	v_add_f32_e32 v189, v71, v87
	v_add_f32_e32 v190, 0, v190
	v_add_f32_e32 v191, 0, v191
	v_cvt_pk_bf16_f32 v68, v68, v69
	v_cvt_pk_bf16_f32 v69, v70, v71
	v_cvt_pk_bf16_f32 v70, v72, v73
	v_cvt_pk_bf16_f32 v71, v74, v75
	v_cvt_pk_bf16_f32 v72, v76, v77
	v_cvt_pk_bf16_f32 v73, v78, v79
	v_cvt_pk_bf16_f32 v74, v80, v81
	v_cvt_pk_bf16_f32 v75, v82, v83
	v_cvt_pk_bf16_f32 v76, v84, v85
	v_cvt_pk_bf16_f32 v77, v86, v87
	v_cvt_pk_bf16_f32 v78, v88, v89
	v_cvt_pk_bf16_f32 v79, v90, v91
	v_cvt_pk_bf16_f32 v80, v92, v93
	v_cvt_pk_bf16_f32 v81, v94, v95
	v_cvt_pk_bf16_f32 v82, v96, v97
	v_cvt_pk_bf16_f32 v83, v98, v99
	ds_read_b64_tr_b16 v[84:85], v176 offset:0
	s_nop 0
	v_add_f32_e32 v188, v188, v190
	v_add_f32_e32 v189, v189, v191
	ds_read_b64_tr_b16 v[86:87], v176 offset:0x800
	ds_read_b64_tr_b16 v[88:89], v176 offset:0x1000
	ds_read_b64_tr_b16 v[90:91], v176 offset:0x1800
	ds_read_b64_tr_b16 v[92:93], v176 offset:0x2000
	ds_read_b64_tr_b16 v[94:95], v176 offset:0x2800
	s_nop 0
	v_add_f32_e32 v186, v186, v188
	v_add_f32_e32 v187, v187, v189
	ds_read_b64_tr_b16 v[96:97], v176 offset:0x3000
	ds_read_b64_tr_b16 v[98:99], v176 offset:0x3800
	s_waitcnt lgkmcnt(0)
	v_permlane32_swap_b32_e32 v68, v70
	v_add_f32_e32 v184, v184, v186
	v_add_f32_e32 v185, v185, v187
	v_permlane32_swap_b32_e32 v69, v71
	v_add_f32_e32 v182, v182, v184
	v_add_f32_e32 v183, v183, v185
	v_permlane32_swap_b32_e32 v72, v74
	v_add_f32_e32 v180, v180, v182
	v_add_f32_e32 v181, v181, v183
	v_permlane32_swap_b32_e32 v73, v75
	v_add_f32_e32 v178, v178, v180
	v_add_f32_e32 v179, v179, v181
	v_permlane32_swap_b32_e32 v76, v78
	v_add_f32_e32 v0, v0, v178
	v_add_f32_e32 v1, v1, v179
	v_permlane32_swap_b32_e32 v77, v79
	v_pk_add_f32 v[0:1], v[0:1], v[0:1] op_sel:[0,1] op_sel_hi:[1,0]
	v_permlane32_swap_b32_e32 v80, v82
	v_mov_b32_e32 v1, v0
	s_nop 1
	v_permlane32_swap_b32_e32 v0, v1
	v_permlane32_swap_b32_e32 v81, v83
	v_mfma_f32_32x32x16_bf16 v[20:35], v[68:71], v[84:87], v[20:35]
	ds_read_b64_tr_b16 v[84:85], v176 offset:0x200
	ds_read_b64_tr_b16 v[86:87], v176 offset:0xa00
	v_mfma_f32_32x32x16_bf16 v[20:35], v[72:75], v[88:91], v[20:35]
	ds_read_b64_tr_b16 v[88:89], v176 offset:0x1200
	ds_read_b64_tr_b16 v[90:91], v176 offset:0x1a00
	v_mfma_f32_32x32x16_bf16 v[20:35], v[76:79], v[92:95], v[20:35]
	ds_read_b64_tr_b16 v[92:93], v176 offset:0x2200
	ds_read_b64_tr_b16 v[94:95], v176 offset:0x2a00
	v_mfma_f32_32x32x16_bf16 v[20:35], v[80:83], v[96:99], v[20:35]
	ds_read_b64_tr_b16 v[96:97], v176 offset:0x3200
	ds_read_b64_tr_b16 v[98:99], v176 offset:0x3a00
	s_waitcnt lgkmcnt(0)
	v_mfma_f32_32x32x16_bf16 v[36:51], v[68:71], v[84:87], v[36:51]
	ds_read_b64_tr_b16 v[84:85], v176 offset:0x400
	ds_read_b64_tr_b16 v[86:87], v176 offset:0xc00
	v_mfma_f32_32x32x16_bf16 v[36:51], v[72:75], v[88:91], v[36:51]
	ds_read_b64_tr_b16 v[88:89], v176 offset:0x1400
	ds_read_b64_tr_b16 v[90:91], v176 offset:0x1c00
	v_mfma_f32_32x32x16_bf16 v[36:51], v[76:79], v[92:95], v[36:51]
	ds_read_b64_tr_b16 v[92:93], v176 offset:0x2400
	ds_read_b64_tr_b16 v[94:95], v176 offset:0x2c00
	v_mfma_f32_32x32x16_bf16 v[36:51], v[80:83], v[96:99], v[36:51]
	ds_read_b64_tr_b16 v[96:97], v176 offset:0x3400
	ds_read_b64_tr_b16 v[98:99], v176 offset:0x3c00
	s_waitcnt lgkmcnt(0)
	v_mfma_f32_32x32x16_bf16 v[52:67], v[68:71], v[84:87], v[52:67]
	ds_read_b64_tr_b16 v[84:85], v176 offset:0x600
	ds_read_b64_tr_b16 v[86:87], v176 offset:0xe00
	v_mfma_f32_32x32x16_bf16 v[52:67], v[72:75], v[88:91], v[52:67]
	ds_read_b64_tr_b16 v[88:89], v176 offset:0x1600
	ds_read_b64_tr_b16 v[90:91], v176 offset:0x1e00
	v_mfma_f32_32x32x16_bf16 v[52:67], v[76:79], v[92:95], v[52:67]
	ds_read_b64_tr_b16 v[92:93], v176 offset:0x2600
	ds_read_b64_tr_b16 v[94:95], v176 offset:0x2e00
	v_mfma_f32_32x32x16_bf16 v[52:67], v[80:83], v[96:99], v[52:67]
	ds_read_b64_tr_b16 v[96:97], v176 offset:0x3600
	ds_read_b64_tr_b16 v[98:99], v176 offset:0x3e00
	s_waitcnt lgkmcnt(0)
	v_mfma_f32_32x32x16_bf16 v[4:19], v[68:71], v[84:87], v[4:19]
	s_mov_b64 s[86:87], -1
	s_andn2_b64 vcc, exec, s[8:9]
	v_mfma_f32_32x32x16_bf16 v[4:19], v[72:75], v[88:91], v[4:19]
	v_mfma_f32_32x32x16_bf16 v[4:19], v[76:79], v[92:95], v[4:19]
	v_mfma_f32_32x32x16_bf16 v[4:19], v[80:83], v[96:99], v[4:19]
	s_cbranch_vccnz .LBB0_1954
	s_waitcnt vmcnt(2) lgkmcnt(0)
	s_mov_b64 s[86:87], 0

.LBB0_1971:
	v_cmp_gt_f32_e32 vcc, 1.0, v1
	s_cbranch_vccz .LBB0_1975
	s_and_saveexec_b64 s[4:5], s[78:79]
	ds_write_b32 v174, v1
	s_or_b64 exec, exec, s[4:5]
	v_readlane_b32 s4, v254, 32
	s_waitcnt lgkmcnt(0)
	s_nop 1
	v_add_u32_e32 v0, s4, v175
	v_readlane_b32 s4, v254, 33
	s_nop 1
	v_add_u32_e32 v177, s4, v175
	v_readlane_b32 s4, v254, 31
	ds_read_b128 v[178:181], v0
	ds_read_b128 v[182:185], v177
	v_add_u32_e32 v0, s4, v175
	v_readlane_b32 s4, v254, 30
	ds_read_b128 v[186:189], v0
	s_waitcnt lgkmcnt(2)
	v_mul_f32_e32 v28, v28, v178
	v_mul_f32_e32 v29, v29, v179
	v_add_u32_e32 v0, s4, v175
	ds_read_b128 v[190:193], v0
	s_waitcnt lgkmcnt(2)
	v_mul_f32_e32 v32, v32, v182
	v_mul_f32_e32 v33, v33, v183
	s_waitcnt lgkmcnt(1)
	v_mul_f32_e32 v24, v24, v186
	v_mul_f32_e32 v25, v25, v187
	v_mul_f32_e32 v34, v34, v184
	v_mul_f32_e32 v35, v35, v185
	v_mul_f32_e32 v30, v30, v180
	v_mul_f32_e32 v31, v31, v181
	v_mul_f32_e32 v26, v26, v188
	v_mul_f32_e32 v27, v27, v189
	s_waitcnt lgkmcnt(0)
	v_mul_f32_e32 v22, v22, v192
	v_mul_f32_e32 v23, v23, v193
	v_mul_f32_e32 v20, v20, v190
	v_mul_f32_e32 v21, v21, v191
	v_mul_f32_e32 v48, v48, v182
	v_mul_f32_e32 v49, v49, v183
	v_mul_f32_e32 v44, v44, v178
	v_mul_f32_e32 v45, v45, v179
	v_mul_f32_e32 v40, v40, v186
	v_mul_f32_e32 v41, v41, v187
	v_mul_f32_e32 v50, v50, v184
	v_mul_f32_e32 v51, v51, v185
	v_mul_f32_e32 v46, v46, v180
	v_mul_f32_e32 v47, v47, v181
	v_mul_f32_e32 v42, v42, v188
	v_mul_f32_e32 v43, v43, v189
	v_mul_f32_e32 v38, v38, v192
	v_mul_f32_e32 v39, v39, v193
	v_mul_f32_e32 v36, v36, v190
	v_mul_f32_e32 v37, v37, v191
	v_mul_f32_e32 v64, v64, v182
	v_mul_f32_e32 v65, v65, v183
	v_mul_f32_e32 v60, v60, v178
	v_mul_f32_e32 v61, v61, v179
	v_mul_f32_e32 v56, v56, v186
	v_mul_f32_e32 v57, v57, v187
	v_mul_f32_e32 v66, v66, v184
	v_mul_f32_e32 v67, v67, v185
	v_mul_f32_e32 v62, v62, v180
	v_mul_f32_e32 v63, v63, v181
	v_mul_f32_e32 v58, v58, v188
	v_mul_f32_e32 v59, v59, v189
	v_mul_f32_e32 v54, v54, v192
	v_mul_f32_e32 v55, v55, v193
	v_mul_f32_e32 v52, v52, v190
	v_mul_f32_e32 v53, v53, v191
	v_mul_f32_e32 v16, v16, v182
	v_mul_f32_e32 v17, v17, v183
	v_mul_f32_e32 v12, v12, v178
	v_mul_f32_e32 v13, v13, v179
	v_mul_f32_e32 v8, v8, v186
	v_mul_f32_e32 v9, v9, v187
	v_mul_f32_e32 v18, v18, v184
	v_mul_f32_e32 v19, v19, v185
	v_mul_f32_e32 v14, v14, v180
	v_mul_f32_e32 v15, v15, v181
	v_mul_f32_e32 v10, v10, v188
	v_mul_f32_e32 v11, v11, v189
	v_mul_f32_e32 v6, v6, v192
	v_mul_f32_e32 v7, v7, v193
	v_mul_f32_e32 v4, v4, v190
	v_mul_f32_e32 v5, v5, v191
.LBB0_1975:
	v_mul_f32_e32 v0, 0xbe0293ee, v173
	v_fma_f32 v84, v84, s2, v0
	v_fma_f32 v85, v85, s2, v0
	v_fma_f32 v68, v68, s2, v0
	v_fma_f32 v69, v69, s2, v0
	v_fma_f32 v86, v86, s2, v0
	v_fma_f32 v87, v87, s2, v0
	v_exp_f32_e32 v84, v84
	v_exp_f32_e32 v85, v85
	v_exp_f32_e32 v178, v68
	v_exp_f32_e32 v179, v69
	v_fma_f32 v68, v70, s2, v0
	v_fma_f32 v69, v71, s2, v0
	v_fma_f32 v88, v88, s2, v0
	v_fma_f32 v89, v89, s2, v0
	v_exp_f32_e32 v86, v86
	v_exp_f32_e32 v87, v87
	v_exp_f32_e32 v180, v68
	v_exp_f32_e32 v181, v69
	v_fma_f32 v68, v72, s2, v0
	v_fma_f32 v69, v73, s2, v0
	v_fma_f32 v90, v90, s2, v0
	v_fma_f32 v91, v91, s2, v0
	v_exp_f32_e32 v88, v88
	v_exp_f32_e32 v89, v89
	v_exp_f32_e32 v72, v68
	v_exp_f32_e32 v73, v69
	v_fma_f32 v68, v74, s2, v0
	v_fma_f32 v69, v75, s2, v0
	v_fma_f32 v92, v92, s2, v0
	v_fma_f32 v93, v93, s2, v0
	v_exp_f32_e32 v90, v90
	v_exp_f32_e32 v91, v91
	v_exp_f32_e32 v74, v68
	v_exp_f32_e32 v75, v69
	v_fma_f32 v68, v76, s2, v0
	v_fma_f32 v69, v77, s2, v0
	v_fma_f32 v94, v94, s2, v0
	v_fma_f32 v95, v95, s2, v0
	v_exp_f32_e32 v92, v92
	v_exp_f32_e32 v93, v93
	v_exp_f32_e32 v76, v68
	v_exp_f32_e32 v77, v69
	v_fma_f32 v68, v78, s2, v0
	v_fma_f32 v69, v79, s2, v0
	v_add_f32_e32 v192, v178, v84
	v_add_f32_e32 v193, v179, v85
	v_fma_f32 v96, v96, s2, v0
	v_fma_f32 v97, v97, s2, v0
	v_exp_f32_e32 v94, v94
	v_exp_f32_e32 v95, v95
	v_exp_f32_e32 v78, v68
	v_exp_f32_e32 v79, v69
	v_fma_f32 v68, v80, s2, v0
	v_fma_f32 v69, v81, s2, v0
	v_add_f32_e32 v190, v180, v86
	v_add_f32_e32 v191, v181, v87
	v_add_f32_e32 v192, 0, v192
	v_add_f32_e32 v193, 0, v193
	v_fma_f32 v98, v98, s2, v0
	v_fma_f32 v99, v99, s2, v0
	v_exp_f32_e32 v96, v96
	v_exp_f32_e32 v97, v97
	v_exp_f32_e32 v80, v68
	v_exp_f32_e32 v81, v69
	v_fma_f32 v68, v82, s2, v0
	v_fma_f32 v69, v83, s2, v0
	v_add_f32_e32 v188, v72, v88
	v_add_f32_e32 v189, v73, v89
	v_add_f32_e32 v190, v190, v192
	v_add_f32_e32 v191, v191, v193
	v_exp_f32_e32 v98, v98
	v_exp_f32_e32 v99, v99
	v_exp_f32_e32 v82, v68
	v_exp_f32_e32 v83, v69
	v_add_f32_e32 v186, v74, v90
	v_add_f32_e32 v187, v75, v91
	v_add_f32_e32 v188, v188, v190
	v_add_f32_e32 v189, v189, v191
	v_add_f32_e32 v184, v76, v92
	v_add_f32_e32 v185, v77, v93
	v_add_f32_e32 v186, v186, v188
	v_add_f32_e32 v187, v187, v189
	v_add_f32_e32 v182, v78, v94
	v_add_f32_e32 v183, v79, v95
	v_add_f32_e32 v184, v184, v186
	v_add_f32_e32 v185, v185, v187
	v_add_f32_e32 v70, v80, v96
	v_add_f32_e32 v71, v81, v97
	v_add_f32_e32 v182, v182, v184
	v_add_f32_e32 v183, v183, v185
	v_add_f32_e32 v68, v82, v98
	v_add_f32_e32 v69, v83, v99
	v_add_f32_e32 v70, v70, v182
	v_add_f32_e32 v71, v71, v183
	s_nop 0
	v_add_f32_e32 v68, v68, v70
	v_add_f32_e32 v69, v69, v71
	v_cvt_pk_bf16_f32 v70, v178, v179
	v_cvt_pk_bf16_f32 v71, v180, v181
	v_cvt_pk_bf16_f32 v72, v72, v73
	v_cvt_pk_bf16_f32 v73, v74, v75
	v_cvt_pk_bf16_f32 v74, v76, v77
	v_cvt_pk_bf16_f32 v75, v78, v79
	v_cvt_pk_bf16_f32 v76, v80, v81
	v_cvt_pk_bf16_f32 v77, v82, v83
	v_cvt_pk_bf16_f32 v78, v84, v85
	v_cvt_pk_bf16_f32 v79, v86, v87
	v_cvt_pk_bf16_f32 v80, v88, v89
	v_cvt_pk_bf16_f32 v81, v90, v91
	v_cvt_pk_bf16_f32 v82, v92, v93
	v_cvt_pk_bf16_f32 v83, v94, v95
	v_cvt_pk_bf16_f32 v84, v96, v97
	v_cvt_pk_bf16_f32 v85, v98, v99
	ds_read_b64_tr_b16 v[86:87], v136 offset:0
	ds_read_b64_tr_b16 v[88:89], v136 offset:0x800
	ds_read_b64_tr_b16 v[90:91], v136 offset:0x1000
	ds_read_b64_tr_b16 v[92:93], v136 offset:0x1800
	ds_read_b64_tr_b16 v[94:95], v136 offset:0x2000
	ds_read_b64_tr_b16 v[96:97], v136 offset:0x2800
	ds_read_b64_tr_b16 v[178:179], v136 offset:0x3000
	ds_read_b64_tr_b16 v[180:181], v136 offset:0x3800
	s_nop 0
	v_pk_add_f32 v[68:69], v[68:69], v[68:69] op_sel:[0,1] op_sel_hi:[1,0]
	s_waitcnt lgkmcnt(0)
	v_permlane32_swap_b32_e32 v70, v72
	v_mov_b32_e32 v69, v68
	s_nop 1
	v_permlane32_swap_b32_e32 v68, v69
	v_permlane32_swap_b32_e32 v71, v73
	v_permlane32_swap_b32_e32 v74, v76
	v_permlane32_swap_b32_e32 v75, v77
	v_permlane32_swap_b32_e32 v78, v80
	v_permlane32_swap_b32_e32 v79, v81
	v_permlane32_swap_b32_e32 v82, v84
	v_permlane32_swap_b32_e32 v83, v85
	v_mfma_f32_32x32x16_bf16 v[20:35], v[70:73], v[86:89], v[20:35]
	ds_read_b64_tr_b16 v[86:87], v136 offset:0x200
	ds_read_b64_tr_b16 v[88:89], v136 offset:0xa00
	v_mfma_f32_32x32x16_bf16 v[20:35], v[74:77], v[90:93], v[20:35]
	ds_read_b64_tr_b16 v[90:91], v136 offset:0x1200
	ds_read_b64_tr_b16 v[92:93], v136 offset:0x1a00
	v_mfma_f32_32x32x16_bf16 v[20:35], v[78:81], v[94:97], v[20:35]
	ds_read_b64_tr_b16 v[94:95], v136 offset:0x2200
	ds_read_b64_tr_b16 v[96:97], v136 offset:0x2a00
	v_mfma_f32_32x32x16_bf16 v[20:35], v[82:85], v[178:181], v[20:35]
	ds_read_b64_tr_b16 v[178:179], v136 offset:0x3200
	ds_read_b64_tr_b16 v[180:181], v136 offset:0x3a00
	s_waitcnt lgkmcnt(0)
	v_mfma_f32_32x32x16_bf16 v[36:51], v[70:73], v[86:89], v[36:51]
	ds_read_b64_tr_b16 v[86:87], v136 offset:0x400
	ds_read_b64_tr_b16 v[88:89], v136 offset:0xc00
	v_mfma_f32_32x32x16_bf16 v[36:51], v[74:77], v[90:93], v[36:51]
	ds_read_b64_tr_b16 v[90:91], v136 offset:0x1400
	ds_read_b64_tr_b16 v[92:93], v136 offset:0x1c00
	v_mfma_f32_32x32x16_bf16 v[36:51], v[78:81], v[94:97], v[36:51]
	ds_read_b64_tr_b16 v[94:95], v136 offset:0x2400
	ds_read_b64_tr_b16 v[96:97], v136 offset:0x2c00
	v_mfma_f32_32x32x16_bf16 v[36:51], v[82:85], v[178:181], v[36:51]
	ds_read_b64_tr_b16 v[178:179], v136 offset:0x3400
	ds_read_b64_tr_b16 v[180:181], v136 offset:0x3c00
	s_waitcnt lgkmcnt(0)
	v_mfma_f32_32x32x16_bf16 v[52:67], v[70:73], v[86:89], v[52:67]
	ds_read_b64_tr_b16 v[86:87], v136 offset:0x600
	ds_read_b64_tr_b16 v[88:89], v136 offset:0xe00
	v_mfma_f32_32x32x16_bf16 v[52:67], v[74:77], v[90:93], v[52:67]
	ds_read_b64_tr_b16 v[90:91], v136 offset:0x1600
	ds_read_b64_tr_b16 v[92:93], v136 offset:0x1e00
	v_mfma_f32_32x32x16_bf16 v[52:67], v[78:81], v[94:97], v[52:67]
	ds_read_b64_tr_b16 v[94:95], v136 offset:0x2600
	ds_read_b64_tr_b16 v[96:97], v136 offset:0x2e00
	v_mfma_f32_32x32x16_bf16 v[52:67], v[82:85], v[178:181], v[52:67]
	ds_read_b64_tr_b16 v[178:179], v136 offset:0x3600
	ds_read_b64_tr_b16 v[180:181], v136 offset:0x3e00
	s_waitcnt lgkmcnt(0)
	v_mfma_f32_32x32x16_bf16 v[4:19], v[70:73], v[86:89], v[4:19]
	v_cndmask_b32_e64 v70, 0, 1, s[86:87]
	s_mov_b64 s[4:5], -1
	v_cmp_ne_u32_e64 s[80:81], 1, v70
	s_andn2_b64 vcc, exec, s[86:87]
	v_mfma_f32_32x32x16_bf16 v[4:19], v[74:77], v[90:93], v[4:19]
	v_mfma_f32_32x32x16_bf16 v[4:19], v[78:81], v[94:97], v[4:19]
	v_mfma_f32_32x32x16_bf16 v[4:19], v[82:85], v[178:181], v[4:19]
	s_cbranch_vccnz .LBB0_1977
	s_waitcnt vmcnt(2) lgkmcnt(0)
	s_mov_b64 s[4:5], 0

.LBB0_1991:
	v_cmp_gt_f32_e32 vcc, 1.0, v178
	s_cbranch_vccz .LBB0_1995
	s_and_saveexec_b64 s[4:5], s[78:79]
	ds_write_b32 v174, v178
	s_or_b64 exec, exec, s[4:5]
	v_readlane_b32 s4, v254, 32
	s_waitcnt lgkmcnt(0)
	s_nop 1
	v_add_u32_e32 v1, s4, v175
	v_readlane_b32 s4, v254, 33
	s_nop 1
	v_add_u32_e32 v140, s4, v175
	v_readlane_b32 s4, v254, 31
	ds_read_b128 v[180:183], v1
	ds_read_b128 v[184:187], v140
	v_add_u32_e32 v1, s4, v175
	v_readlane_b32 s4, v254, 30
	ds_read_b128 v[188:191], v1
	s_waitcnt lgkmcnt(2)
	v_mul_f32_e32 v28, v28, v180
	v_mul_f32_e32 v29, v29, v181
	v_add_u32_e32 v1, s4, v175
	ds_read_b128 v[192:195], v1
	s_waitcnt lgkmcnt(2)
	v_mul_f32_e32 v32, v32, v184
	v_mul_f32_e32 v33, v33, v185
	s_waitcnt lgkmcnt(1)
	v_mul_f32_e32 v24, v24, v188
	v_mul_f32_e32 v25, v25, v189
	v_mul_f32_e32 v34, v34, v186
	v_mul_f32_e32 v35, v35, v187
	v_mul_f32_e32 v30, v30, v182
	v_mul_f32_e32 v31, v31, v183
	v_mul_f32_e32 v26, v26, v190
	v_mul_f32_e32 v27, v27, v191
	s_waitcnt lgkmcnt(0)
	v_mul_f32_e32 v22, v22, v194
	v_mul_f32_e32 v23, v23, v195
	v_mul_f32_e32 v20, v20, v192
	v_mul_f32_e32 v21, v21, v193
	v_mul_f32_e32 v48, v48, v184
	v_mul_f32_e32 v49, v49, v185
	v_mul_f32_e32 v44, v44, v180
	v_mul_f32_e32 v45, v45, v181
	v_mul_f32_e32 v40, v40, v188
	v_mul_f32_e32 v41, v41, v189
	v_mul_f32_e32 v50, v50, v186
	v_mul_f32_e32 v51, v51, v187
	v_mul_f32_e32 v46, v46, v182
	v_mul_f32_e32 v47, v47, v183
	v_mul_f32_e32 v42, v42, v190
	v_mul_f32_e32 v43, v43, v191
	v_mul_f32_e32 v38, v38, v194
	v_mul_f32_e32 v39, v39, v195
	v_mul_f32_e32 v36, v36, v192
	v_mul_f32_e32 v37, v37, v193
	v_mul_f32_e32 v64, v64, v184
	v_mul_f32_e32 v65, v65, v185
	v_mul_f32_e32 v60, v60, v180
	v_mul_f32_e32 v61, v61, v181
	v_mul_f32_e32 v56, v56, v188
	v_mul_f32_e32 v57, v57, v189
	v_mul_f32_e32 v66, v66, v186
	v_mul_f32_e32 v67, v67, v187
	v_mul_f32_e32 v62, v62, v182
	v_mul_f32_e32 v63, v63, v183
	v_mul_f32_e32 v58, v58, v190
	v_mul_f32_e32 v59, v59, v191
	v_mul_f32_e32 v54, v54, v194
	v_mul_f32_e32 v55, v55, v195
	v_mul_f32_e32 v52, v52, v192
	v_mul_f32_e32 v53, v53, v193
	v_mul_f32_e32 v16, v16, v184
	v_mul_f32_e32 v17, v17, v185
	v_mul_f32_e32 v12, v12, v180
	v_mul_f32_e32 v13, v13, v181
	v_mul_f32_e32 v8, v8, v188
	v_mul_f32_e32 v9, v9, v189
	v_mul_f32_e32 v18, v18, v186
	v_mul_f32_e32 v19, v19, v187
	v_mul_f32_e32 v14, v14, v182
	v_mul_f32_e32 v15, v15, v183
	v_mul_f32_e32 v10, v10, v190
	v_mul_f32_e32 v11, v11, v191
	v_mul_f32_e32 v6, v6, v194
	v_mul_f32_e32 v7, v7, v195
	v_mul_f32_e32 v4, v4, v192
	v_mul_f32_e32 v5, v5, v193
.LBB0_1995:
	v_mov_b32_e32 v1, v0
	v_fma_f32 v84, v84, s2, v0
	v_fma_f32 v85, v85, s2, v1
	v_fma_f32 v68, v68, s2, v0
	v_fma_f32 v69, v69, s2, v1
	v_fma_f32 v86, v86, s2, v0
	v_fma_f32 v87, v87, s2, v1
	v_fma_f32 v88, v88, s2, v0
	v_fma_f32 v89, v89, s2, v1
	v_fma_f32 v90, v90, s2, v0
	v_fma_f32 v91, v91, s2, v1
	v_fma_f32 v92, v92, s2, v0
	v_fma_f32 v93, v93, s2, v1
	v_fma_f32 v94, v94, s2, v0
	v_fma_f32 v95, v95, s2, v1
	v_fma_f32 v96, v96, s2, v0
	v_fma_f32 v97, v97, s2, v1
	v_fma_f32 v98, v98, s2, v0
	v_fma_f32 v99, v99, s2, v1
	v_exp_f32_e32 v84, v84
	v_exp_f32_e32 v85, v85
	v_exp_f32_e32 v68, v68
	v_exp_f32_e32 v69, v69
	v_fma_f32 v70, v70, s2, v0
	v_fma_f32 v71, v71, s2, v1
	v_fma_f32 v72, v72, s2, v0
	v_fma_f32 v73, v73, s2, v1
	v_fma_f32 v74, v74, s2, v0
	v_fma_f32 v75, v75, s2, v1
	v_fma_f32 v76, v76, s2, v0
	v_fma_f32 v77, v77, s2, v1
	v_fma_f32 v78, v78, s2, v0
	v_fma_f32 v79, v79, s2, v1
	v_fma_f32 v80, v80, s2, v0
	v_fma_f32 v81, v81, s2, v1
	v_fma_f32 v0, v82, s2, v0
	v_fma_f32 v1, v83, s2, v1
	v_exp_f32_e32 v86, v86
	v_exp_f32_e32 v87, v87
	v_exp_f32_e32 v88, v88
	v_exp_f32_e32 v89, v89
	v_exp_f32_e32 v90, v90
	v_exp_f32_e32 v91, v91
	v_exp_f32_e32 v92, v92
	v_exp_f32_e32 v93, v93
	v_exp_f32_e32 v94, v94
	v_exp_f32_e32 v95, v95
	v_exp_f32_e32 v96, v96
	v_exp_f32_e32 v97, v97
	v_exp_f32_e32 v98, v98
	v_exp_f32_e32 v99, v99
	v_exp_f32_e32 v70, v70
	v_exp_f32_e32 v71, v71
	v_exp_f32_e32 v72, v72
	v_exp_f32_e32 v73, v73
	v_exp_f32_e32 v74, v74
	v_exp_f32_e32 v75, v75
	v_exp_f32_e32 v76, v76
	v_exp_f32_e32 v77, v77
	v_exp_f32_e32 v78, v78
	v_exp_f32_e32 v79, v79
	v_exp_f32_e32 v80, v80
	v_exp_f32_e32 v81, v81
	v_exp_f32_e32 v82, v0
	v_exp_f32_e32 v83, v1
	v_add_f32_e32 v192, v68, v84
	v_add_f32_e32 v193, v69, v85
	v_add_f32_e32 v180, v80, v96
	v_add_f32_e32 v181, v81, v97
	v_add_f32_e32 v182, v78, v94
	v_add_f32_e32 v183, v79, v95
	v_add_f32_e32 v0, v82, v98
	v_add_f32_e32 v1, v83, v99
	v_add_f32_e32 v184, v76, v92
	v_add_f32_e32 v185, v77, v93
	v_add_f32_e32 v186, v74, v90
	v_add_f32_e32 v187, v75, v91
	v_add_f32_e32 v188, v72, v88
	v_add_f32_e32 v189, v73, v89
	v_add_f32_e32 v190, v70, v86
	v_add_f32_e32 v191, v71, v87
	v_add_f32_e32 v192, 0, v192
	v_add_f32_e32 v193, 0, v193
	v_cvt_pk_bf16_f32 v68, v68, v69
	v_cvt_pk_bf16_f32 v69, v70, v71
	v_cvt_pk_bf16_f32 v70, v72, v73
	v_cvt_pk_bf16_f32 v71, v74, v75
	v_cvt_pk_bf16_f32 v72, v76, v77
	v_cvt_pk_bf16_f32 v73, v78, v79
	v_cvt_pk_bf16_f32 v74, v80, v81
	v_cvt_pk_bf16_f32 v75, v82, v83
	v_cvt_pk_bf16_f32 v76, v84, v85
	v_cvt_pk_bf16_f32 v77, v86, v87
	v_cvt_pk_bf16_f32 v78, v88, v89
	v_cvt_pk_bf16_f32 v79, v90, v91
	v_cvt_pk_bf16_f32 v80, v92, v93
	v_cvt_pk_bf16_f32 v81, v94, v95
	v_cvt_pk_bf16_f32 v82, v96, v97
	v_cvt_pk_bf16_f32 v83, v98, v99
	ds_read_b64_tr_b16 v[84:85], v176 offset:0
	s_nop 0
	v_add_f32_e32 v190, v190, v192
	v_add_f32_e32 v191, v191, v193
	ds_read_b64_tr_b16 v[86:87], v176 offset:0x800
	ds_read_b64_tr_b16 v[88:89], v176 offset:0x1000
	ds_read_b64_tr_b16 v[90:91], v176 offset:0x1800
	ds_read_b64_tr_b16 v[92:93], v176 offset:0x2000
	ds_read_b64_tr_b16 v[94:95], v176 offset:0x2800
	s_nop 0
	v_add_f32_e32 v188, v188, v190
	v_add_f32_e32 v189, v189, v191
	ds_read_b64_tr_b16 v[96:97], v176 offset:0x3000
	ds_read_b64_tr_b16 v[98:99], v176 offset:0x3800
	s_waitcnt lgkmcnt(0)
	v_permlane32_swap_b32_e32 v68, v70
	v_add_f32_e32 v186, v186, v188
	v_add_f32_e32 v187, v187, v189
	v_permlane32_swap_b32_e32 v69, v71
	v_add_f32_e32 v184, v184, v186
	v_add_f32_e32 v185, v185, v187
	v_permlane32_swap_b32_e32 v72, v74
	v_add_f32_e32 v182, v182, v184
	v_add_f32_e32 v183, v183, v185
	v_permlane32_swap_b32_e32 v73, v75
	v_add_f32_e32 v180, v180, v182
	v_add_f32_e32 v181, v181, v183
	v_permlane32_swap_b32_e32 v76, v78
	v_add_f32_e32 v0, v0, v180
	v_add_f32_e32 v1, v1, v181
	v_permlane32_swap_b32_e32 v77, v79
	v_pk_add_f32 v[0:1], v[0:1], v[0:1] op_sel:[0,1] op_sel_hi:[1,0]
	v_permlane32_swap_b32_e32 v80, v82
	v_mov_b32_e32 v1, v0
	s_nop 1
	v_permlane32_swap_b32_e32 v0, v1
	v_permlane32_swap_b32_e32 v81, v83
	v_mfma_f32_32x32x16_bf16 v[20:35], v[68:71], v[84:87], v[20:35]
	ds_read_b64_tr_b16 v[84:85], v176 offset:0x200
	ds_read_b64_tr_b16 v[86:87], v176 offset:0xa00
	v_mfma_f32_32x32x16_bf16 v[20:35], v[72:75], v[88:91], v[20:35]
	ds_read_b64_tr_b16 v[88:89], v176 offset:0x1200
	ds_read_b64_tr_b16 v[90:91], v176 offset:0x1a00
	v_mfma_f32_32x32x16_bf16 v[20:35], v[76:79], v[92:95], v[20:35]
	ds_read_b64_tr_b16 v[92:93], v176 offset:0x2200
	ds_read_b64_tr_b16 v[94:95], v176 offset:0x2a00
	v_mfma_f32_32x32x16_bf16 v[20:35], v[80:83], v[96:99], v[20:35]
	ds_read_b64_tr_b16 v[96:97], v176 offset:0x3200
	ds_read_b64_tr_b16 v[98:99], v176 offset:0x3a00
	s_waitcnt lgkmcnt(0)
	v_mfma_f32_32x32x16_bf16 v[36:51], v[68:71], v[84:87], v[36:51]
	ds_read_b64_tr_b16 v[84:85], v176 offset:0x400
	ds_read_b64_tr_b16 v[86:87], v176 offset:0xc00
	v_mfma_f32_32x32x16_bf16 v[36:51], v[72:75], v[88:91], v[36:51]
	ds_read_b64_tr_b16 v[88:89], v176 offset:0x1400
	ds_read_b64_tr_b16 v[90:91], v176 offset:0x1c00
	v_mfma_f32_32x32x16_bf16 v[36:51], v[76:79], v[92:95], v[36:51]
	ds_read_b64_tr_b16 v[92:93], v176 offset:0x2400
	ds_read_b64_tr_b16 v[94:95], v176 offset:0x2c00
	v_mfma_f32_32x32x16_bf16 v[36:51], v[80:83], v[96:99], v[36:51]
	ds_read_b64_tr_b16 v[96:97], v176 offset:0x3400
	ds_read_b64_tr_b16 v[98:99], v176 offset:0x3c00
	s_waitcnt lgkmcnt(0)
	v_mfma_f32_32x32x16_bf16 v[52:67], v[68:71], v[84:87], v[52:67]
	ds_read_b64_tr_b16 v[84:85], v176 offset:0x600
	ds_read_b64_tr_b16 v[86:87], v176 offset:0xe00
	v_mfma_f32_32x32x16_bf16 v[52:67], v[72:75], v[88:91], v[52:67]
	ds_read_b64_tr_b16 v[88:89], v176 offset:0x1600
	ds_read_b64_tr_b16 v[90:91], v176 offset:0x1e00
	v_mfma_f32_32x32x16_bf16 v[52:67], v[76:79], v[92:95], v[52:67]
	ds_read_b64_tr_b16 v[92:93], v176 offset:0x2600
	ds_read_b64_tr_b16 v[94:95], v176 offset:0x2e00
	v_mfma_f32_32x32x16_bf16 v[52:67], v[80:83], v[96:99], v[52:67]
	ds_read_b64_tr_b16 v[96:97], v176 offset:0x3600
	ds_read_b64_tr_b16 v[98:99], v176 offset:0x3e00
	s_waitcnt lgkmcnt(0)
	v_mfma_f32_32x32x16_bf16 v[4:19], v[68:71], v[84:87], v[4:19]
	s_mov_b64 s[4:5], -1
	s_andn2_b64 vcc, exec, s[8:9]
	v_mfma_f32_32x32x16_bf16 v[4:19], v[72:75], v[88:91], v[4:19]
	v_mfma_f32_32x32x16_bf16 v[4:19], v[76:79], v[92:95], v[4:19]
	v_mfma_f32_32x32x16_bf16 v[4:19], v[80:83], v[96:99], v[4:19]
	s_cbranch_vccnz .LBB0_1997
	s_waitcnt vmcnt(2) lgkmcnt(0)
	s_mov_b64 s[4:5], 0

.LBB0_2012:
	s_waitcnt vmcnt(0) lgkmcnt(0)
	s_barrier
	v_readlane_b32 s1, v254, 30
	v_cmp_eq_u32_e64 s[10:11], 0, v139
	v_lshlrev_b32_e32 v139, 4, v139
	v_lshl_add_u32 v138, v138, 2, s1
	v_cmp_gt_f32_e32 vcc, 1.0, v1
	s_cbranch_vccz .LBB0_2016
	s_and_saveexec_b64 s[4:5], s[10:11]
	ds_write_b32 v138, v1
	s_or_b64 exec, exec, s[4:5]
	v_readlane_b32 s1, v254, 30
	s_waitcnt lgkmcnt(0)
	s_nop 1
	v_add_u32_e32 v0, s1, v139
	v_readlane_b32 s1, v254, 32
	s_nop 1
	v_add_u32_e32 v4, s1, v139
	v_readlane_b32 s1, v254, 33
	s_nop 1
	v_add_u32_e32 v8, s1, v139
	v_readlane_b32 s1, v254, 31
	ds_read_b128 v[4:7], v4
	ds_read_b128 v[8:11], v8
	v_add_u32_e32 v12, s1, v139
	ds_read_b128 v[52:55], v12
	ds_read_b128 v[56:59], v0
	s_waitcnt lgkmcnt(3)
	v_mul_f32_e32 v14, 0, v6
	v_mul_f32_e32 v15, 0, v7
	s_waitcnt lgkmcnt(2)
	v_mul_f32_e32 v18, 0, v10
	v_mul_f32_e32 v19, 0, v11
	s_waitcnt lgkmcnt(1)
	v_mul_f32_e32 v10, 0, v54
	v_mul_f32_e32 v11, 0, v55
	s_waitcnt lgkmcnt(0)
	v_mul_f32_e32 v6, 0, v58
	v_mul_f32_e32 v7, 0, v59
	v_mul_f32_e32 v16, 0, v8
	v_mul_f32_e32 v17, 0, v9
	v_mul_f32_e32 v12, 0, v4
	v_mul_f32_e32 v13, 0, v5
	v_mul_f32_e32 v8, 0, v52
	v_mul_f32_e32 v9, 0, v53
	v_mul_f32_e32 v4, 0, v56
	v_mul_f32_e32 v5, 0, v57
	s_branch .LBB0_2017

.LBB0_2017:
	v_mul_f32_e32 v0, 0xbe0293ee, v141
	v_fma_f32 v36, v36, s2, v0
	v_fma_f32 v37, v37, s2, v0
	v_fma_f32 v20, v20, s2, v0
	v_fma_f32 v21, v21, s2, v0
	v_exp_f32_e32 v36, v36
	v_exp_f32_e32 v37, v37
	v_fma_f32 v38, v38, s2, v0
	v_fma_f32 v39, v39, s2, v0
	v_fma_f32 v22, v22, s2, v0
	v_fma_f32 v23, v23, s2, v0
	v_exp_f32_e32 v20, v20
	v_exp_f32_e32 v21, v21
	v_exp_f32_e32 v38, v38
	v_exp_f32_e32 v39, v39
	v_fma_f32 v40, v40, s2, v0
	v_fma_f32 v41, v41, s2, v0
	v_fma_f32 v24, v24, s2, v0
	v_fma_f32 v25, v25, s2, v0
	v_exp_f32_e32 v22, v22
	v_exp_f32_e32 v23, v23
	v_exp_f32_e32 v40, v40
	v_exp_f32_e32 v41, v41
	v_fma_f32 v42, v42, s2, v0
	v_fma_f32 v43, v43, s2, v0
	v_fma_f32 v26, v26, s2, v0
	v_fma_f32 v27, v27, s2, v0
	v_exp_f32_e32 v24, v24
	v_exp_f32_e32 v25, v25
	v_exp_f32_e32 v42, v42
	v_exp_f32_e32 v43, v43
	v_fma_f32 v44, v44, s2, v0
	v_fma_f32 v45, v45, s2, v0
	v_fma_f32 v28, v28, s2, v0
	v_fma_f32 v29, v29, s2, v0
	v_exp_f32_e32 v26, v26
	v_exp_f32_e32 v27, v27
	v_exp_f32_e32 v44, v44
	v_exp_f32_e32 v45, v45
	v_fma_f32 v46, v46, s2, v0
	v_fma_f32 v47, v47, s2, v0
	v_fma_f32 v30, v30, s2, v0
	v_fma_f32 v31, v31, s2, v0
	v_exp_f32_e32 v28, v28
	v_exp_f32_e32 v29, v29
	v_add_f32_e32 v66, v36, v20
	v_add_f32_e32 v67, v37, v21
	v_exp_f32_e32 v46, v46
	v_exp_f32_e32 v47, v47
	v_fma_f32 v48, v48, s2, v0
	v_fma_f32 v49, v49, s2, v0
	v_fma_f32 v32, v32, s2, v0
	v_fma_f32 v33, v33, s2, v0
	v_exp_f32_e32 v30, v30
	v_exp_f32_e32 v31, v31
	v_add_f32_e32 v64, v38, v22
	v_add_f32_e32 v65, v39, v23
	v_add_f32_e32 v66, 0, v66
	v_add_f32_e32 v67, 0, v67
	v_exp_f32_e32 v48, v48
	v_exp_f32_e32 v49, v49
	v_fma_f32 v50, v50, s2, v0
	v_fma_f32 v51, v51, s2, v0
	v_fma_f32 v34, v34, s2, v0
	v_fma_f32 v35, v35, s2, v0
	v_exp_f32_e32 v32, v32
	v_exp_f32_e32 v33, v33
	v_add_f32_e32 v62, v40, v24
	v_add_f32_e32 v63, v41, v25
	v_add_f32_e32 v64, v64, v66
	v_add_f32_e32 v65, v65, v67
	v_exp_f32_e32 v50, v50
	v_exp_f32_e32 v51, v51
	v_exp_f32_e32 v34, v34
	v_exp_f32_e32 v35, v35
	v_add_f32_e32 v60, v42, v26
	v_add_f32_e32 v61, v43, v27
	v_add_f32_e32 v62, v62, v64
	v_add_f32_e32 v63, v63, v65
	v_cvt_pk_bf16_f32 v68, v36, v37
	v_cvt_pk_bf16_f32 v69, v38, v39
	v_cvt_pk_bf16_f32 v70, v40, v41
	v_cvt_pk_bf16_f32 v71, v42, v43
	v_cvt_pk_bf16_f32 v72, v44, v45
	v_cvt_pk_bf16_f32 v73, v46, v47
	v_cvt_pk_bf16_f32 v74, v48, v49
	v_cvt_pk_bf16_f32 v75, v50, v51
	v_cvt_pk_bf16_f32 v76, v20, v21
	v_cvt_pk_bf16_f32 v77, v22, v23
	v_cvt_pk_bf16_f32 v78, v24, v25
	v_cvt_pk_bf16_f32 v79, v26, v27
	v_cvt_pk_bf16_f32 v80, v28, v29
	v_cvt_pk_bf16_f32 v81, v30, v31
	v_cvt_pk_bf16_f32 v82, v32, v33
	v_cvt_pk_bf16_f32 v83, v34, v35
	ds_read_b64_tr_b16 v[36:37], v136 offset:0
	v_add_f32_e32 v58, v44, v28
	v_add_f32_e32 v59, v45, v29
	v_add_f32_e32 v60, v60, v62
	v_add_f32_e32 v61, v61, v63
	ds_read_b64_tr_b16 v[38:39], v136 offset:0x800
	v_add_f32_e32 v56, v46, v30
	v_add_f32_e32 v57, v47, v31
	v_add_f32_e32 v58, v58, v60
	v_add_f32_e32 v59, v59, v61
	ds_read_b64_tr_b16 v[40:41], v136 offset:0x1000
	v_add_f32_e32 v54, v48, v32
	v_add_f32_e32 v55, v49, v33
	v_add_f32_e32 v56, v56, v58
	v_add_f32_e32 v57, v57, v59
	ds_read_b64_tr_b16 v[42:43], v136 offset:0x1800
	v_add_f32_e32 v52, v50, v34
	v_add_f32_e32 v53, v51, v35
	v_add_f32_e32 v54, v54, v56
	v_add_f32_e32 v55, v55, v57
	ds_read_b64_tr_b16 v[44:45], v136 offset:0x2000
	ds_read_b64_tr_b16 v[46:47], v136 offset:0x2800
	ds_read_b64_tr_b16 v[48:49], v136 offset:0x3000
	ds_read_b64_tr_b16 v[50:51], v136 offset:0x3800
	s_waitcnt lgkmcnt(0)
	s_nop 0
	v_add_f32_e32 v52, v52, v54
	v_add_f32_e32 v53, v53, v55
	v_add_u32_e32 v137, s78, v137
	v_pk_add_f32 v[52:53], v[52:53], v[52:53] op_sel:[0,1] op_sel_hi:[1,0]
	v_permlane32_swap_b32_e32 v68, v70
	v_mov_b32_e32 v53, v52
	s_nop 1
	v_permlane32_swap_b32_e32 v52, v53
	v_add_f32_e32 v140, v52, v53
	v_fmac_f32_e32 v140, 0, v1
	v_permlane32_swap_b32_e32 v69, v71
	v_permlane32_swap_b32_e32 v72, v74
	v_permlane32_swap_b32_e32 v73, v75
	v_permlane32_swap_b32_e32 v76, v78
	v_permlane32_swap_b32_e32 v77, v79
	v_permlane32_swap_b32_e32 v80, v82
	v_permlane32_swap_b32_e32 v81, v83
	v_mfma_f32_32x32x16_bf16 v[20:35], v[68:71], v[36:39], v[4:19]
	ds_read_b64_tr_b16 v[52:53], v136 offset:0x200
	ds_read_b64_tr_b16 v[54:55], v136 offset:0xa00
	ds_read_b64_tr_b16 v[56:57], v136 offset:0x1200
	ds_read_b64_tr_b16 v[58:59], v136 offset:0x1a00
	ds_read_b64_tr_b16 v[60:61], v136 offset:0x2200
	ds_read_b64_tr_b16 v[62:63], v136 offset:0x2a00
	ds_read_b64_tr_b16 v[64:65], v136 offset:0x3200
	v_mfma_f32_32x32x16_bf16 v[20:35], v[72:75], v[40:43], v[20:35]
	ds_read_b64_tr_b16 v[66:67], v136 offset:0x3a00
	s_waitcnt lgkmcnt(0)
	v_mfma_f32_32x32x16_bf16 v[20:35], v[76:79], v[44:47], v[20:35]
	v_mfma_f32_32x32x16_bf16 v[20:35], v[80:83], v[48:51], v[20:35]
	v_mfma_f32_32x32x16_bf16 v[36:51], v[68:71], v[52:55], v[4:19]
	ds_read_b64_tr_b16 v[84:85], v136 offset:0x400
	ds_read_b64_tr_b16 v[86:87], v136 offset:0xc00
	ds_read_b64_tr_b16 v[88:89], v136 offset:0x1400
	ds_read_b64_tr_b16 v[90:91], v136 offset:0x1c00
	ds_read_b64_tr_b16 v[92:93], v136 offset:0x2400
	ds_read_b64_tr_b16 v[94:95], v136 offset:0x2c00
	ds_read_b64_tr_b16 v[96:97], v136 offset:0x3400
	v_mfma_f32_32x32x16_bf16 v[36:51], v[72:75], v[56:59], v[36:51]
	ds_read_b64_tr_b16 v[98:99], v136 offset:0x3c00
	s_waitcnt lgkmcnt(0)
	v_mfma_f32_32x32x16_bf16 v[36:51], v[76:79], v[60:63], v[36:51]
	v_mfma_f32_32x32x16_bf16 v[36:51], v[80:83], v[64:67], v[36:51]
	v_mfma_f32_32x32x16_bf16 v[52:67], v[68:71], v[84:87], v[4:19]
	ds_read_b64_tr_b16 v[84:85], v136 offset:0x600
	ds_read_b64_tr_b16 v[86:87], v136 offset:0xe00
	v_mfma_f32_32x32x16_bf16 v[52:67], v[72:75], v[88:91], v[52:67]
	ds_read_b64_tr_b16 v[88:89], v136 offset:0x1600
	ds_read_b64_tr_b16 v[90:91], v136 offset:0x1e00
	v_mfma_f32_32x32x16_bf16 v[52:67], v[76:79], v[92:95], v[52:67]
	ds_read_b64_tr_b16 v[92:93], v136 offset:0x2600
	ds_read_b64_tr_b16 v[94:95], v136 offset:0x2e00
	v_mfma_f32_32x32x16_bf16 v[52:67], v[80:83], v[96:99], v[52:67]
	ds_read_b64_tr_b16 v[96:97], v136 offset:0x3600
	ds_read_b64_tr_b16 v[98:99], v136 offset:0x3e00
	s_waitcnt lgkmcnt(0)
	v_mfma_f32_32x32x16_bf16 v[4:19], v[68:71], v[84:87], v[4:19]
	s_waitcnt vmcnt(0) lgkmcnt(0)
	s_barrier
	v_readlane_b32 s4, v255, 14
	v_readlane_b32 s5, v255, 15
	s_andn2_b64 vcc, exec, s[4:5]
	v_mfma_f32_32x32x16_bf16 v[4:19], v[72:75], v[88:91], v[4:19]
	v_mfma_f32_32x32x16_bf16 v[4:19], v[76:79], v[92:95], v[4:19]
	v_mfma_f32_32x32x16_bf16 v[4:19], v[80:83], v[96:99], v[4:19]
	s_cbranch_vccnz .LBB0_2043
	s_cmp_gt_u32 s91, 1
	s_mov_b32 s4, s79
	s_cselect_b64 s[78:79], -1, 0
	s_cmp_lt_u32 s91, 2
	s_cbranch_scc1 .LBB0_2020
	v_readlane_b32 s1, v255, 13
	v_readlane_b32 s3, v254, 46
	s_add_i32 s1, s1, 0x20000
	s_mov_b32 m0, s3
	v_readlane_b32 s3, v254, 47
	s_nop 0
	buffer_load_dwordx4 v132, s[92:95], s1 offen lds
	s_mov_b32 m0, s3
	s_nop 0
	buffer_load_dwordx4 v134, s[92:95], s1 offen lds

.LBB0_2034:
	v_cmp_gt_f32_e32 vcc, 1.0, v142
	s_cbranch_vccz .LBB0_2038
	s_and_saveexec_b64 s[4:5], s[10:11]
	ds_write_b32 v138, v142
	s_or_b64 exec, exec, s[4:5]
	v_readlane_b32 s1, v254, 32
	s_waitcnt lgkmcnt(0)
	s_nop 1
	v_add_u32_e32 v1, s1, v139
	v_readlane_b32 s1, v254, 33
	s_nop 1
	v_add_u32_e32 v2, s1, v139
	v_readlane_b32 s1, v254, 31
	ds_read_b128 v[170:173], v1
	ds_read_b128 v[174:177], v2
	v_add_u32_e32 v1, s1, v139
	v_readlane_b32 s1, v254, 30
	ds_read_b128 v[178:181], v1
	s_waitcnt lgkmcnt(2)
	v_mul_f32_e32 v28, v28, v170
	v_mul_f32_e32 v29, v29, v171
	v_add_u32_e32 v1, s1, v139
	ds_read_b128 v[182:185], v1
	s_waitcnt lgkmcnt(2)
	v_mul_f32_e32 v32, v32, v174
	v_mul_f32_e32 v33, v33, v175
	s_waitcnt lgkmcnt(1)
	v_mul_f32_e32 v24, v24, v178
	v_mul_f32_e32 v25, v25, v179
	v_mul_f32_e32 v34, v34, v176
	v_mul_f32_e32 v35, v35, v177
	v_mul_f32_e32 v30, v30, v172
	v_mul_f32_e32 v31, v31, v173
	v_mul_f32_e32 v26, v26, v180
	v_mul_f32_e32 v27, v27, v181
	s_waitcnt lgkmcnt(0)
	v_mul_f32_e32 v22, v22, v184
	v_mul_f32_e32 v23, v23, v185
	v_mul_f32_e32 v20, v20, v182
	v_mul_f32_e32 v21, v21, v183
	v_mul_f32_e32 v48, v48, v174
	v_mul_f32_e32 v49, v49, v175
	v_mul_f32_e32 v44, v44, v170
	v_mul_f32_e32 v45, v45, v171
	v_mul_f32_e32 v40, v40, v178
	v_mul_f32_e32 v41, v41, v179
	v_mul_f32_e32 v50, v50, v176
	v_mul_f32_e32 v51, v51, v177
	v_mul_f32_e32 v46, v46, v172
	v_mul_f32_e32 v47, v47, v173
	v_mul_f32_e32 v42, v42, v180
	v_mul_f32_e32 v43, v43, v181
	v_mul_f32_e32 v38, v38, v184
	v_mul_f32_e32 v39, v39, v185
	v_mul_f32_e32 v36, v36, v182
	v_mul_f32_e32 v37, v37, v183
	v_mul_f32_e32 v64, v64, v174
	v_mul_f32_e32 v65, v65, v175
	v_mul_f32_e32 v60, v60, v170
	v_mul_f32_e32 v61, v61, v171
	v_mul_f32_e32 v56, v56, v178
	v_mul_f32_e32 v57, v57, v179
	v_mul_f32_e32 v66, v66, v176
	v_mul_f32_e32 v67, v67, v177
	v_mul_f32_e32 v62, v62, v172
	v_mul_f32_e32 v63, v63, v173
	v_mul_f32_e32 v58, v58, v180
	v_mul_f32_e32 v59, v59, v181
	v_mul_f32_e32 v54, v54, v184
	v_mul_f32_e32 v55, v55, v185
	v_mul_f32_e32 v52, v52, v182
	v_mul_f32_e32 v53, v53, v183
	v_mul_f32_e32 v16, v16, v174
	v_mul_f32_e32 v17, v17, v175
	v_mul_f32_e32 v12, v12, v170
	v_mul_f32_e32 v13, v13, v171
	v_mul_f32_e32 v8, v8, v178
	v_mul_f32_e32 v9, v9, v179
	v_mul_f32_e32 v18, v18, v176
	v_mul_f32_e32 v19, v19, v177
	v_mul_f32_e32 v14, v14, v172
	v_mul_f32_e32 v15, v15, v173
	v_mul_f32_e32 v10, v10, v180
	v_mul_f32_e32 v11, v11, v181
	v_mul_f32_e32 v6, v6, v184
	v_mul_f32_e32 v7, v7, v185
	v_mul_f32_e32 v4, v4, v182
	v_mul_f32_e32 v5, v5, v183
.LBB0_2038:
	v_mov_b32_e32 v1, v0
	v_fma_f32 v84, v84, s2, v0
	v_fma_f32 v85, v85, s2, v1
	v_fma_f32 v68, v68, s2, v0
	v_fma_f32 v69, v69, s2, v1
	v_fma_f32 v86, v86, s2, v0
	v_fma_f32 v87, v87, s2, v1
	v_fma_f32 v88, v88, s2, v0
	v_fma_f32 v89, v89, s2, v1
	v_fma_f32 v90, v90, s2, v0
	v_fma_f32 v91, v91, s2, v1
	v_fma_f32 v92, v92, s2, v0
	v_fma_f32 v93, v93, s2, v1
	v_fma_f32 v94, v94, s2, v0
	v_fma_f32 v95, v95, s2, v1
	v_fma_f32 v96, v96, s2, v0
	v_fma_f32 v97, v97, s2, v1
	v_fma_f32 v98, v98, s2, v0
	v_fma_f32 v99, v99, s2, v1
	v_exp_f32_e32 v84, v84
	v_exp_f32_e32 v85, v85
	v_exp_f32_e32 v68, v68
	v_exp_f32_e32 v69, v69
	v_fma_f32 v70, v70, s2, v0
	v_fma_f32 v71, v71, s2, v1
	v_fma_f32 v72, v72, s2, v0
	v_fma_f32 v73, v73, s2, v1
	v_fma_f32 v74, v74, s2, v0
	v_fma_f32 v75, v75, s2, v1
	v_fma_f32 v76, v76, s2, v0
	v_fma_f32 v77, v77, s2, v1
	v_fma_f32 v78, v78, s2, v0
	v_fma_f32 v79, v79, s2, v1
	v_fma_f32 v80, v80, s2, v0
	v_fma_f32 v81, v81, s2, v1
	v_fma_f32 v0, v82, s2, v0
	v_fma_f32 v1, v83, s2, v1
	v_exp_f32_e32 v86, v86
	v_exp_f32_e32 v87, v87
	v_exp_f32_e32 v88, v88
	v_exp_f32_e32 v89, v89
	v_exp_f32_e32 v90, v90
	v_exp_f32_e32 v91, v91
	v_exp_f32_e32 v92, v92
	v_exp_f32_e32 v93, v93
	v_exp_f32_e32 v94, v94
	v_exp_f32_e32 v95, v95
	v_exp_f32_e32 v96, v96
	v_exp_f32_e32 v97, v97
	v_exp_f32_e32 v98, v98
	v_exp_f32_e32 v99, v99
	v_exp_f32_e32 v70, v70
	v_exp_f32_e32 v71, v71
	v_exp_f32_e32 v72, v72
	v_exp_f32_e32 v73, v73
	v_exp_f32_e32 v74, v74
	v_exp_f32_e32 v75, v75
	v_exp_f32_e32 v76, v76
	v_exp_f32_e32 v77, v77
	v_exp_f32_e32 v78, v78
	v_exp_f32_e32 v79, v79
	v_exp_f32_e32 v80, v80
	v_exp_f32_e32 v81, v81
	v_exp_f32_e32 v82, v0
	v_exp_f32_e32 v83, v1
	v_add_f32_e32 v180, v68, v84
	v_add_f32_e32 v181, v69, v85
	v_add_f32_e32 v154, v80, v96
	v_add_f32_e32 v155, v81, v97
	v_add_f32_e32 v170, v78, v94
	v_add_f32_e32 v171, v79, v95
	v_add_f32_e32 v0, v82, v98
	v_add_f32_e32 v1, v83, v99
	v_add_f32_e32 v172, v76, v92
	v_add_f32_e32 v173, v77, v93
	v_add_f32_e32 v174, v74, v90
	v_add_f32_e32 v175, v75, v91
	v_add_f32_e32 v176, v72, v88
	v_add_f32_e32 v177, v73, v89
	v_add_f32_e32 v178, v70, v86
	v_add_f32_e32 v179, v71, v87
	v_add_f32_e32 v180, 0, v180
	v_add_f32_e32 v181, 0, v181
	v_cvt_pk_bf16_f32 v68, v68, v69
	v_cvt_pk_bf16_f32 v69, v70, v71
	v_cvt_pk_bf16_f32 v70, v72, v73
	v_cvt_pk_bf16_f32 v71, v74, v75
	v_cvt_pk_bf16_f32 v72, v76, v77
	v_cvt_pk_bf16_f32 v73, v78, v79
	v_cvt_pk_bf16_f32 v74, v80, v81
	v_cvt_pk_bf16_f32 v75, v82, v83
	v_cvt_pk_bf16_f32 v76, v84, v85
	v_cvt_pk_bf16_f32 v77, v86, v87
	v_cvt_pk_bf16_f32 v78, v88, v89
	v_cvt_pk_bf16_f32 v79, v90, v91
	v_cvt_pk_bf16_f32 v80, v92, v93
	v_cvt_pk_bf16_f32 v81, v94, v95
	v_cvt_pk_bf16_f32 v82, v96, v97
	v_cvt_pk_bf16_f32 v83, v98, v99
	ds_read_b64_tr_b16 v[84:85], v137 offset:0
	s_nop 0
	v_add_f32_e32 v178, v178, v180
	v_add_f32_e32 v179, v179, v181
	ds_read_b64_tr_b16 v[86:87], v137 offset:0x800
	ds_read_b64_tr_b16 v[88:89], v137 offset:0x1000
	ds_read_b64_tr_b16 v[90:91], v137 offset:0x1800
	ds_read_b64_tr_b16 v[92:93], v137 offset:0x2000
	ds_read_b64_tr_b16 v[94:95], v137 offset:0x2800
	s_nop 0
	v_add_f32_e32 v176, v176, v178
	v_add_f32_e32 v177, v177, v179
	ds_read_b64_tr_b16 v[96:97], v137 offset:0x3000
	ds_read_b64_tr_b16 v[98:99], v137 offset:0x3800
	s_waitcnt lgkmcnt(0)
	v_permlane32_swap_b32_e32 v68, v70
	v_add_f32_e32 v174, v174, v176
	v_add_f32_e32 v175, v175, v177
	v_permlane32_swap_b32_e32 v69, v71
	v_add_f32_e32 v172, v172, v174
	v_add_f32_e32 v173, v173, v175
	v_permlane32_swap_b32_e32 v72, v74
	v_add_f32_e32 v170, v170, v172
	v_add_f32_e32 v171, v171, v173
	v_permlane32_swap_b32_e32 v73, v75
	v_add_f32_e32 v154, v154, v170
	v_add_f32_e32 v155, v155, v171
	v_permlane32_swap_b32_e32 v76, v78
	v_add_f32_e32 v0, v0, v154
	v_add_f32_e32 v1, v1, v155
	v_permlane32_swap_b32_e32 v77, v79
	v_pk_add_f32 v[0:1], v[0:1], v[0:1] op_sel:[0,1] op_sel_hi:[1,0]
	v_permlane32_swap_b32_e32 v80, v82
	v_mov_b32_e32 v1, v0
	s_nop 1
	v_permlane32_swap_b32_e32 v0, v1
	v_permlane32_swap_b32_e32 v81, v83
	v_mfma_f32_32x32x16_bf16 v[20:35], v[68:71], v[84:87], v[20:35]
	ds_read_b64_tr_b16 v[84:85], v137 offset:0x200
	ds_read_b64_tr_b16 v[86:87], v137 offset:0xa00
	v_mfma_f32_32x32x16_bf16 v[20:35], v[72:75], v[88:91], v[20:35]
	ds_read_b64_tr_b16 v[88:89], v137 offset:0x1200
	ds_read_b64_tr_b16 v[90:91], v137 offset:0x1a00
	v_mfma_f32_32x32x16_bf16 v[20:35], v[76:79], v[92:95], v[20:35]
	ds_read_b64_tr_b16 v[92:93], v137 offset:0x2200
	ds_read_b64_tr_b16 v[94:95], v137 offset:0x2a00
	v_mfma_f32_32x32x16_bf16 v[20:35], v[80:83], v[96:99], v[20:35]
	ds_read_b64_tr_b16 v[96:97], v137 offset:0x3200
	ds_read_b64_tr_b16 v[98:99], v137 offset:0x3a00
	s_waitcnt lgkmcnt(0)
	v_mfma_f32_32x32x16_bf16 v[36:51], v[68:71], v[84:87], v[36:51]
	ds_read_b64_tr_b16 v[84:85], v137 offset:0x400
	ds_read_b64_tr_b16 v[86:87], v137 offset:0xc00
	v_mfma_f32_32x32x16_bf16 v[36:51], v[72:75], v[88:91], v[36:51]
	ds_read_b64_tr_b16 v[88:89], v137 offset:0x1400
	ds_read_b64_tr_b16 v[90:91], v137 offset:0x1c00
	v_mfma_f32_32x32x16_bf16 v[36:51], v[76:79], v[92:95], v[36:51]
	ds_read_b64_tr_b16 v[92:93], v137 offset:0x2400
	ds_read_b64_tr_b16 v[94:95], v137 offset:0x2c00
	v_mfma_f32_32x32x16_bf16 v[36:51], v[80:83], v[96:99], v[36:51]
	ds_read_b64_tr_b16 v[96:97], v137 offset:0x3400
	ds_read_b64_tr_b16 v[98:99], v137 offset:0x3c00
	s_waitcnt lgkmcnt(0)
	v_mfma_f32_32x32x16_bf16 v[52:67], v[68:71], v[84:87], v[52:67]
	ds_read_b64_tr_b16 v[84:85], v137 offset:0x600
	ds_read_b64_tr_b16 v[86:87], v137 offset:0xe00
	v_mfma_f32_32x32x16_bf16 v[52:67], v[72:75], v[88:91], v[52:67]
	ds_read_b64_tr_b16 v[88:89], v137 offset:0x1600
	ds_read_b64_tr_b16 v[90:91], v137 offset:0x1e00
	v_mfma_f32_32x32x16_bf16 v[52:67], v[76:79], v[92:95], v[52:67]
	ds_read_b64_tr_b16 v[92:93], v137 offset:0x2600
	ds_read_b64_tr_b16 v[94:95], v137 offset:0x2e00
	v_mfma_f32_32x32x16_bf16 v[52:67], v[80:83], v[96:99], v[52:67]
	ds_read_b64_tr_b16 v[96:97], v137 offset:0x3600
	ds_read_b64_tr_b16 v[98:99], v137 offset:0x3e00
	s_waitcnt lgkmcnt(0)
	v_mfma_f32_32x32x16_bf16 v[4:19], v[68:71], v[84:87], v[4:19]
	s_mov_b64 s[4:5], -1
	s_and_b64 vcc, exec, s[8:9]
	v_mfma_f32_32x32x16_bf16 v[4:19], v[72:75], v[88:91], v[4:19]
	v_mfma_f32_32x32x16_bf16 v[4:19], v[76:79], v[92:95], v[4:19]
	v_mfma_f32_32x32x16_bf16 v[4:19], v[80:83], v[96:99], v[4:19]
	s_cbranch_vccnz .LBB0_2040
	s_waitcnt vmcnt(2) lgkmcnt(0)
	s_mov_b64 s[4:5], 0

.LBB0_2055:
	v_cmp_gt_f32_e32 vcc, 1.0, v1
	s_cbranch_vccz .LBB0_2059
	s_and_saveexec_b64 s[4:5], s[10:11]
	ds_write_b32 v138, v1
	s_or_b64 exec, exec, s[4:5]
	v_readlane_b32 s4, v254, 32
	s_waitcnt lgkmcnt(0)
	s_nop 1
	v_add_u32_e32 v0, s4, v139
	v_readlane_b32 s4, v254, 33
	s_nop 1
	v_add_u32_e32 v2, s4, v139
	v_readlane_b32 s4, v254, 31
	ds_read_b128 v[170:173], v0
	ds_read_b128 v[174:177], v2
	v_add_u32_e32 v0, s4, v139
	v_readlane_b32 s4, v254, 30
	ds_read_b128 v[178:181], v0
	s_waitcnt lgkmcnt(2)
	v_mul_f32_e32 v28, v28, v170
	v_mul_f32_e32 v29, v29, v171
	v_add_u32_e32 v0, s4, v139
	ds_read_b128 v[182:185], v0
	s_waitcnt lgkmcnt(2)
	v_mul_f32_e32 v32, v32, v174
	v_mul_f32_e32 v33, v33, v175
	s_waitcnt lgkmcnt(1)
	v_mul_f32_e32 v24, v24, v178
	v_mul_f32_e32 v25, v25, v179
	v_mul_f32_e32 v34, v34, v176
	v_mul_f32_e32 v35, v35, v177
	v_mul_f32_e32 v30, v30, v172
	v_mul_f32_e32 v31, v31, v173
	v_mul_f32_e32 v26, v26, v180
	v_mul_f32_e32 v27, v27, v181
	s_waitcnt lgkmcnt(0)
	v_mul_f32_e32 v22, v22, v184
	v_mul_f32_e32 v23, v23, v185
	v_mul_f32_e32 v20, v20, v182
	v_mul_f32_e32 v21, v21, v183
	v_mul_f32_e32 v48, v48, v174
	v_mul_f32_e32 v49, v49, v175
	v_mul_f32_e32 v44, v44, v170
	v_mul_f32_e32 v45, v45, v171
	v_mul_f32_e32 v40, v40, v178
	v_mul_f32_e32 v41, v41, v179
	v_mul_f32_e32 v50, v50, v176
	v_mul_f32_e32 v51, v51, v177
	v_mul_f32_e32 v46, v46, v172
	v_mul_f32_e32 v47, v47, v173
	v_mul_f32_e32 v42, v42, v180
	v_mul_f32_e32 v43, v43, v181
	v_mul_f32_e32 v38, v38, v184
	v_mul_f32_e32 v39, v39, v185
	v_mul_f32_e32 v36, v36, v182
	v_mul_f32_e32 v37, v37, v183
	v_mul_f32_e32 v64, v64, v174
	v_mul_f32_e32 v65, v65, v175
	v_mul_f32_e32 v60, v60, v170
	v_mul_f32_e32 v61, v61, v171
	v_mul_f32_e32 v56, v56, v178
	v_mul_f32_e32 v57, v57, v179
	v_mul_f32_e32 v66, v66, v176
	v_mul_f32_e32 v67, v67, v177
	v_mul_f32_e32 v62, v62, v172
	v_mul_f32_e32 v63, v63, v173
	v_mul_f32_e32 v58, v58, v180
	v_mul_f32_e32 v59, v59, v181
	v_mul_f32_e32 v54, v54, v184
	v_mul_f32_e32 v55, v55, v185
	v_mul_f32_e32 v52, v52, v182
	v_mul_f32_e32 v53, v53, v183
	v_mul_f32_e32 v16, v16, v174
	v_mul_f32_e32 v17, v17, v175
	v_mul_f32_e32 v12, v12, v170
	v_mul_f32_e32 v13, v13, v171
	v_mul_f32_e32 v8, v8, v178
	v_mul_f32_e32 v9, v9, v179
	v_mul_f32_e32 v18, v18, v176
	v_mul_f32_e32 v19, v19, v177
	v_mul_f32_e32 v14, v14, v172
	v_mul_f32_e32 v15, v15, v173
	v_mul_f32_e32 v10, v10, v180
	v_mul_f32_e32 v11, v11, v181
	v_mul_f32_e32 v6, v6, v184
	v_mul_f32_e32 v7, v7, v185
	v_mul_f32_e32 v4, v4, v182
	v_mul_f32_e32 v5, v5, v183
.LBB0_2059:
	v_mul_f32_e32 v0, 0xbe0293ee, v141
	v_fma_f32 v84, v84, s2, v0
	v_fma_f32 v85, v85, s2, v0
	v_fma_f32 v68, v68, s2, v0
	v_fma_f32 v69, v69, s2, v0
	v_fma_f32 v86, v86, s2, v0
	v_fma_f32 v87, v87, s2, v0
	v_exp_f32_e32 v84, v84
	v_exp_f32_e32 v85, v85
	v_exp_f32_e32 v154, v68
	v_exp_f32_e32 v155, v69
	v_fma_f32 v68, v70, s2, v0
	v_fma_f32 v69, v71, s2, v0
	v_fma_f32 v88, v88, s2, v0
	v_fma_f32 v89, v89, s2, v0
	v_exp_f32_e32 v86, v86
	v_exp_f32_e32 v87, v87
	v_exp_f32_e32 v170, v68
	v_exp_f32_e32 v171, v69
	v_fma_f32 v68, v72, s2, v0
	v_fma_f32 v69, v73, s2, v0
	v_fma_f32 v90, v90, s2, v0
	v_fma_f32 v91, v91, s2, v0
	v_exp_f32_e32 v88, v88
	v_exp_f32_e32 v89, v89
	v_exp_f32_e32 v72, v68
	v_exp_f32_e32 v73, v69
	v_fma_f32 v68, v74, s2, v0
	v_fma_f32 v69, v75, s2, v0
	v_fma_f32 v92, v92, s2, v0
	v_fma_f32 v93, v93, s2, v0
	v_exp_f32_e32 v90, v90
	v_exp_f32_e32 v91, v91
	v_exp_f32_e32 v74, v68
	v_exp_f32_e32 v75, v69
	v_fma_f32 v68, v76, s2, v0
	v_fma_f32 v69, v77, s2, v0
	v_fma_f32 v94, v94, s2, v0
	v_fma_f32 v95, v95, s2, v0
	v_exp_f32_e32 v92, v92
	v_exp_f32_e32 v93, v93
	v_exp_f32_e32 v76, v68
	v_exp_f32_e32 v77, v69
	v_fma_f32 v68, v78, s2, v0
	v_fma_f32 v69, v79, s2, v0
	v_add_f32_e32 v182, v154, v84
	v_add_f32_e32 v183, v155, v85
	v_fma_f32 v96, v96, s2, v0
	v_fma_f32 v97, v97, s2, v0
	v_exp_f32_e32 v94, v94
	v_exp_f32_e32 v95, v95
	v_exp_f32_e32 v78, v68
	v_exp_f32_e32 v79, v69
	v_fma_f32 v68, v80, s2, v0
	v_fma_f32 v69, v81, s2, v0
	v_add_f32_e32 v180, v170, v86
	v_add_f32_e32 v181, v171, v87
	v_add_f32_e32 v182, 0, v182
	v_add_f32_e32 v183, 0, v183
	v_fma_f32 v98, v98, s2, v0
	v_fma_f32 v99, v99, s2, v0
	v_exp_f32_e32 v96, v96
	v_exp_f32_e32 v97, v97
	v_exp_f32_e32 v80, v68
	v_exp_f32_e32 v81, v69
	v_fma_f32 v68, v82, s2, v0
	v_fma_f32 v69, v83, s2, v0
	v_add_f32_e32 v178, v72, v88
	v_add_f32_e32 v179, v73, v89
	v_add_f32_e32 v180, v180, v182
	v_add_f32_e32 v181, v181, v183
	v_exp_f32_e32 v98, v98
	v_exp_f32_e32 v99, v99
	v_exp_f32_e32 v82, v68
	v_exp_f32_e32 v83, v69
	v_add_f32_e32 v176, v74, v90
	v_add_f32_e32 v177, v75, v91
	v_add_f32_e32 v178, v178, v180
	v_add_f32_e32 v179, v179, v181
	v_add_f32_e32 v174, v76, v92
	v_add_f32_e32 v175, v77, v93
	v_add_f32_e32 v176, v176, v178
	v_add_f32_e32 v177, v177, v179
	v_add_f32_e32 v172, v78, v94
	v_add_f32_e32 v173, v79, v95
	v_add_f32_e32 v174, v174, v176
	v_add_f32_e32 v175, v175, v177
	v_add_f32_e32 v70, v80, v96
	v_add_f32_e32 v71, v81, v97
	v_add_f32_e32 v172, v172, v174
	v_add_f32_e32 v173, v173, v175
	v_add_f32_e32 v68, v82, v98
	v_add_f32_e32 v69, v83, v99
	v_add_f32_e32 v70, v70, v172
	v_add_f32_e32 v71, v71, v173
	s_nop 0
	v_add_f32_e32 v68, v68, v70
	v_add_f32_e32 v69, v69, v71
	v_cvt_pk_bf16_f32 v70, v154, v155
	v_cvt_pk_bf16_f32 v71, v170, v171
	v_cvt_pk_bf16_f32 v72, v72, v73
	v_cvt_pk_bf16_f32 v73, v74, v75
	v_cvt_pk_bf16_f32 v74, v76, v77
	v_cvt_pk_bf16_f32 v75, v78, v79
	v_cvt_pk_bf16_f32 v76, v80, v81
	v_cvt_pk_bf16_f32 v77, v82, v83
	v_cvt_pk_bf16_f32 v78, v84, v85
	v_cvt_pk_bf16_f32 v79, v86, v87
	v_cvt_pk_bf16_f32 v80, v88, v89
	v_cvt_pk_bf16_f32 v81, v90, v91
	v_cvt_pk_bf16_f32 v82, v92, v93
	v_cvt_pk_bf16_f32 v83, v94, v95
	v_cvt_pk_bf16_f32 v84, v96, v97
	v_cvt_pk_bf16_f32 v85, v98, v99
	ds_read_b64_tr_b16 v[86:87], v136 offset:0
	ds_read_b64_tr_b16 v[88:89], v136 offset:0x800
	ds_read_b64_tr_b16 v[90:91], v136 offset:0x1000
	ds_read_b64_tr_b16 v[92:93], v136 offset:0x1800
	ds_read_b64_tr_b16 v[94:95], v136 offset:0x2000
	ds_read_b64_tr_b16 v[96:97], v136 offset:0x2800
	ds_read_b64_tr_b16 v[170:171], v136 offset:0x3000
	ds_read_b64_tr_b16 v[172:173], v136 offset:0x3800
	s_nop 0
	v_pk_add_f32 v[68:69], v[68:69], v[68:69] op_sel:[0,1] op_sel_hi:[1,0]
	s_waitcnt lgkmcnt(0)
	v_permlane32_swap_b32_e32 v70, v72
	v_mov_b32_e32 v2, v68
	s_nop 1
	v_permlane32_swap_b32_e32 v68, v2
	v_permlane32_swap_b32_e32 v71, v73
	v_permlane32_swap_b32_e32 v74, v76
	v_permlane32_swap_b32_e32 v75, v77
	v_permlane32_swap_b32_e32 v78, v80
	v_permlane32_swap_b32_e32 v79, v81
	v_permlane32_swap_b32_e32 v82, v84
	v_permlane32_swap_b32_e32 v83, v85
	v_mfma_f32_32x32x16_bf16 v[20:35], v[70:73], v[86:89], v[20:35]
	ds_read_b64_tr_b16 v[86:87], v136 offset:0x200
	ds_read_b64_tr_b16 v[88:89], v136 offset:0xa00
	v_mfma_f32_32x32x16_bf16 v[20:35], v[74:77], v[90:93], v[20:35]
	ds_read_b64_tr_b16 v[90:91], v136 offset:0x1200
	ds_read_b64_tr_b16 v[92:93], v136 offset:0x1a00
	v_mfma_f32_32x32x16_bf16 v[20:35], v[78:81], v[94:97], v[20:35]
	ds_read_b64_tr_b16 v[94:95], v136 offset:0x2200
	ds_read_b64_tr_b16 v[96:97], v136 offset:0x2a00
	v_mfma_f32_32x32x16_bf16 v[20:35], v[82:85], v[170:173], v[20:35]
	ds_read_b64_tr_b16 v[170:171], v136 offset:0x3200
	ds_read_b64_tr_b16 v[172:173], v136 offset:0x3a00
	s_waitcnt lgkmcnt(0)
	v_mfma_f32_32x32x16_bf16 v[36:51], v[70:73], v[86:89], v[36:51]
	ds_read_b64_tr_b16 v[86:87], v136 offset:0x400
	ds_read_b64_tr_b16 v[88:89], v136 offset:0xc00
	v_mfma_f32_32x32x16_bf16 v[36:51], v[74:77], v[90:93], v[36:51]
	ds_read_b64_tr_b16 v[90:91], v136 offset:0x1400
	ds_read_b64_tr_b16 v[92:93], v136 offset:0x1c00
	v_mfma_f32_32x32x16_bf16 v[36:51], v[78:81], v[94:97], v[36:51]
	ds_read_b64_tr_b16 v[94:95], v136 offset:0x2400
	ds_read_b64_tr_b16 v[96:97], v136 offset:0x2c00
	v_mfma_f32_32x32x16_bf16 v[36:51], v[82:85], v[170:173], v[36:51]
	ds_read_b64_tr_b16 v[170:171], v136 offset:0x3400
	ds_read_b64_tr_b16 v[172:173], v136 offset:0x3c00
	s_waitcnt lgkmcnt(0)
	v_mfma_f32_32x32x16_bf16 v[52:67], v[70:73], v[86:89], v[52:67]
	ds_read_b64_tr_b16 v[86:87], v136 offset:0x600
	ds_read_b64_tr_b16 v[88:89], v136 offset:0xe00
	v_mfma_f32_32x32x16_bf16 v[52:67], v[74:77], v[90:93], v[52:67]
	ds_read_b64_tr_b16 v[90:91], v136 offset:0x1600
	ds_read_b64_tr_b16 v[92:93], v136 offset:0x1e00
	v_mfma_f32_32x32x16_bf16 v[52:67], v[78:81], v[94:97], v[52:67]
	ds_read_b64_tr_b16 v[94:95], v136 offset:0x2600
	ds_read_b64_tr_b16 v[96:97], v136 offset:0x2e00
	v_mfma_f32_32x32x16_bf16 v[52:67], v[82:85], v[170:173], v[52:67]
	ds_read_b64_tr_b16 v[170:171], v136 offset:0x3600
	ds_read_b64_tr_b16 v[172:173], v136 offset:0x3e00
	s_waitcnt lgkmcnt(0)
	v_mfma_f32_32x32x16_bf16 v[4:19], v[70:73], v[86:89], v[4:19]
	s_mov_b64 s[80:81], -1
	s_and_b64 vcc, exec, s[78:79]
	v_mfma_f32_32x32x16_bf16 v[4:19], v[74:77], v[90:93], v[4:19]
	v_mfma_f32_32x32x16_bf16 v[4:19], v[78:81], v[94:97], v[4:19]
	v_mfma_f32_32x32x16_bf16 v[4:19], v[82:85], v[170:173], v[4:19]
	s_cbranch_vccz .LBB0_2061
	s_waitcnt vmcnt(0) lgkmcnt(0)
	s_mov_b64 s[80:81], 0

.LBB0_2076:
	v_cmp_gt_f32_e32 vcc, 1.0, v142
	s_cbranch_vccz .LBB0_2080
	s_and_saveexec_b64 s[4:5], s[10:11]
	ds_write_b32 v138, v142
	s_or_b64 exec, exec, s[4:5]
	v_readlane_b32 s4, v254, 32
	s_waitcnt lgkmcnt(0)
	s_nop 1
	v_add_u32_e32 v1, s4, v139
	v_readlane_b32 s4, v254, 33
	s_nop 1
	v_add_u32_e32 v140, s4, v139
	v_readlane_b32 s4, v254, 31
	ds_read_b128 v[170:173], v1
	ds_read_b128 v[174:177], v140
	v_add_u32_e32 v1, s4, v139
	v_readlane_b32 s4, v254, 30
	ds_read_b128 v[178:181], v1
	s_waitcnt lgkmcnt(2)
	v_mul_f32_e32 v28, v28, v170
	v_mul_f32_e32 v29, v29, v171
	v_add_u32_e32 v1, s4, v139
	ds_read_b128 v[182:185], v1
	s_waitcnt lgkmcnt(2)
	v_mul_f32_e32 v32, v32, v174
	v_mul_f32_e32 v33, v33, v175
	s_waitcnt lgkmcnt(1)
	v_mul_f32_e32 v24, v24, v178
	v_mul_f32_e32 v25, v25, v179
	v_mul_f32_e32 v34, v34, v176
	v_mul_f32_e32 v35, v35, v177
	v_mul_f32_e32 v30, v30, v172
	v_mul_f32_e32 v31, v31, v173
	v_mul_f32_e32 v26, v26, v180
	v_mul_f32_e32 v27, v27, v181
	s_waitcnt lgkmcnt(0)
	v_mul_f32_e32 v22, v22, v184
	v_mul_f32_e32 v23, v23, v185
	v_mul_f32_e32 v20, v20, v182
	v_mul_f32_e32 v21, v21, v183
	v_mul_f32_e32 v48, v48, v174
	v_mul_f32_e32 v49, v49, v175
	v_mul_f32_e32 v44, v44, v170
	v_mul_f32_e32 v45, v45, v171
	v_mul_f32_e32 v40, v40, v178
	v_mul_f32_e32 v41, v41, v179
	v_mul_f32_e32 v50, v50, v176
	v_mul_f32_e32 v51, v51, v177
	v_mul_f32_e32 v46, v46, v172
	v_mul_f32_e32 v47, v47, v173
	v_mul_f32_e32 v42, v42, v180
	v_mul_f32_e32 v43, v43, v181
	v_mul_f32_e32 v38, v38, v184
	v_mul_f32_e32 v39, v39, v185
	v_mul_f32_e32 v36, v36, v182
	v_mul_f32_e32 v37, v37, v183
	v_mul_f32_e32 v64, v64, v174
	v_mul_f32_e32 v65, v65, v175
	v_mul_f32_e32 v60, v60, v170
	v_mul_f32_e32 v61, v61, v171
	v_mul_f32_e32 v56, v56, v178
	v_mul_f32_e32 v57, v57, v179
	v_mul_f32_e32 v66, v66, v176
	v_mul_f32_e32 v67, v67, v177
	v_mul_f32_e32 v62, v62, v172
	v_mul_f32_e32 v63, v63, v173
	v_mul_f32_e32 v58, v58, v180
	v_mul_f32_e32 v59, v59, v181
	v_mul_f32_e32 v54, v54, v184
	v_mul_f32_e32 v55, v55, v185
	v_mul_f32_e32 v52, v52, v182
	v_mul_f32_e32 v53, v53, v183
	v_mul_f32_e32 v16, v16, v174
	v_mul_f32_e32 v17, v17, v175
	v_mul_f32_e32 v12, v12, v170
	v_mul_f32_e32 v13, v13, v171
	v_mul_f32_e32 v8, v8, v178
	v_mul_f32_e32 v9, v9, v179
	v_mul_f32_e32 v18, v18, v176
	v_mul_f32_e32 v19, v19, v177
	v_mul_f32_e32 v14, v14, v172
	v_mul_f32_e32 v15, v15, v173
	v_mul_f32_e32 v10, v10, v180
	v_mul_f32_e32 v11, v11, v181
	v_mul_f32_e32 v6, v6, v184
	v_mul_f32_e32 v7, v7, v185
	v_mul_f32_e32 v4, v4, v182
	v_mul_f32_e32 v5, v5, v183
